# speedup vs baseline: 1.0237x; 1.0222x over previous
.LBB0_2:
	s_or_b64 exec, exec, s[80:81]
	v_lshl_add_u32 v1, v206, 2, s22
	s_add_i32 s19, s19, 0x22200
	ds_write_b32 v1, v72
	v_lshl_or_b32 v1, v124, 3, s19
	v_lshl_add_u32 v187, v67, 2, s22
	s_movk_i32 s22, 0x110
	v_mad_u32_u24 v186, v67, s22, v1
	s_add_i32 s22, s7, 0x180
	v_and_b32_e32 v102, 15, v0
	s_lshl_b32 s27, s34, 8
	s_and_b32 s25, s22, 0x380
	s_add_i32 s22, s7, 0x280
	v_lshlrev_b32_e32 v66, 2, v124
	v_mul_u32_u24_e32 v1, 0x110, v102
	v_and_b32_e32 v209, 48, v0
	s_and_b32 s23, s22, 0x380
	s_add_i32 s22, s7, 0x300
	v_mov_b32_e32 v67, 0x200
	s_addk_i32 s27, 0x380
	v_or_b32_e32 v133, s7, v66
	v_add3_u32 v1, s19, v1, v209
	s_lshl_b32 s19, s35, 15
	v_lshlrev_b32_e32 v210, 4, v206
	v_or_b32_e32 v189, s24, v66
	s_xor_b32 s24, s7, 0x200
	s_and_b32 s22, s22, 0x300
	v_bitop3_b32 v197, s7, v66, v67 bitop3:0xde
	s_and_b32 s7, s27, 0x380
	v_lshrrev_b32_e32 v185, 4, v206
	s_ashr_i32 s11, s10, 31
	v_or_b32_e32 v184, s19, v210
	v_or_b32_e32 v188, s26, v66
	v_or_b32_e32 v198, s25, v66
	v_or_b32_e32 v196, s23, v66
	v_or_b32_e32 v195, s22, v66
	v_or_b32_e32 v194, s7, v66
	v_mov_b32_e32 v102, v133
	v_and_b32_e32 v248, 2, v206
	v_cmp_ne_u32_e32 vcc, 0, v248
	v_mov_b32_e32 v249, 0x44444444
	v_mov_b32_e32 v250, 0xeeeeeeee
	s_nop 1
	v_cndmask_b32_e32 v223, v249, v250, vcc
	v_lshrrev_b32_e32 v248, 4, v206
	v_lshl_add_u32 v248, v248, 4, 1
	v_add_u32_e32 v249, 0, v248
	v_cvt_f32_u32_e32 v249, v249
	v_add_u32_e32 v250, 1, v248
	v_cvt_f32_u32_e32 v250, v250
	v_cvt_pk_bf16_f32 v232, v249, v250
	v_add_u32_e32 v249, 2, v248
	v_cvt_f32_u32_e32 v249, v249
	v_add_u32_e32 v250, 3, v248
	v_cvt_f32_u32_e32 v250, v250
	v_cvt_pk_bf16_f32 v233, v249, v250
	v_add_u32_e32 v249, 4, v248
	v_cvt_f32_u32_e32 v249, v249
	v_add_u32_e32 v250, 5, v248
	v_cvt_f32_u32_e32 v250, v250
	v_cvt_pk_bf16_f32 v234, v249, v250
	v_add_u32_e32 v249, 6, v248
	v_cvt_f32_u32_e32 v249, v249
	v_add_u32_e32 v250, 7, v248
	v_cvt_f32_u32_e32 v250, v250
	v_cvt_pk_bf16_f32 v235, v249, v250
	v_add_u32_e32 v249, 8, v248
	v_cvt_f32_u32_e32 v249, v249
	v_add_u32_e32 v250, 9, v248
	v_cvt_f32_u32_e32 v250, v250
	v_cvt_pk_bf16_f32 v236, v249, v250
	v_add_u32_e32 v249, 10, v248
	v_cvt_f32_u32_e32 v249, v249
	v_add_u32_e32 v250, 11, v248
	v_cvt_f32_u32_e32 v250, v250
	v_cvt_pk_bf16_f32 v237, v249, v250
	v_add_u32_e32 v249, 12, v248
	v_cvt_f32_u32_e32 v249, v249
	v_add_u32_e32 v250, 13, v248
	v_cvt_f32_u32_e32 v250, v250
	v_cvt_pk_bf16_f32 v238, v249, v250
	v_add_u32_e32 v249, 14, v248
	v_cvt_f32_u32_e32 v249, v249
	v_add_u32_e32 v250, 15, v248
	v_cvt_f32_u32_e32 v250, v250
	v_cvt_pk_bf16_f32 v239, v249, v250
	v_and_b32_e32 v248, 15, v206
	v_lshrrev_b32_e32 v249, 2, v248
	v_and_b32_e32 v250, 1, v248
	v_lshl_add_u32 v249, v249, 1, v250
	v_and_b32_e32 v250, 3, v249
	v_lshrrev_b32_e32 v251, 4, v206
	v_cmp_eq_u32_e32 vcc, v250, v251
	v_lshrrev_b32_e32 v249, 2, v249
	v_cmp_ne_u32_e64 s[78:79], 0, v249
	v_mov_b32_e32 v250, 0x3f80
	v_mov_b32_e32 v251, 0x3f800000
	s_nop 1
	v_cndmask_b32_e64 v250, v250, v251, s[78:79]
	v_cndmask_b32_e32 v252, 0, v250, vcc
	s_lshr_b32 s77, s19, 15
	s_mulk_i32 s77, 0x1100
	s_add_i32 s77, s77, 0x22200
	v_lshrrev_b32_e32 v248, 4, v206
	v_and_b32_e32 v249, 1, v248
	v_lshrrev_b32_e32 v250, 1, v248
	v_lshlrev_b32_e32 v249, 6, v249
	v_lshl_add_u32 v253, v250, 1, v249
	v_and_b32_e32 v248, 15, v206
	v_cmp_eq_u32_e64 s[78:79], 0, v248
	v_mov_b32_e32 v244, v252
	v_mov_b32_e32 v245, 0
	v_mov_b32_e32 v246, 0
	v_mov_b32_e32 v247, 0
	v_mov_b64_e32 v[240:241], 0
	v_mov_b64_e32 v[242:243], 0
	s_nop 1
	v_smfmac_f32_16x16x64_bf16 v[240:243], v[244:247], v[232:239], v223
	s_nop 15
	s_nop 3
	s_and_saveexec_b64 s[80:81], s[78:79]
	v_cvt_u32_f32_e32 v248, v240
	v_add_u32_e32 v248, -1, v248
	v_lshl_add_u32 v248, v248, 2, s77
	v_add_u32_e32 v249, 0, v253
	ds_write_b32 v248, v249
	v_cvt_u32_f32_e32 v248, v241
	v_add_u32_e32 v248, -1, v248
	v_lshl_add_u32 v248, v248, 2, s77
	v_add_u32_e32 v249, 32, v253
	ds_write_b32 v248, v249
	v_cvt_u32_f32_e32 v248, v242
	v_add_u32_e32 v248, -1, v248
	v_lshl_add_u32 v248, v248, 2, s77
	v_add_u32_e32 v249, 16, v253
	ds_write_b32 v248, v249
	v_cvt_u32_f32_e32 v248, v243
	v_add_u32_e32 v248, -1, v248
	v_lshl_add_u32 v248, v248, 2, s77
	v_add_u32_e32 v249, 48, v253
	ds_write_b32 v248, v249
	s_or_b64 exec, exec, s[80:81]
	v_mov_b32_e32 v244, 0
	v_mov_b32_e32 v245, v252
	v_mov_b32_e32 v246, 0
	v_mov_b32_e32 v247, 0
	v_mov_b64_e32 v[240:241], 0
	v_mov_b64_e32 v[242:243], 0
	s_nop 1
	v_smfmac_f32_16x16x64_bf16 v[240:243], v[244:247], v[232:239], v223
	s_nop 15
	s_nop 3
	s_and_saveexec_b64 s[80:81], s[78:79]
	v_cvt_u32_f32_e32 v248, v240
	v_add_u32_e32 v248, -1, v248
	v_lshl_add_u32 v248, v248, 2, s77
	v_add_u32_e32 v249, 4, v253
	ds_write_b32 v248, v249
	v_cvt_u32_f32_e32 v248, v241
	v_add_u32_e32 v248, -1, v248
	v_lshl_add_u32 v248, v248, 2, s77
	v_add_u32_e32 v249, 36, v253
	ds_write_b32 v248, v249
	v_cvt_u32_f32_e32 v248, v242
	v_add_u32_e32 v248, -1, v248
	v_lshl_add_u32 v248, v248, 2, s77
	v_add_u32_e32 v249, 20, v253
	ds_write_b32 v248, v249
	v_cvt_u32_f32_e32 v248, v243
	v_add_u32_e32 v248, -1, v248
	v_lshl_add_u32 v248, v248, 2, s77
	v_add_u32_e32 v249, 52, v253
	ds_write_b32 v248, v249
	s_or_b64 exec, exec, s[80:81]
	v_mov_b32_e32 v244, 0
	v_mov_b32_e32 v245, 0
	v_mov_b32_e32 v246, v252
	v_mov_b32_e32 v247, 0
	v_mov_b64_e32 v[240:241], 0
	v_mov_b64_e32 v[242:243], 0
	s_nop 1
	v_smfmac_f32_16x16x64_bf16 v[240:243], v[244:247], v[232:239], v223
	s_nop 15
	s_nop 3
	s_and_saveexec_b64 s[80:81], s[78:79]
	v_cvt_u32_f32_e32 v248, v240
	v_add_u32_e32 v248, -1, v248
	v_lshl_add_u32 v248, v248, 2, s77
	v_add_u32_e32 v249, 8, v253
	ds_write_b32 v248, v249
	v_cvt_u32_f32_e32 v248, v241
	v_add_u32_e32 v248, -1, v248
	v_lshl_add_u32 v248, v248, 2, s77
	v_add_u32_e32 v249, 40, v253
	ds_write_b32 v248, v249
	v_cvt_u32_f32_e32 v248, v242
	v_add_u32_e32 v248, -1, v248
	v_lshl_add_u32 v248, v248, 2, s77
	v_add_u32_e32 v249, 24, v253
	ds_write_b32 v248, v249
	v_cvt_u32_f32_e32 v248, v243
	v_add_u32_e32 v248, -1, v248
	v_lshl_add_u32 v248, v248, 2, s77
	v_add_u32_e32 v249, 56, v253
	ds_write_b32 v248, v249
	s_or_b64 exec, exec, s[80:81]
	v_mov_b32_e32 v244, 0
	v_mov_b32_e32 v245, 0
	v_mov_b32_e32 v246, 0
	v_mov_b32_e32 v247, v252
	v_mov_b64_e32 v[240:241], 0
	v_mov_b64_e32 v[242:243], 0
	s_nop 1
	v_smfmac_f32_16x16x64_bf16 v[240:243], v[244:247], v[232:239], v223
	s_nop 15
	s_nop 3
	s_and_saveexec_b64 s[80:81], s[78:79]
	v_cvt_u32_f32_e32 v248, v240
	v_add_u32_e32 v248, -1, v248
	v_lshl_add_u32 v248, v248, 2, s77
	v_add_u32_e32 v249, 12, v253
	ds_write_b32 v248, v249
	v_cvt_u32_f32_e32 v248, v241
	v_add_u32_e32 v248, -1, v248
	v_lshl_add_u32 v248, v248, 2, s77
	v_add_u32_e32 v249, 44, v253
	ds_write_b32 v248, v249
	v_cvt_u32_f32_e32 v248, v242
	v_add_u32_e32 v248, -1, v248
	v_lshl_add_u32 v248, v248, 2, s77
	v_add_u32_e32 v249, 28, v253
	ds_write_b32 v248, v249
	v_cvt_u32_f32_e32 v248, v243
	v_add_u32_e32 v248, -1, v248
	v_lshl_add_u32 v248, v248, 2, s77
	v_add_u32_e32 v249, 60, v253
	ds_write_b32 v248, v249
	s_or_b64 exec, exec, s[80:81]
	v_bfe_u32 v248, v206, 3, 2
	v_lshrrev_b32_e32 v249, 5, v206
	v_lshlrev_b32_e32 v248, 4, v248
	v_lshl_or_b32 v248, v249, 3, v248
	v_and_b32_e32 v249, 7, v206
	v_or_b32_e32 v248, v248, v249
	v_lshl_add_u32 v248, v248, 2, s77
	s_waitcnt lgkmcnt(0)
	ds_read_b32 v254, v248
	v_and_b32_e32 v248, 15, v206
	v_bfe_u32 v249, v248, 1, 2
	v_lshrrev_b32_e32 v250, 3, v248
	v_lshlrev_b32_e32 v249, 4, v249
	v_lshl_or_b32 v249, v250, 3, v249
	v_and_b32_e32 v250, 1, v248
	v_lshl_or_b32 v249, v250, 2, v249
	v_lshl_add_u32 v249, v249, 2, s77
	ds_read_b128 v[248:251], v249
	s_lshr_b32 s76, s19, 6
	s_add_i32 s76, s76, 0x20000
	v_lshrrev_b32_e32 v252, 4, v206
	v_lshl_add_u32 v252, v252, 7, s76
	s_waitcnt lgkmcnt(0)
	v_add_u32_e32 v248, v252, v248
	v_add_u32_e32 v249, v252, v249
	v_add_u32_e32 v250, v252, v250
	v_add_u32_e32 v251, v252, v251
	v_cvt_pk_bf16_f32 v236, v224, v225
	v_cvt_pk_bf16_f32 v237, v226, v227
	v_lshlrev_b32_e32 v238, 16, v236
	v_and_b32_e32 v239, 0xffff0000, v236
	v_lshlrev_b32_e32 v240, 16, v237
	v_and_b32_e32 v241, 0xffff0000, v237
	v_sub_f32_e32 v238, v224, v238
	v_sub_f32_e32 v239, v225, v239
	v_sub_f32_e32 v240, v226, v240
	v_sub_f32_e32 v241, v227, v241
	v_cvt_pk_bf16_f32 v238, v238, v239
	v_cvt_pk_bf16_f32 v239, v240, v241
	ds_write_b16 v248, v236
	ds_write_b16_d16_hi v249, v236
	ds_write_b16 v250, v237
	ds_write_b16_d16_hi v251, v237
	ds_write_b16 v248, v238 offset:2176
	ds_write_b16_d16_hi v249, v238 offset:2176
	ds_write_b16 v250, v239 offset:2176
	ds_write_b16_d16_hi v251, v239 offset:2176
	s_waitcnt vmcnt(23)
	s_waitcnt vmcnt(22)
	s_waitcnt vmcnt(21)
	s_waitcnt vmcnt(20)
	s_waitcnt vmcnt(19)
	s_waitcnt vmcnt(18)
	s_waitcnt vmcnt(17)
	s_waitcnt vmcnt(16)
	ds_read_b32 v66, v187 offset:192
	v_or_b32_e32 v103, 48, v132
	v_add_u32_e32 v104, 1, v102
	v_cmp_eq_u32_e32 vcc, v102, v103
	v_add_u32_e32 v105, 3, v102
	v_add_u32_e32 v106, 2, v102
	v_cndmask_b32_e64 v72, 0, 1.0, vcc
	v_cmp_eq_u32_e32 vcc, v104, v103
	v_or_b32_e32 v107, 50, v132
	v_or_b32_e32 v108, 52, v132
	v_cndmask_b32_e64 v73, 0, 1.0, vcc
	v_cmp_eq_u32_e32 vcc, v105, v103
	s_waitcnt lgkmcnt(0)
	v_pk_fma_f32 v[68:69], v[66:67], v[68:69], v[72:73] op_sel_hi:[0,1,1] neg_lo:[1,0,0] neg_hi:[1,0,0]
	v_cvt_pk_bf16_f32 v68, v68, v69
	v_cndmask_b32_e64 v73, 0, 1.0, vcc
	v_cmp_eq_u32_e32 vcc, v106, v103
	v_or_b32_e32 v109, 54, v132
	v_or_b32_e32 v110, 56, v132
	v_cndmask_b32_e64 v72, 0, 1.0, vcc
	v_pk_fma_f32 v[66:67], v[66:67], v[70:71], v[72:73] op_sel_hi:[0,1,1] neg_lo:[1,0,0] neg_hi:[1,0,0]
	v_cvt_pk_bf16_f32 v69, v66, v67
	ds_write_b64 v186, v[68:69]
	ds_read_b32 v66, v187 offset:200
	v_cmp_eq_u32_e32 vcc, v102, v107
	v_or_b32_e32 v111, 58, v132
	v_or_b32_e32 v112, 60, v132
	v_cndmask_b32_e64 v68, 0, 1.0, vcc
	v_cmp_eq_u32_e32 vcc, v104, v107
	v_or_b32_e32 v113, 62, v132
	v_or_b32_e32 v193, 2, v132
	v_cndmask_b32_e64 v69, 0, 1.0, vcc
	v_cmp_eq_u32_e32 vcc, v105, v107
	s_waitcnt lgkmcnt(0)
	v_pk_fma_f32 v[68:69], v[66:67], v[78:79], v[68:69] op_sel_hi:[0,1,1] neg_lo:[1,0,0] neg_hi:[1,0,0]
	v_cvt_pk_bf16_f32 v68, v68, v69
	v_cndmask_b32_e64 v71, 0, 1.0, vcc
	v_cmp_eq_u32_e32 vcc, v106, v107
	v_or_b32_e32 v192, 4, v132
	v_or_b32_e32 v190, 6, v132
	v_cndmask_b32_e64 v70, 0, 1.0, vcc
	v_pk_fma_f32 v[66:67], v[66:67], v[80:81], v[70:71] op_sel_hi:[0,1,1] neg_lo:[1,0,0] neg_hi:[1,0,0]
	v_cvt_pk_bf16_f32 v69, v66, v67
	ds_write_b64 v186, v[68:69] offset:544
	ds_read_b32 v66, v187 offset:208
	v_cmp_eq_u32_e32 vcc, v102, v108
	v_or_b32_e32 v149, 8, v132
	v_or_b32_e32 v148, 10, v132
	v_cndmask_b32_e64 v68, 0, 1.0, vcc
	v_cmp_eq_u32_e32 vcc, v104, v108
	v_or_b32_e32 v147, 12, v132
	v_or_b32_e32 v146, 14, v132
	v_cndmask_b32_e64 v69, 0, 1.0, vcc
	v_cmp_eq_u32_e32 vcc, v105, v108
	s_waitcnt lgkmcnt(0)
	v_pk_fma_f32 v[68:69], v[66:67], v[82:83], v[68:69] op_sel_hi:[0,1,1] neg_lo:[1,0,0] neg_hi:[1,0,0]
	v_cvt_pk_bf16_f32 v68, v68, v69
	v_cndmask_b32_e64 v71, 0, 1.0, vcc
	v_cmp_eq_u32_e32 vcc, v106, v108
	s_nop 1
	v_cndmask_b32_e64 v70, 0, 1.0, vcc
	v_pk_fma_f32 v[66:67], v[66:67], v[84:85], v[70:71] op_sel_hi:[0,1,1] neg_lo:[1,0,0] neg_hi:[1,0,0]
	v_cvt_pk_bf16_f32 v69, v66, v67
	ds_write_b64 v186, v[68:69] offset:1088
	ds_read_b32 v66, v187 offset:216
	v_cmp_eq_u32_e32 vcc, v102, v109
	s_nop 1
	v_cndmask_b32_e64 v68, 0, 1.0, vcc
	v_cmp_eq_u32_e32 vcc, v104, v109
	s_nop 1
	v_cndmask_b32_e64 v69, 0, 1.0, vcc
	v_cmp_eq_u32_e32 vcc, v105, v109
	s_waitcnt lgkmcnt(0)
	v_pk_fma_f32 v[68:69], v[66:67], v[90:91], v[68:69] op_sel_hi:[0,1,1] neg_lo:[1,0,0] neg_hi:[1,0,0]
	v_cvt_pk_bf16_f32 v68, v68, v69
	v_cndmask_b32_e64 v71, 0, 1.0, vcc
	v_cmp_eq_u32_e32 vcc, v106, v109
	s_nop 1
	v_cndmask_b32_e64 v70, 0, 1.0, vcc
	v_pk_fma_f32 v[66:67], v[66:67], v[92:93], v[70:71] op_sel_hi:[0,1,1] neg_lo:[1,0,0] neg_hi:[1,0,0]
	v_cvt_pk_bf16_f32 v69, v66, v67
	ds_write_b64 v186, v[68:69] offset:1632
	ds_read_b32 v66, v187 offset:224
	v_cmp_eq_u32_e32 vcc, v102, v110
	s_nop 1
	v_cndmask_b32_e64 v68, 0, 1.0, vcc
	v_cmp_eq_u32_e32 vcc, v104, v110
	s_nop 1
	v_cndmask_b32_e64 v69, 0, 1.0, vcc
	v_cmp_eq_u32_e32 vcc, v105, v110
	s_waitcnt lgkmcnt(0)
	v_pk_fma_f32 v[68:69], v[66:67], v[98:99], v[68:69] op_sel_hi:[0,1,1] neg_lo:[1,0,0] neg_hi:[1,0,0]
	v_cvt_pk_bf16_f32 v68, v68, v69
	v_cndmask_b32_e64 v71, 0, 1.0, vcc
	v_cmp_eq_u32_e32 vcc, v106, v110
	s_nop 1
	v_cndmask_b32_e64 v70, 0, 1.0, vcc
	v_pk_fma_f32 v[66:67], v[66:67], v[100:101], v[70:71] op_sel_hi:[0,1,1] neg_lo:[1,0,0] neg_hi:[1,0,0]
	v_cvt_pk_bf16_f32 v69, v66, v67
	ds_write_b64 v186, v[68:69] offset:2176
	ds_read_b32 v66, v187 offset:232
	v_cmp_eq_u32_e32 vcc, v102, v111
	s_nop 1
	v_cndmask_b32_e64 v68, 0, 1.0, vcc
	v_cmp_eq_u32_e32 vcc, v104, v111
	s_nop 1
	v_cndmask_b32_e64 v69, 0, 1.0, vcc
	v_cmp_eq_u32_e32 vcc, v105, v111
	s_waitcnt lgkmcnt(0)
	v_pk_fma_f32 v[62:63], v[66:67], v[62:63], v[68:69] op_sel_hi:[0,1,1] neg_lo:[1,0,0] neg_hi:[1,0,0]
	v_cvt_pk_bf16_f32 v62, v62, v63
	v_cndmask_b32_e64 v69, 0, 1.0, vcc
	v_cmp_eq_u32_e32 vcc, v106, v111
	s_nop 1
	v_cndmask_b32_e64 v68, 0, 1.0, vcc
	v_pk_fma_f32 v[64:65], v[66:67], v[64:65], v[68:69] op_sel_hi:[0,1,1] neg_lo:[1,0,0] neg_hi:[1,0,0]
	v_cvt_pk_bf16_f32 v63, v64, v65
	ds_write_b64 v186, v[62:63] offset:2720
	ds_read_b32 v62, v187 offset:240
	v_cmp_eq_u32_e32 vcc, v102, v112
	s_nop 1
	v_cndmask_b32_e64 v64, 0, 1.0, vcc
	v_cmp_eq_u32_e32 vcc, v104, v112
	s_nop 1
	v_cndmask_b32_e64 v65, 0, 1.0, vcc
	v_cmp_eq_u32_e32 vcc, v105, v112
	s_waitcnt lgkmcnt(0)
	v_pk_fma_f32 v[54:55], v[62:63], v[54:55], v[64:65] op_sel_hi:[0,1,1] neg_lo:[1,0,0] neg_hi:[1,0,0]
	v_cvt_pk_bf16_f32 v54, v54, v55
	v_cndmask_b32_e64 v65, 0, 1.0, vcc
	v_cmp_eq_u32_e32 vcc, v106, v112
	s_nop 1
	v_cndmask_b32_e64 v64, 0, 1.0, vcc
	v_pk_fma_f32 v[56:57], v[62:63], v[56:57], v[64:65] op_sel_hi:[0,1,1] neg_lo:[1,0,0] neg_hi:[1,0,0]
	v_cvt_pk_bf16_f32 v55, v56, v57
	ds_write_b64 v186, v[54:55] offset:3264
	ds_read_b32 v54, v187 offset:248
	v_cmp_eq_u32_e32 vcc, v102, v113
	s_nop 1
	v_cndmask_b32_e64 v56, 0, 1.0, vcc
	v_cmp_eq_u32_e32 vcc, v104, v113
	s_nop 1
	v_cndmask_b32_e64 v57, 0, 1.0, vcc
	v_cmp_eq_u32_e32 vcc, v105, v113
	s_waitcnt lgkmcnt(0)
	v_pk_fma_f32 v[46:47], v[54:55], v[46:47], v[56:57] op_sel_hi:[0,1,1] neg_lo:[1,0,0] neg_hi:[1,0,0]
	v_cvt_pk_bf16_f32 v46, v46, v47
	v_cndmask_b32_e64 v57, 0, 1.0, vcc
	v_cmp_eq_u32_e32 vcc, v106, v113
	s_nop 1
	v_cndmask_b32_e64 v56, 0, 1.0, vcc
	v_pk_fma_f32 v[48:49], v[54:55], v[48:49], v[56:57] op_sel_hi:[0,1,1] neg_lo:[1,0,0] neg_hi:[1,0,0]
	v_cvt_pk_bf16_f32 v47, v48, v49
	ds_write_b64 v186, v[46:47] offset:3808
	ds_read_b128 v[46:49], v1
	s_waitcnt lgkmcnt(0)
	ds_write_b128 v184, v[46:49]
	ds_read_b128 v[46:49], v1 offset:64
	s_waitcnt lgkmcnt(0)
	ds_write_b128 v184, v[46:49] offset:1024
	ds_read_b128 v[46:49], v1 offset:128
	s_waitcnt lgkmcnt(0)
	ds_write_b128 v184, v[46:49] offset:2048
	ds_read_b128 v[46:49], v1 offset:192
	s_waitcnt lgkmcnt(0)
	ds_write_b128 v184, v[46:49] offset:3072
	s_lshl_b32 s30, s25, 2
	s_mov_b32 s31, s21
	v_lshl_add_u64 v[46:47], v[126:127], 0, s[30:31]
	v_lshl_add_u64 v[48:49], v[128:129], 0, s[30:31]
	v_lshl_add_u64 v[54:55], v[134:135], 0, s[30:31]
	v_lshl_add_u64 v[56:57], v[136:137], 0, s[30:31]
	v_lshl_add_u64 v[62:63], v[138:139], 0, s[30:31]
	v_lshl_add_u64 v[64:65], v[140:141], 0, s[30:31]
	v_lshl_add_u64 v[98:99], v[142:143], 0, s[30:31]
	v_lshl_add_u64 v[100:101], v[144:145], 0, s[30:31]
	global_load_dwordx4 v[90:93], v[46:47], off nt
	global_load_dwordx4 v[82:85], v[48:49], off nt
	global_load_dwordx4 v[78:81], v[54:55], off nt
	global_load_dwordx4 v[70:73], v[56:57], off nt
	global_load_dwordx4 v[66:69], v[62:63], off nt
	s_nop 0
	global_load_dwordx4 v[62:65], v[64:65], off nt
	s_nop 0
	global_load_dwordx4 v[54:57], v[98:99], off nt
	global_load_dwordx4 v[46:49], v[100:101], off nt
	v_mov_b32_e32 v99, v189
	s_waitcnt vmcnt(23)
	s_waitcnt vmcnt(22)
	s_waitcnt vmcnt(21)
	s_waitcnt vmcnt(20)
	s_waitcnt vmcnt(19)
	s_waitcnt vmcnt(18)
	s_waitcnt vmcnt(17)
	s_waitcnt vmcnt(16)
	ds_read_b32 v98, v187 offset:192
	v_add_u32_e32 v102, 1, v99
	v_cmp_eq_u32_e32 vcc, v99, v103
	v_add_u32_e32 v104, 3, v99
	v_add_u32_e32 v105, 2, v99
	v_cndmask_b32_e64 v100, 0, 1.0, vcc
	v_cmp_eq_u32_e32 vcc, v102, v103
	s_nop 1
	v_cndmask_b32_e64 v101, 0, 1.0, vcc
	v_cmp_eq_u32_e32 vcc, v104, v103
	s_waitcnt lgkmcnt(0)
	v_pk_fma_f32 v[94:95], v[98:99], v[94:95], v[100:101] op_sel_hi:[0,1,1] neg_lo:[1,0,0] neg_hi:[1,0,0]
	v_cvt_pk_bf16_f32 v94, v94, v95
	v_cndmask_b32_e64 v101, 0, 1.0, vcc
	v_cmp_eq_u32_e32 vcc, v105, v103
	s_nop 1
	v_cndmask_b32_e64 v100, 0, 1.0, vcc
	v_pk_fma_f32 v[96:97], v[98:99], v[96:97], v[100:101] op_sel_hi:[0,1,1] neg_lo:[1,0,0] neg_hi:[1,0,0]
	v_cvt_pk_bf16_f32 v95, v96, v97
	ds_write_b64 v186, v[94:95]
	ds_read_b32 v94, v187 offset:200
	v_cmp_eq_u32_e32 vcc, v99, v107
	s_nop 1
	v_cndmask_b32_e64 v96, 0, 1.0, vcc
	v_cmp_eq_u32_e32 vcc, v102, v107
	s_nop 1
	v_cndmask_b32_e64 v97, 0, 1.0, vcc
	v_cmp_eq_u32_e32 vcc, v104, v107
	s_waitcnt lgkmcnt(0)
	v_pk_fma_f32 v[86:87], v[94:95], v[86:87], v[96:97] op_sel_hi:[0,1,1] neg_lo:[1,0,0] neg_hi:[1,0,0]
	v_cvt_pk_bf16_f32 v86, v86, v87
	v_cndmask_b32_e64 v97, 0, 1.0, vcc
	v_cmp_eq_u32_e32 vcc, v105, v107
	s_nop 1
	v_cndmask_b32_e64 v96, 0, 1.0, vcc
	v_pk_fma_f32 v[88:89], v[94:95], v[88:89], v[96:97] op_sel_hi:[0,1,1] neg_lo:[1,0,0] neg_hi:[1,0,0]
	v_cvt_pk_bf16_f32 v87, v88, v89
	ds_write_b64 v186, v[86:87] offset:544
	ds_read_b32 v86, v187 offset:208
	v_cmp_eq_u32_e32 vcc, v99, v108
	s_nop 1
	v_cndmask_b32_e64 v88, 0, 1.0, vcc
	v_cmp_eq_u32_e32 vcc, v102, v108
	s_nop 1
	v_cndmask_b32_e64 v89, 0, 1.0, vcc
	v_cmp_eq_u32_e32 vcc, v104, v108
	s_waitcnt lgkmcnt(0)
	v_pk_fma_f32 v[74:75], v[86:87], v[74:75], v[88:89] op_sel_hi:[0,1,1] neg_lo:[1,0,0] neg_hi:[1,0,0]
	v_cvt_pk_bf16_f32 v74, v74, v75
	v_cndmask_b32_e64 v89, 0, 1.0, vcc
	v_cmp_eq_u32_e32 vcc, v105, v108
	s_nop 1
	v_cndmask_b32_e64 v88, 0, 1.0, vcc
	v_pk_fma_f32 v[76:77], v[86:87], v[76:77], v[88:89] op_sel_hi:[0,1,1] neg_lo:[1,0,0] neg_hi:[1,0,0]
	v_cvt_pk_bf16_f32 v75, v76, v77
	ds_write_b64 v186, v[74:75] offset:1088
	ds_read_b32 v74, v187 offset:216
	v_cmp_eq_u32_e32 vcc, v99, v109
	s_nop 1
	v_cndmask_b32_e64 v76, 0, 1.0, vcc
	v_cmp_eq_u32_e32 vcc, v102, v109
	s_nop 1
	v_cndmask_b32_e64 v77, 0, 1.0, vcc
	v_cmp_eq_u32_e32 vcc, v104, v109
	s_waitcnt lgkmcnt(0)
	v_pk_fma_f32 v[58:59], v[74:75], v[58:59], v[76:77] op_sel_hi:[0,1,1] neg_lo:[1,0,0] neg_hi:[1,0,0]
	v_cvt_pk_bf16_f32 v58, v58, v59
	v_cndmask_b32_e64 v77, 0, 1.0, vcc
	v_cmp_eq_u32_e32 vcc, v105, v109
	s_nop 1
	v_cndmask_b32_e64 v76, 0, 1.0, vcc
	v_pk_fma_f32 v[60:61], v[74:75], v[60:61], v[76:77] op_sel_hi:[0,1,1] neg_lo:[1,0,0] neg_hi:[1,0,0]
	v_cvt_pk_bf16_f32 v59, v60, v61
	ds_write_b64 v186, v[58:59] offset:1632
	ds_read_b32 v58, v187 offset:224
	v_cmp_eq_u32_e32 vcc, v99, v110
	s_nop 1
	v_cndmask_b32_e64 v60, 0, 1.0, vcc
	v_cmp_eq_u32_e32 vcc, v102, v110
	s_nop 1
	v_cndmask_b32_e64 v61, 0, 1.0, vcc
	v_cmp_eq_u32_e32 vcc, v104, v110
	s_waitcnt lgkmcnt(0)
	v_pk_fma_f32 v[50:51], v[58:59], v[50:51], v[60:61] op_sel_hi:[0,1,1] neg_lo:[1,0,0] neg_hi:[1,0,0]
	v_cvt_pk_bf16_f32 v50, v50, v51
	v_cndmask_b32_e64 v61, 0, 1.0, vcc
	v_cmp_eq_u32_e32 vcc, v105, v110
	s_nop 1
	v_cndmask_b32_e64 v60, 0, 1.0, vcc
	v_pk_fma_f32 v[52:53], v[58:59], v[52:53], v[60:61] op_sel_hi:[0,1,1] neg_lo:[1,0,0] neg_hi:[1,0,0]
	v_cvt_pk_bf16_f32 v51, v52, v53
	ds_write_b64 v186, v[50:51] offset:2176
	ds_read_b32 v50, v187 offset:232
	v_cmp_eq_u32_e32 vcc, v99, v111
	s_nop 1
	v_cndmask_b32_e64 v52, 0, 1.0, vcc
	v_cmp_eq_u32_e32 vcc, v102, v111
	s_nop 1
	v_cndmask_b32_e64 v53, 0, 1.0, vcc
	v_cmp_eq_u32_e32 vcc, v104, v111
	s_waitcnt lgkmcnt(0)
	v_pk_fma_f32 v[42:43], v[50:51], v[42:43], v[52:53] op_sel_hi:[0,1,1] neg_lo:[1,0,0] neg_hi:[1,0,0]
	v_cvt_pk_bf16_f32 v42, v42, v43
	v_cndmask_b32_e64 v53, 0, 1.0, vcc
	v_cmp_eq_u32_e32 vcc, v105, v111
	s_nop 1
	v_cndmask_b32_e64 v52, 0, 1.0, vcc
	v_pk_fma_f32 v[44:45], v[50:51], v[44:45], v[52:53] op_sel_hi:[0,1,1] neg_lo:[1,0,0] neg_hi:[1,0,0]
	v_cvt_pk_bf16_f32 v43, v44, v45
	ds_write_b64 v186, v[42:43] offset:2720
	ds_read_b32 v42, v187 offset:240
	v_cmp_eq_u32_e32 vcc, v99, v112
	s_nop 1
	v_cndmask_b32_e64 v44, 0, 1.0, vcc
	v_cmp_eq_u32_e32 vcc, v102, v112
	s_nop 1
	v_cndmask_b32_e64 v45, 0, 1.0, vcc
	v_cmp_eq_u32_e32 vcc, v104, v112
	s_waitcnt lgkmcnt(0)
	v_pk_fma_f32 v[38:39], v[42:43], v[38:39], v[44:45] op_sel_hi:[0,1,1] neg_lo:[1,0,0] neg_hi:[1,0,0]
	v_cvt_pk_bf16_f32 v38, v38, v39
	v_cndmask_b32_e64 v45, 0, 1.0, vcc
	v_cmp_eq_u32_e32 vcc, v105, v112
	s_nop 1
	v_cndmask_b32_e64 v44, 0, 1.0, vcc
	v_pk_fma_f32 v[40:41], v[42:43], v[40:41], v[44:45] op_sel_hi:[0,1,1] neg_lo:[1,0,0] neg_hi:[1,0,0]
	v_cvt_pk_bf16_f32 v39, v40, v41
	ds_write_b64 v186, v[38:39] offset:3264
	ds_read_b32 v38, v187 offset:248
	v_cmp_eq_u32_e32 vcc, v99, v113
	s_nop 1
	v_cndmask_b32_e64 v40, 0, 1.0, vcc
	v_cmp_eq_u32_e32 vcc, v102, v113
	s_nop 1
	v_cndmask_b32_e64 v41, 0, 1.0, vcc
	v_cmp_eq_u32_e32 vcc, v104, v113
	s_waitcnt lgkmcnt(0)
	v_pk_fma_f32 v[34:35], v[38:39], v[34:35], v[40:41] op_sel_hi:[0,1,1] neg_lo:[1,0,0] neg_hi:[1,0,0]
	v_cvt_pk_bf16_f32 v34, v34, v35
	v_cndmask_b32_e64 v41, 0, 1.0, vcc
	v_cmp_eq_u32_e32 vcc, v105, v113
	s_nop 1
	v_cndmask_b32_e64 v40, 0, 1.0, vcc
	v_pk_fma_f32 v[36:37], v[38:39], v[36:37], v[40:41] op_sel_hi:[0,1,1] neg_lo:[1,0,0] neg_hi:[1,0,0]
	v_cvt_pk_bf16_f32 v35, v36, v37
	ds_write_b64 v186, v[34:35] offset:3808
	ds_read_b128 v[34:37], v1
	s_waitcnt lgkmcnt(0)
	ds_write_b128 v184, v[34:37] offset:4096
	ds_read_b128 v[34:37], v1 offset:64
	s_waitcnt lgkmcnt(0)
	ds_write_b128 v184, v[34:37] offset:5120
	ds_read_b128 v[34:37], v1 offset:128
	s_waitcnt lgkmcnt(0)
	ds_write_b128 v184, v[34:37] offset:6144
	ds_read_b128 v[34:37], v1 offset:192
	s_waitcnt lgkmcnt(0)
	ds_write_b128 v184, v[34:37] offset:7168
	s_lshl_b32 s28, s24, 2
	s_mov_b32 s29, s21
	v_lshl_add_u64 v[34:35], v[126:127], 0, s[28:29]
	v_lshl_add_u64 v[36:37], v[128:129], 0, s[28:29]
	v_lshl_add_u64 v[38:39], v[134:135], 0, s[28:29]
	v_lshl_add_u64 v[40:41], v[136:137], 0, s[28:29]
	v_lshl_add_u64 v[42:43], v[138:139], 0, s[28:29]
	v_lshl_add_u64 v[44:45], v[140:141], 0, s[28:29]
	v_lshl_add_u64 v[50:51], v[142:143], 0, s[28:29]
	v_lshl_add_u64 v[52:53], v[144:145], 0, s[28:29]
	global_load_dwordx4 v[122:125], v[34:35], off nt
	global_load_dwordx4 v[114:117], v[36:37], off nt
	global_load_dwordx4 v[106:109], v[38:39], off nt
	global_load_dwordx4 v[86:89], v[40:41], off nt
	global_load_dwordx4 v[74:77], v[42:43], off nt
	s_nop 0
	global_load_dwordx4 v[42:45], v[44:45], off nt
	s_nop 0
	global_load_dwordx4 v[38:41], v[50:51], off nt
	global_load_dwordx4 v[34:37], v[52:53], off nt
	v_mov_b32_e32 v50, v188
	s_waitcnt vmcnt(23)
	s_waitcnt vmcnt(22)
	s_waitcnt vmcnt(21)
	s_waitcnt vmcnt(20)
	s_waitcnt vmcnt(19)
	s_waitcnt vmcnt(18)
	s_waitcnt vmcnt(17)
	s_waitcnt vmcnt(16)
	ds_read_b32 v50, v187 offset:192
	s_waitcnt lgkmcnt(0)
	v_pk_fma_f32 v[30:31], v[50:51], v[30:31], 0 op_sel_hi:[0,1,0] neg_lo:[1,0,0] neg_hi:[1,0,0]
	v_pk_fma_f32 v[32:33], v[50:51], v[32:33], 0 op_sel_hi:[0,1,0] neg_lo:[1,0,0] neg_hi:[1,0,0]
	v_cvt_pk_bf16_f32 v30, v30, v31
	v_cvt_pk_bf16_f32 v31, v32, v33
	ds_write_b64 v186, v[30:31]
	ds_read_b32 v30, v187 offset:200
	s_waitcnt lgkmcnt(0)
	v_pk_fma_f32 v[26:27], v[30:31], v[26:27], 0 op_sel_hi:[0,1,0] neg_lo:[1,0,0] neg_hi:[1,0,0]
	v_pk_fma_f32 v[28:29], v[30:31], v[28:29], 0 op_sel_hi:[0,1,0] neg_lo:[1,0,0] neg_hi:[1,0,0]
	v_cvt_pk_bf16_f32 v26, v26, v27
	v_cvt_pk_bf16_f32 v27, v28, v29
	ds_write_b64 v186, v[26:27] offset:544
	ds_read_b32 v26, v187 offset:208
	s_waitcnt lgkmcnt(0)
	v_pk_fma_f32 v[22:23], v[26:27], v[22:23], 0 op_sel_hi:[0,1,0] neg_lo:[1,0,0] neg_hi:[1,0,0]
	v_pk_fma_f32 v[24:25], v[26:27], v[24:25], 0 op_sel_hi:[0,1,0] neg_lo:[1,0,0] neg_hi:[1,0,0]
	v_cvt_pk_bf16_f32 v22, v22, v23
	v_cvt_pk_bf16_f32 v23, v24, v25
	ds_write_b64 v186, v[22:23] offset:1088
	ds_read_b32 v22, v187 offset:216
	s_waitcnt lgkmcnt(0)
	v_pk_fma_f32 v[18:19], v[22:23], v[18:19], 0 op_sel_hi:[0,1,0] neg_lo:[1,0,0] neg_hi:[1,0,0]
	v_pk_fma_f32 v[20:21], v[22:23], v[20:21], 0 op_sel_hi:[0,1,0] neg_lo:[1,0,0] neg_hi:[1,0,0]
	v_cvt_pk_bf16_f32 v18, v18, v19
	v_cvt_pk_bf16_f32 v19, v20, v21
	ds_write_b64 v186, v[18:19] offset:1632
	ds_read_b32 v18, v187 offset:224
	s_waitcnt lgkmcnt(0)
	v_pk_fma_f32 v[14:15], v[18:19], v[14:15], 0 op_sel_hi:[0,1,0] neg_lo:[1,0,0] neg_hi:[1,0,0]
	v_pk_fma_f32 v[16:17], v[18:19], v[16:17], 0 op_sel_hi:[0,1,0] neg_lo:[1,0,0] neg_hi:[1,0,0]
	v_cvt_pk_bf16_f32 v14, v14, v15
	v_cvt_pk_bf16_f32 v15, v16, v17
	ds_write_b64 v186, v[14:15] offset:2176
	ds_read_b32 v14, v187 offset:232
	s_waitcnt lgkmcnt(0)
	v_pk_fma_f32 v[10:11], v[14:15], v[10:11], 0 op_sel_hi:[0,1,0] neg_lo:[1,0,0] neg_hi:[1,0,0]
	v_pk_fma_f32 v[12:13], v[14:15], v[12:13], 0 op_sel_hi:[0,1,0] neg_lo:[1,0,0] neg_hi:[1,0,0]
	v_cvt_pk_bf16_f32 v10, v10, v11
	v_cvt_pk_bf16_f32 v11, v12, v13
	ds_write_b64 v186, v[10:11] offset:2720
	ds_read_b32 v10, v187 offset:240
	s_waitcnt lgkmcnt(0)
	v_pk_fma_f32 v[6:7], v[10:11], v[6:7], 0 op_sel_hi:[0,1,0] neg_lo:[1,0,0] neg_hi:[1,0,0]
	v_pk_fma_f32 v[8:9], v[10:11], v[8:9], 0 op_sel_hi:[0,1,0] neg_lo:[1,0,0] neg_hi:[1,0,0]
	v_cvt_pk_bf16_f32 v6, v6, v7
	v_cvt_pk_bf16_f32 v7, v8, v9
	ds_write_b64 v186, v[6:7] offset:3264
	ds_read_b32 v6, v187 offset:248
	s_waitcnt lgkmcnt(0)
	v_pk_fma_f32 v[2:3], v[6:7], v[2:3], 0 op_sel_hi:[0,1,0] neg_lo:[1,0,0] neg_hi:[1,0,0]
	v_pk_fma_f32 v[4:5], v[6:7], v[4:5], 0 op_sel_hi:[0,1,0] neg_lo:[1,0,0] neg_hi:[1,0,0]
	v_cvt_pk_bf16_f32 v2, v2, v3
	v_cvt_pk_bf16_f32 v3, v4, v5
	ds_write_b64 v186, v[2:3] offset:3808
	ds_read_b128 v[2:5], v1
	s_waitcnt lgkmcnt(0)
	ds_write_b128 v184, v[2:5] offset:8192
	ds_read_b128 v[2:5], v1 offset:64
	s_waitcnt lgkmcnt(0)
	ds_write_b128 v184, v[2:5] offset:9216
	ds_read_b128 v[2:5], v1 offset:128
	s_waitcnt lgkmcnt(0)
	ds_write_b128 v184, v[2:5] offset:10240
	ds_read_b128 v[2:5], v1 offset:192
	s_waitcnt lgkmcnt(0)
	ds_write_b128 v184, v[2:5] offset:11264
	s_lshl_b32 s26, s23, 2
	s_mov_b32 s27, s21
	v_lshl_add_u64 v[2:3], v[126:127], 0, s[26:27]
	v_lshl_add_u64 v[4:5], v[128:129], 0, s[26:27]
	v_lshl_add_u64 v[6:7], v[134:135], 0, s[26:27]
	v_lshl_add_u64 v[8:9], v[136:137], 0, s[26:27]
	v_lshl_add_u64 v[10:11], v[138:139], 0, s[26:27]
	v_lshl_add_u64 v[12:13], v[140:141], 0, s[26:27]
	v_lshl_add_u64 v[14:15], v[142:143], 0, s[26:27]
	v_lshl_add_u64 v[16:17], v[144:145], 0, s[26:27]
	global_load_dwordx4 v[118:121], v[2:3], off nt
	global_load_dwordx4 v[110:113], v[4:5], off nt
	global_load_dwordx4 v[102:105], v[6:7], off nt
	global_load_dwordx4 v[98:101], v[8:9], off nt
	global_load_dwordx4 v[58:61], v[10:11], off nt
	global_load_dwordx4 v[50:53], v[12:13], off nt
	global_load_dwordx4 v[30:33], v[14:15], off nt
	global_load_dwordx4 v[22:25], v[16:17], off nt
	v_mov_b32_e32 v2, v198
	s_waitcnt vmcnt(23)
	s_waitcnt vmcnt(22)
	s_waitcnt vmcnt(21)
	s_waitcnt vmcnt(20)
	s_waitcnt vmcnt(19)
	s_waitcnt vmcnt(18)
	s_waitcnt vmcnt(17)
	s_waitcnt vmcnt(16)
	ds_read_b32 v2, v187 offset:192
	s_waitcnt lgkmcnt(0)
	v_pk_fma_f32 v[4:5], v[2:3], v[90:91], 0 op_sel_hi:[0,1,0] neg_lo:[1,0,0] neg_hi:[1,0,0]
	v_pk_fma_f32 v[2:3], v[2:3], v[92:93], 0 op_sel_hi:[0,1,0] neg_lo:[1,0,0] neg_hi:[1,0,0]
	v_cvt_pk_bf16_f32 v4, v4, v5
	v_cvt_pk_bf16_f32 v5, v2, v3
	ds_write_b64 v186, v[4:5]
	ds_read_b32 v2, v187 offset:200
	s_waitcnt lgkmcnt(0)
	v_pk_fma_f32 v[4:5], v[2:3], v[82:83], 0 op_sel_hi:[0,1,0] neg_lo:[1,0,0] neg_hi:[1,0,0]
	v_pk_fma_f32 v[2:3], v[2:3], v[84:85], 0 op_sel_hi:[0,1,0] neg_lo:[1,0,0] neg_hi:[1,0,0]
	v_cvt_pk_bf16_f32 v4, v4, v5
	v_cvt_pk_bf16_f32 v5, v2, v3
	ds_write_b64 v186, v[4:5] offset:544
	ds_read_b32 v2, v187 offset:208
	s_waitcnt lgkmcnt(0)
	v_pk_fma_f32 v[4:5], v[2:3], v[78:79], 0 op_sel_hi:[0,1,0] neg_lo:[1,0,0] neg_hi:[1,0,0]
	v_pk_fma_f32 v[2:3], v[2:3], v[80:81], 0 op_sel_hi:[0,1,0] neg_lo:[1,0,0] neg_hi:[1,0,0]
	v_cvt_pk_bf16_f32 v4, v4, v5
	v_cvt_pk_bf16_f32 v5, v2, v3
	ds_write_b64 v186, v[4:5] offset:1088
	ds_read_b32 v2, v187 offset:216
	s_waitcnt lgkmcnt(0)
	v_pk_fma_f32 v[4:5], v[2:3], v[70:71], 0 op_sel_hi:[0,1,0] neg_lo:[1,0,0] neg_hi:[1,0,0]
	v_pk_fma_f32 v[2:3], v[2:3], v[72:73], 0 op_sel_hi:[0,1,0] neg_lo:[1,0,0] neg_hi:[1,0,0]
	v_cvt_pk_bf16_f32 v4, v4, v5
	v_cvt_pk_bf16_f32 v5, v2, v3
	ds_write_b64 v186, v[4:5] offset:1632
	ds_read_b32 v2, v187 offset:224
	s_waitcnt lgkmcnt(0)
	v_pk_fma_f32 v[4:5], v[2:3], v[66:67], 0 op_sel_hi:[0,1,0] neg_lo:[1,0,0] neg_hi:[1,0,0]
	v_pk_fma_f32 v[2:3], v[2:3], v[68:69], 0 op_sel_hi:[0,1,0] neg_lo:[1,0,0] neg_hi:[1,0,0]
	v_cvt_pk_bf16_f32 v4, v4, v5
	v_cvt_pk_bf16_f32 v5, v2, v3
	ds_write_b64 v186, v[4:5] offset:2176
	ds_read_b32 v2, v187 offset:232
	s_waitcnt lgkmcnt(0)
	v_pk_fma_f32 v[4:5], v[2:3], v[62:63], 0 op_sel_hi:[0,1,0] neg_lo:[1,0,0] neg_hi:[1,0,0]
	v_pk_fma_f32 v[2:3], v[2:3], v[64:65], 0 op_sel_hi:[0,1,0] neg_lo:[1,0,0] neg_hi:[1,0,0]
	v_cvt_pk_bf16_f32 v4, v4, v5
	v_cvt_pk_bf16_f32 v5, v2, v3
	ds_write_b64 v186, v[4:5] offset:2720
	ds_read_b32 v2, v187 offset:240
	s_waitcnt lgkmcnt(0)
	v_pk_fma_f32 v[4:5], v[2:3], v[54:55], 0 op_sel_hi:[0,1,0] neg_lo:[1,0,0] neg_hi:[1,0,0]
	v_pk_fma_f32 v[2:3], v[2:3], v[56:57], 0 op_sel_hi:[0,1,0] neg_lo:[1,0,0] neg_hi:[1,0,0]
	v_cvt_pk_bf16_f32 v4, v4, v5
	v_cvt_pk_bf16_f32 v5, v2, v3
	ds_write_b64 v186, v[4:5] offset:3264
	ds_read_b32 v2, v187 offset:248
	s_waitcnt lgkmcnt(0)
	v_pk_fma_f32 v[4:5], v[2:3], v[46:47], 0 op_sel_hi:[0,1,0] neg_lo:[1,0,0] neg_hi:[1,0,0]
	v_pk_fma_f32 v[2:3], v[2:3], v[48:49], 0 op_sel_hi:[0,1,0] neg_lo:[1,0,0] neg_hi:[1,0,0]
	v_cvt_pk_bf16_f32 v4, v4, v5
	v_cvt_pk_bf16_f32 v5, v2, v3
	ds_write_b64 v186, v[4:5] offset:3808
	ds_read_b128 v[2:5], v1
	s_waitcnt lgkmcnt(0)
	ds_write_b128 v184, v[2:5] offset:12288
	ds_read_b128 v[2:5], v1 offset:64
	s_waitcnt lgkmcnt(0)
	ds_write_b128 v184, v[2:5] offset:13312
	ds_read_b128 v[2:5], v1 offset:128
	s_waitcnt lgkmcnt(0)
	ds_write_b128 v184, v[2:5] offset:14336
	ds_read_b128 v[2:5], v1 offset:192
	s_waitcnt lgkmcnt(0)
	ds_write_b128 v184, v[2:5] offset:15360
	s_lshl_b32 s24, s22, 2
	s_mov_b32 s25, s21
	v_lshl_add_u64 v[2:3], v[126:127], 0, s[24:25]
	v_lshl_add_u64 v[6:7], v[134:135], 0, s[24:25]
	v_lshl_add_u64 v[8:9], v[136:137], 0, s[24:25]
	v_lshl_add_u64 v[14:15], v[142:143], 0, s[24:25]
	v_lshl_add_u64 v[4:5], v[128:129], 0, s[24:25]
	v_lshl_add_u64 v[10:11], v[138:139], 0, s[24:25]
	v_lshl_add_u64 v[12:13], v[140:141], 0, s[24:25]
	v_lshl_add_u64 v[18:19], v[144:145], 0, s[24:25]
	global_load_dwordx4 v[94:97], v[2:3], off nt
	global_load_dwordx4 v[90:93], v[4:5], off nt
	global_load_dwordx4 v[82:85], v[6:7], off nt
	global_load_dwordx4 v[70:73], v[8:9], off nt
	global_load_dwordx4 v[54:57], v[10:11], off nt
	global_load_dwordx4 v[26:29], v[12:13], off nt
	s_nop 0
	global_load_dwordx4 v[14:17], v[14:15], off nt
	s_nop 0
	global_load_dwordx4 v[6:9], v[18:19], off nt
	v_mov_b32_e32 v2, v197
	s_waitcnt vmcnt(23)
	s_waitcnt vmcnt(22)
	s_waitcnt vmcnt(21)
	s_waitcnt vmcnt(20)
	s_waitcnt vmcnt(19)
	s_waitcnt vmcnt(18)
	s_waitcnt vmcnt(17)
	s_waitcnt vmcnt(16)
	ds_read_b32 v2, v187 offset:192
	s_waitcnt lgkmcnt(0)
	v_pk_fma_f32 v[4:5], v[2:3], v[122:123], 0 op_sel_hi:[0,1,0] neg_lo:[1,0,0] neg_hi:[1,0,0]
	v_pk_fma_f32 v[2:3], v[2:3], v[124:125], 0 op_sel_hi:[0,1,0] neg_lo:[1,0,0] neg_hi:[1,0,0]
	v_cvt_pk_bf16_f32 v4, v4, v5
	v_cvt_pk_bf16_f32 v5, v2, v3
	ds_write_b64 v186, v[4:5]
	ds_read_b32 v2, v187 offset:200
	s_waitcnt lgkmcnt(0)
	v_pk_fma_f32 v[4:5], v[2:3], v[114:115], 0 op_sel_hi:[0,1,0] neg_lo:[1,0,0] neg_hi:[1,0,0]
	v_pk_fma_f32 v[2:3], v[2:3], v[116:117], 0 op_sel_hi:[0,1,0] neg_lo:[1,0,0] neg_hi:[1,0,0]
	v_cvt_pk_bf16_f32 v4, v4, v5
	v_cvt_pk_bf16_f32 v5, v2, v3
	ds_write_b64 v186, v[4:5] offset:544
	ds_read_b32 v2, v187 offset:208
	s_waitcnt lgkmcnt(0)
	v_pk_fma_f32 v[4:5], v[2:3], v[106:107], 0 op_sel_hi:[0,1,0] neg_lo:[1,0,0] neg_hi:[1,0,0]
	v_pk_fma_f32 v[2:3], v[2:3], v[108:109], 0 op_sel_hi:[0,1,0] neg_lo:[1,0,0] neg_hi:[1,0,0]
	v_cvt_pk_bf16_f32 v4, v4, v5
	v_cvt_pk_bf16_f32 v5, v2, v3
	ds_write_b64 v186, v[4:5] offset:1088
	ds_read_b32 v2, v187 offset:216
	s_waitcnt lgkmcnt(0)
	v_pk_fma_f32 v[4:5], v[2:3], v[86:87], 0 op_sel_hi:[0,1,0] neg_lo:[1,0,0] neg_hi:[1,0,0]
	v_pk_fma_f32 v[2:3], v[2:3], v[88:89], 0 op_sel_hi:[0,1,0] neg_lo:[1,0,0] neg_hi:[1,0,0]
	v_cvt_pk_bf16_f32 v4, v4, v5
	v_cvt_pk_bf16_f32 v5, v2, v3
	ds_write_b64 v186, v[4:5] offset:1632
	ds_read_b32 v2, v187 offset:224
	s_waitcnt lgkmcnt(0)
	v_pk_fma_f32 v[4:5], v[2:3], v[74:75], 0 op_sel_hi:[0,1,0] neg_lo:[1,0,0] neg_hi:[1,0,0]
	v_pk_fma_f32 v[2:3], v[2:3], v[76:77], 0 op_sel_hi:[0,1,0] neg_lo:[1,0,0] neg_hi:[1,0,0]
	v_cvt_pk_bf16_f32 v4, v4, v5
	v_cvt_pk_bf16_f32 v5, v2, v3
	ds_write_b64 v186, v[4:5] offset:2176
	ds_read_b32 v2, v187 offset:232
	s_waitcnt lgkmcnt(0)
	v_pk_fma_f32 v[4:5], v[2:3], v[42:43], 0 op_sel_hi:[0,1,0] neg_lo:[1,0,0] neg_hi:[1,0,0]
	v_pk_fma_f32 v[2:3], v[2:3], v[44:45], 0 op_sel_hi:[0,1,0] neg_lo:[1,0,0] neg_hi:[1,0,0]
	v_cvt_pk_bf16_f32 v4, v4, v5
	v_cvt_pk_bf16_f32 v5, v2, v3
	ds_write_b64 v186, v[4:5] offset:2720
	ds_read_b32 v2, v187 offset:240
	s_waitcnt lgkmcnt(0)
	v_pk_fma_f32 v[4:5], v[2:3], v[38:39], 0 op_sel_hi:[0,1,0] neg_lo:[1,0,0] neg_hi:[1,0,0]
	v_pk_fma_f32 v[2:3], v[2:3], v[40:41], 0 op_sel_hi:[0,1,0] neg_lo:[1,0,0] neg_hi:[1,0,0]
	v_cvt_pk_bf16_f32 v4, v4, v5
	v_cvt_pk_bf16_f32 v5, v2, v3
	ds_write_b64 v186, v[4:5] offset:3264
	ds_read_b32 v2, v187 offset:248
	s_waitcnt lgkmcnt(0)
	v_pk_fma_f32 v[4:5], v[2:3], v[34:35], 0 op_sel_hi:[0,1,0] neg_lo:[1,0,0] neg_hi:[1,0,0]
	v_pk_fma_f32 v[2:3], v[2:3], v[36:37], 0 op_sel_hi:[0,1,0] neg_lo:[1,0,0] neg_hi:[1,0,0]
	v_cvt_pk_bf16_f32 v4, v4, v5
	v_cvt_pk_bf16_f32 v5, v2, v3
	ds_write_b64 v186, v[4:5] offset:3808
	ds_read_b128 v[2:5], v1
	s_waitcnt lgkmcnt(0)
	ds_write_b128 v184, v[2:5] offset:16384
	ds_read_b128 v[2:5], v1 offset:64
	s_waitcnt lgkmcnt(0)
	ds_write_b128 v184, v[2:5] offset:17408
	ds_read_b128 v[2:5], v1 offset:128
	s_waitcnt lgkmcnt(0)
	ds_write_b128 v184, v[2:5] offset:18432
	ds_read_b128 v[2:5], v1 offset:192
	s_waitcnt lgkmcnt(0)
	ds_write_b128 v184, v[2:5] offset:19456
	s_lshl_b32 s22, s7, 2
	s_mov_b32 s23, s21
	v_lshl_add_u64 v[2:3], v[126:127], 0, s[22:23]
	v_lshl_add_u64 v[4:5], v[128:129], 0, s[22:23]
	v_lshl_add_u64 v[10:11], v[134:135], 0, s[22:23]
	v_lshl_add_u64 v[12:13], v[136:137], 0, s[22:23]
	v_lshl_add_u64 v[34:35], v[138:139], 0, s[22:23]
	v_lshl_add_u64 v[36:37], v[140:141], 0, s[22:23]
	v_lshl_add_u64 v[46:47], v[142:143], 0, s[22:23]
	v_lshl_add_u64 v[48:49], v[144:145], 0, s[22:23]
	global_load_dwordx4 v[86:89], v[2:3], off nt
	global_load_dwordx4 v[78:81], v[4:5], off nt
	global_load_dwordx4 v[66:69], v[10:11], off nt
	global_load_dwordx4 v[42:45], v[12:13], off nt
	global_load_dwordx4 v[38:41], v[34:35], off nt
	global_load_dwordx4 v[18:21], v[36:37], off nt
	s_nop 0
	global_load_dwordx4 v[10:13], v[46:47], off nt
	global_load_dwordx4 v[2:5], v[48:49], off nt
	v_mov_b32_e32 v34, v196
	s_waitcnt vmcnt(23)
	s_waitcnt vmcnt(22)
	s_waitcnt vmcnt(21)
	s_waitcnt vmcnt(20)
	s_waitcnt vmcnt(19)
	s_waitcnt vmcnt(18)
	s_waitcnt vmcnt(17)
	s_waitcnt vmcnt(16)
	ds_read_b32 v34, v187 offset:192
	s_waitcnt lgkmcnt(0)
	v_pk_fma_f32 v[36:37], v[34:35], v[118:119], 0 op_sel_hi:[0,1,0] neg_lo:[1,0,0] neg_hi:[1,0,0]
	v_pk_fma_f32 v[34:35], v[34:35], v[120:121], 0 op_sel_hi:[0,1,0] neg_lo:[1,0,0] neg_hi:[1,0,0]
	v_cvt_pk_bf16_f32 v36, v36, v37
	v_cvt_pk_bf16_f32 v37, v34, v35
	ds_write_b64 v186, v[36:37]
	ds_read_b32 v34, v187 offset:200
	s_waitcnt lgkmcnt(0)
	v_pk_fma_f32 v[36:37], v[34:35], v[110:111], 0 op_sel_hi:[0,1,0] neg_lo:[1,0,0] neg_hi:[1,0,0]
	v_pk_fma_f32 v[34:35], v[34:35], v[112:113], 0 op_sel_hi:[0,1,0] neg_lo:[1,0,0] neg_hi:[1,0,0]
	v_cvt_pk_bf16_f32 v36, v36, v37
	v_cvt_pk_bf16_f32 v37, v34, v35
	ds_write_b64 v186, v[36:37] offset:544
	ds_read_b32 v34, v187 offset:208
	s_waitcnt lgkmcnt(0)
	v_pk_fma_f32 v[36:37], v[34:35], v[102:103], 0 op_sel_hi:[0,1,0] neg_lo:[1,0,0] neg_hi:[1,0,0]
	v_pk_fma_f32 v[34:35], v[34:35], v[104:105], 0 op_sel_hi:[0,1,0] neg_lo:[1,0,0] neg_hi:[1,0,0]
	v_cvt_pk_bf16_f32 v36, v36, v37
	v_cvt_pk_bf16_f32 v37, v34, v35
	ds_write_b64 v186, v[36:37] offset:1088
	ds_read_b32 v34, v187 offset:216
	s_waitcnt lgkmcnt(0)
	v_pk_fma_f32 v[36:37], v[34:35], v[98:99], 0 op_sel_hi:[0,1,0] neg_lo:[1,0,0] neg_hi:[1,0,0]
	v_pk_fma_f32 v[34:35], v[34:35], v[100:101], 0 op_sel_hi:[0,1,0] neg_lo:[1,0,0] neg_hi:[1,0,0]
	v_cvt_pk_bf16_f32 v36, v36, v37
	v_cvt_pk_bf16_f32 v37, v34, v35
	ds_write_b64 v186, v[36:37] offset:1632
	ds_read_b32 v34, v187 offset:224
	s_waitcnt lgkmcnt(0)
	v_pk_fma_f32 v[36:37], v[34:35], v[58:59], 0 op_sel_hi:[0,1,0] neg_lo:[1,0,0] neg_hi:[1,0,0]
	v_pk_fma_f32 v[34:35], v[34:35], v[60:61], 0 op_sel_hi:[0,1,0] neg_lo:[1,0,0] neg_hi:[1,0,0]
	v_cvt_pk_bf16_f32 v36, v36, v37
	v_cvt_pk_bf16_f32 v37, v34, v35
	ds_write_b64 v186, v[36:37] offset:2176
	ds_read_b32 v34, v187 offset:232
	s_waitcnt lgkmcnt(0)
	v_pk_fma_f32 v[36:37], v[34:35], v[50:51], 0 op_sel_hi:[0,1,0] neg_lo:[1,0,0] neg_hi:[1,0,0]
	v_pk_fma_f32 v[34:35], v[34:35], v[52:53], 0 op_sel_hi:[0,1,0] neg_lo:[1,0,0] neg_hi:[1,0,0]
	v_cvt_pk_bf16_f32 v36, v36, v37
	v_cvt_pk_bf16_f32 v37, v34, v35
	ds_write_b64 v186, v[36:37] offset:2720
	ds_read_b32 v34, v187 offset:240
	s_waitcnt lgkmcnt(0)
	v_pk_fma_f32 v[30:31], v[34:35], v[30:31], 0 op_sel_hi:[0,1,0] neg_lo:[1,0,0] neg_hi:[1,0,0]
	v_pk_fma_f32 v[32:33], v[34:35], v[32:33], 0 op_sel_hi:[0,1,0] neg_lo:[1,0,0] neg_hi:[1,0,0]
	v_cvt_pk_bf16_f32 v30, v30, v31
	v_cvt_pk_bf16_f32 v31, v32, v33
	ds_write_b64 v186, v[30:31] offset:3264
	ds_read_b32 v30, v187 offset:248
	s_waitcnt lgkmcnt(0)
	v_pk_fma_f32 v[22:23], v[30:31], v[22:23], 0 op_sel_hi:[0,1,0] neg_lo:[1,0,0] neg_hi:[1,0,0]
	v_pk_fma_f32 v[24:25], v[30:31], v[24:25], 0 op_sel_hi:[0,1,0] neg_lo:[1,0,0] neg_hi:[1,0,0]
	v_cvt_pk_bf16_f32 v22, v22, v23
	v_cvt_pk_bf16_f32 v23, v24, v25
	ds_write_b64 v186, v[22:23] offset:3808
	ds_read_b128 v[22:25], v1
	s_waitcnt lgkmcnt(0)
	ds_write_b128 v184, v[22:25] offset:20480
	ds_read_b128 v[22:25], v1 offset:64
	s_waitcnt lgkmcnt(0)
	ds_write_b128 v184, v[22:25] offset:21504
	ds_read_b128 v[22:25], v1 offset:128
	s_waitcnt lgkmcnt(0)
	ds_write_b128 v184, v[22:25] offset:22528
	ds_read_b128 v[22:25], v1 offset:192
	s_waitcnt lgkmcnt(0)
	ds_write_b128 v184, v[22:25] offset:23552
	v_lshl_add_u64 v[22:23], v[130:131], 0, s[30:31]
	s_movk_i32 s7, 0x2000
	v_add_co_u32_e32 v24, vcc, s7, v22
	s_movk_i32 s36, 0x4000
	s_nop 0
	v_addc_co_u32_e32 v25, vcc, 0, v23, vcc
	global_load_dwordx4 v[74:77], v[22:23], off nt
	global_load_dwordx4 v[62:65], v[24:25], off nt
	v_add_co_u32_e32 v24, vcc, s36, v22
	s_movk_i32 s37, 0x6000
	s_nop 0
	v_addc_co_u32_e32 v25, vcc, 0, v23, vcc
	v_add_co_u32_e32 v30, vcc, s37, v22
	s_mov_b32 s38, 0x8000
	s_nop 0
	v_addc_co_u32_e32 v31, vcc, 0, v23, vcc
	global_load_dwordx4 v[58:61], v[24:25], off nt
	global_load_dwordx4 v[46:49], v[30:31], off nt
	v_add_co_u32_e32 v24, vcc, s38, v22
	s_mov_b32 s39, 0xa000
	s_nop 0
	v_addc_co_u32_e32 v25, vcc, 0, v23, vcc
	v_add_co_u32_e32 v34, vcc, s39, v22
	s_mov_b32 s41, 0xc000
	s_nop 0
	v_addc_co_u32_e32 v35, vcc, 0, v23, vcc
	global_load_dwordx4 v[50:53], v[24:25], off nt
	global_load_dwordx4 v[30:33], v[34:35], off nt
	v_add_co_u32_e32 v24, vcc, s41, v22
	s_mov_b32 s42, 0xe000
	s_nop 0
	v_addc_co_u32_e32 v25, vcc, 0, v23, vcc
	v_add_co_u32_e32 v22, vcc, s42, v22
	s_nop 1
	v_addc_co_u32_e32 v23, vcc, 0, v23, vcc
	global_load_dwordx4 v[34:37], v[24:25], off nt
	s_nop 0
	global_load_dwordx4 v[22:25], v[22:23], off nt
	v_mov_b32_e32 v98, v195
	s_waitcnt vmcnt(23)
	s_waitcnt vmcnt(22)
	s_waitcnt vmcnt(21)
	s_waitcnt vmcnt(20)
	s_waitcnt vmcnt(19)
	s_waitcnt vmcnt(18)
	s_waitcnt vmcnt(17)
	s_waitcnt vmcnt(16)
	ds_read_b32 v98, v187 offset:192
	s_waitcnt lgkmcnt(0)
	v_pk_fma_f32 v[94:95], v[98:99], v[94:95], 0 op_sel_hi:[0,1,0] neg_lo:[1,0,0] neg_hi:[1,0,0]
	v_pk_fma_f32 v[96:97], v[98:99], v[96:97], 0 op_sel_hi:[0,1,0] neg_lo:[1,0,0] neg_hi:[1,0,0]
	v_cvt_pk_bf16_f32 v94, v94, v95
	v_cvt_pk_bf16_f32 v95, v96, v97
	ds_write_b64 v186, v[94:95]
	ds_read_b32 v94, v187 offset:200
	s_waitcnt lgkmcnt(0)
	v_pk_fma_f32 v[90:91], v[94:95], v[90:91], 0 op_sel_hi:[0,1,0] neg_lo:[1,0,0] neg_hi:[1,0,0]
	v_pk_fma_f32 v[92:93], v[94:95], v[92:93], 0 op_sel_hi:[0,1,0] neg_lo:[1,0,0] neg_hi:[1,0,0]
	v_cvt_pk_bf16_f32 v90, v90, v91
	v_cvt_pk_bf16_f32 v91, v92, v93
	ds_write_b64 v186, v[90:91] offset:544
	ds_read_b32 v90, v187 offset:208
	s_waitcnt lgkmcnt(0)
	v_pk_fma_f32 v[82:83], v[90:91], v[82:83], 0 op_sel_hi:[0,1,0] neg_lo:[1,0,0] neg_hi:[1,0,0]
	v_pk_fma_f32 v[84:85], v[90:91], v[84:85], 0 op_sel_hi:[0,1,0] neg_lo:[1,0,0] neg_hi:[1,0,0]
	v_cvt_pk_bf16_f32 v82, v82, v83
	v_cvt_pk_bf16_f32 v83, v84, v85
	ds_write_b64 v186, v[82:83] offset:1088
	ds_read_b32 v82, v187 offset:216
	s_waitcnt lgkmcnt(0)
	v_pk_fma_f32 v[70:71], v[82:83], v[70:71], 0 op_sel_hi:[0,1,0] neg_lo:[1,0,0] neg_hi:[1,0,0]
	v_pk_fma_f32 v[72:73], v[82:83], v[72:73], 0 op_sel_hi:[0,1,0] neg_lo:[1,0,0] neg_hi:[1,0,0]
	v_cvt_pk_bf16_f32 v70, v70, v71
	v_cvt_pk_bf16_f32 v71, v72, v73
	ds_write_b64 v186, v[70:71] offset:1632
	ds_read_b32 v70, v187 offset:224
	s_waitcnt lgkmcnt(0)
	v_pk_fma_f32 v[54:55], v[70:71], v[54:55], 0 op_sel_hi:[0,1,0] neg_lo:[1,0,0] neg_hi:[1,0,0]
	v_pk_fma_f32 v[56:57], v[70:71], v[56:57], 0 op_sel_hi:[0,1,0] neg_lo:[1,0,0] neg_hi:[1,0,0]
	v_cvt_pk_bf16_f32 v54, v54, v55
	v_cvt_pk_bf16_f32 v55, v56, v57
	ds_write_b64 v186, v[54:55] offset:2176
	ds_read_b32 v54, v187 offset:232
	s_waitcnt lgkmcnt(0)
	v_pk_fma_f32 v[26:27], v[54:55], v[26:27], 0 op_sel_hi:[0,1,0] neg_lo:[1,0,0] neg_hi:[1,0,0]
	v_pk_fma_f32 v[28:29], v[54:55], v[28:29], 0 op_sel_hi:[0,1,0] neg_lo:[1,0,0] neg_hi:[1,0,0]
	v_cvt_pk_bf16_f32 v26, v26, v27
	v_cvt_pk_bf16_f32 v27, v28, v29
	ds_write_b64 v186, v[26:27] offset:2720
	ds_read_b32 v26, v187 offset:240
	s_waitcnt lgkmcnt(0)
	v_pk_fma_f32 v[14:15], v[26:27], v[14:15], 0 op_sel_hi:[0,1,0] neg_lo:[1,0,0] neg_hi:[1,0,0]
	v_pk_fma_f32 v[16:17], v[26:27], v[16:17], 0 op_sel_hi:[0,1,0] neg_lo:[1,0,0] neg_hi:[1,0,0]
	v_cvt_pk_bf16_f32 v14, v14, v15
	v_cvt_pk_bf16_f32 v15, v16, v17
	ds_write_b64 v186, v[14:15] offset:3264
	ds_read_b32 v14, v187 offset:248
	s_waitcnt lgkmcnt(0)
	v_pk_fma_f32 v[6:7], v[14:15], v[6:7], 0 op_sel_hi:[0,1,0] neg_lo:[1,0,0] neg_hi:[1,0,0]
	v_pk_fma_f32 v[8:9], v[14:15], v[8:9], 0 op_sel_hi:[0,1,0] neg_lo:[1,0,0] neg_hi:[1,0,0]
	v_cvt_pk_bf16_f32 v6, v6, v7
	v_cvt_pk_bf16_f32 v7, v8, v9
	ds_write_b64 v186, v[6:7] offset:3808
	ds_read_b128 v[6:9], v1
	s_waitcnt lgkmcnt(0)
	ds_write_b128 v184, v[6:9] offset:24576
	ds_read_b128 v[6:9], v1 offset:64
	s_waitcnt lgkmcnt(0)
	ds_write_b128 v184, v[6:9] offset:25600
	ds_read_b128 v[6:9], v1 offset:128
	s_waitcnt lgkmcnt(0)
	ds_write_b128 v184, v[6:9] offset:26624
	ds_read_b128 v[6:9], v1 offset:192
	s_waitcnt lgkmcnt(0)
	ds_write_b128 v184, v[6:9] offset:27648
	s_mov_b64 s[44:45], 0x10000
	v_lshl_add_u64 v[150:151], v[130:131], 0, s[44:45]
	s_mov_b64 s[44:45], 0x12000
	v_lshl_add_u64 v[152:153], v[130:131], 0, s[44:45]
	s_mov_b64 s[44:45], 0x14000
	v_lshl_add_u64 v[156:157], v[130:131], 0, s[44:45]
	s_mov_b64 s[44:45], 0x16000
	v_lshl_add_u64 v[158:159], v[130:131], 0, s[44:45]
	s_mov_b64 s[44:45], 0x18000
	v_lshl_add_u64 v[160:161], v[130:131], 0, s[44:45]
	s_mov_b64 s[44:45], 0x1a000
	v_lshl_add_u64 v[162:163], v[130:131], 0, s[44:45]
	s_mov_b64 s[44:45], 0x1c000
	v_lshl_add_u64 v[164:165], v[130:131], 0, s[44:45]
	s_mov_b64 s[44:45], 0x1e000
	v_lshl_add_u64 v[6:7], v[150:151], 0, s[30:31]
	v_lshl_add_u64 v[8:9], v[152:153], 0, s[30:31]
	v_lshl_add_u64 v[14:15], v[156:157], 0, s[30:31]
	v_lshl_add_u64 v[16:17], v[158:159], 0, s[30:31]
	v_lshl_add_u64 v[26:27], v[160:161], 0, s[30:31]
	v_lshl_add_u64 v[28:29], v[162:163], 0, s[30:31]
	v_lshl_add_u64 v[166:167], v[130:131], 0, s[44:45]
	v_lshl_add_u64 v[98:99], v[164:165], 0, s[30:31]
	v_lshl_add_u64 v[100:101], v[166:167], 0, s[30:31]
	global_load_dwordx4 v[94:97], v[6:7], off nt
	global_load_dwordx4 v[90:93], v[8:9], off nt
	global_load_dwordx4 v[82:85], v[14:15], off nt
	global_load_dwordx4 v[70:73], v[16:17], off nt
	global_load_dwordx4 v[54:57], v[26:27], off nt
	s_nop 0
	global_load_dwordx4 v[26:29], v[28:29], off nt
	s_nop 0
	global_load_dwordx4 v[14:17], v[98:99], off nt
	global_load_dwordx4 v[6:9], v[100:101], off nt
	v_mov_b32_e32 v98, v194
	s_waitcnt vmcnt(23)
	s_waitcnt vmcnt(22)
	s_waitcnt vmcnt(21)
	s_waitcnt vmcnt(20)
	s_waitcnt vmcnt(19)
	s_waitcnt vmcnt(18)
	s_waitcnt vmcnt(17)
	s_waitcnt vmcnt(16)
	ds_read_b32 v98, v187 offset:192
	s_waitcnt lgkmcnt(0)
	v_pk_fma_f32 v[86:87], v[98:99], v[86:87], 0 op_sel_hi:[0,1,0] neg_lo:[1,0,0] neg_hi:[1,0,0]
	v_pk_fma_f32 v[88:89], v[98:99], v[88:89], 0 op_sel_hi:[0,1,0] neg_lo:[1,0,0] neg_hi:[1,0,0]
	v_cvt_pk_bf16_f32 v86, v86, v87
	v_cvt_pk_bf16_f32 v87, v88, v89
	ds_write_b64 v186, v[86:87]
	ds_read_b32 v86, v187 offset:200
	s_waitcnt lgkmcnt(0)
	v_pk_fma_f32 v[78:79], v[86:87], v[78:79], 0 op_sel_hi:[0,1,0] neg_lo:[1,0,0] neg_hi:[1,0,0]
	v_pk_fma_f32 v[80:81], v[86:87], v[80:81], 0 op_sel_hi:[0,1,0] neg_lo:[1,0,0] neg_hi:[1,0,0]
	v_cvt_pk_bf16_f32 v78, v78, v79
	v_cvt_pk_bf16_f32 v79, v80, v81
	ds_write_b64 v186, v[78:79] offset:544
	ds_read_b32 v78, v187 offset:208
	s_waitcnt lgkmcnt(0)
	v_pk_fma_f32 v[66:67], v[78:79], v[66:67], 0 op_sel_hi:[0,1,0] neg_lo:[1,0,0] neg_hi:[1,0,0]
	v_pk_fma_f32 v[68:69], v[78:79], v[68:69], 0 op_sel_hi:[0,1,0] neg_lo:[1,0,0] neg_hi:[1,0,0]
	v_cvt_pk_bf16_f32 v66, v66, v67
	v_cvt_pk_bf16_f32 v67, v68, v69
	ds_write_b64 v186, v[66:67] offset:1088
	ds_read_b32 v66, v187 offset:216
	s_waitcnt lgkmcnt(0)
	v_pk_fma_f32 v[42:43], v[66:67], v[42:43], 0 op_sel_hi:[0,1,0] neg_lo:[1,0,0] neg_hi:[1,0,0]
	v_pk_fma_f32 v[44:45], v[66:67], v[44:45], 0 op_sel_hi:[0,1,0] neg_lo:[1,0,0] neg_hi:[1,0,0]
	v_cvt_pk_bf16_f32 v42, v42, v43
	v_cvt_pk_bf16_f32 v43, v44, v45
	ds_write_b64 v186, v[42:43] offset:1632
	ds_read_b32 v42, v187 offset:224
	s_waitcnt lgkmcnt(0)
	v_pk_fma_f32 v[38:39], v[42:43], v[38:39], 0 op_sel_hi:[0,1,0] neg_lo:[1,0,0] neg_hi:[1,0,0]
	v_pk_fma_f32 v[40:41], v[42:43], v[40:41], 0 op_sel_hi:[0,1,0] neg_lo:[1,0,0] neg_hi:[1,0,0]
	v_cvt_pk_bf16_f32 v38, v38, v39
	v_cvt_pk_bf16_f32 v39, v40, v41
	ds_write_b64 v186, v[38:39] offset:2176
	ds_read_b32 v38, v187 offset:232
	s_waitcnt lgkmcnt(0)
	v_pk_fma_f32 v[18:19], v[38:39], v[18:19], 0 op_sel_hi:[0,1,0] neg_lo:[1,0,0] neg_hi:[1,0,0]
	v_pk_fma_f32 v[20:21], v[38:39], v[20:21], 0 op_sel_hi:[0,1,0] neg_lo:[1,0,0] neg_hi:[1,0,0]
	v_cvt_pk_bf16_f32 v18, v18, v19
	v_cvt_pk_bf16_f32 v19, v20, v21
	ds_write_b64 v186, v[18:19] offset:2720
	ds_read_b32 v18, v187 offset:240
	s_waitcnt lgkmcnt(0)
	v_pk_fma_f32 v[10:11], v[18:19], v[10:11], 0 op_sel_hi:[0,1,0] neg_lo:[1,0,0] neg_hi:[1,0,0]
	v_pk_fma_f32 v[12:13], v[18:19], v[12:13], 0 op_sel_hi:[0,1,0] neg_lo:[1,0,0] neg_hi:[1,0,0]
	v_cvt_pk_bf16_f32 v10, v10, v11
	v_cvt_pk_bf16_f32 v11, v12, v13
	ds_write_b64 v186, v[10:11] offset:3264
	ds_read_b32 v10, v187 offset:248
	s_waitcnt lgkmcnt(0)
	v_pk_fma_f32 v[2:3], v[10:11], v[2:3], 0 op_sel_hi:[0,1,0] neg_lo:[1,0,0] neg_hi:[1,0,0]
	v_pk_fma_f32 v[4:5], v[10:11], v[4:5], 0 op_sel_hi:[0,1,0] neg_lo:[1,0,0] neg_hi:[1,0,0]
	v_cvt_pk_bf16_f32 v2, v2, v3
	v_cvt_pk_bf16_f32 v3, v4, v5
	ds_write_b64 v186, v[2:3] offset:3808
	ds_read_b128 v[2:5], v1
	s_waitcnt lgkmcnt(0)
	ds_write_b128 v184, v[2:5] offset:28672
	ds_read_b128 v[2:5], v1 offset:64
	s_waitcnt lgkmcnt(0)
	ds_write_b128 v184, v[2:5] offset:29696
	ds_read_b128 v[2:5], v1 offset:128
	s_waitcnt lgkmcnt(0)
	ds_write_b128 v184, v[2:5] offset:30720
	ds_read_b128 v[2:5], v1 offset:192
	s_waitcnt lgkmcnt(0)
	ds_write_b128 v184, v[2:5] offset:31744
	s_mov_b64 s[44:45], 0x20000
	v_lshl_add_u64 v[168:169], v[130:131], 0, s[44:45]
	s_mov_b64 s[44:45], 0x22000
	v_lshl_add_u64 v[170:171], v[130:131], 0, s[44:45]
	s_mov_b64 s[44:45], 0x24000
	v_lshl_add_u64 v[172:173], v[130:131], 0, s[44:45]
	s_mov_b64 s[44:45], 0x26000
	v_lshl_add_u64 v[174:175], v[130:131], 0, s[44:45]
	s_mov_b64 s[44:45], 0x28000
	v_lshl_add_u64 v[176:177], v[130:131], 0, s[44:45]
	s_mov_b64 s[44:45], 0x2a000
	v_lshl_add_u64 v[178:179], v[130:131], 0, s[44:45]
	s_mov_b64 s[44:45], 0x2c000
	v_lshl_add_u64 v[180:181], v[130:131], 0, s[44:45]
	s_mov_b64 s[44:45], 0x2e000
	v_lshl_add_u64 v[2:3], v[168:169], 0, s[30:31]
	v_lshl_add_u64 v[4:5], v[170:171], 0, s[30:31]
	v_lshl_add_u64 v[10:11], v[172:173], 0, s[30:31]
	v_lshl_add_u64 v[12:13], v[174:175], 0, s[30:31]
	v_lshl_add_u64 v[18:19], v[176:177], 0, s[30:31]
	v_lshl_add_u64 v[20:21], v[178:179], 0, s[30:31]
	v_lshl_add_u64 v[182:183], v[130:131], 0, s[44:45]
	v_lshl_add_u64 v[42:43], v[180:181], 0, s[30:31]
	v_lshl_add_u64 v[44:45], v[182:183], 0, s[30:31]
	global_load_dwordx4 v[106:109], v[2:3], off nt
	global_load_dwordx4 v[98:101], v[4:5], off nt
	global_load_dwordx4 v[78:81], v[10:11], off nt
	global_load_dwordx4 v[66:69], v[12:13], off nt
	global_load_dwordx4 v[38:41], v[18:19], off nt
	s_nop 0
	global_load_dwordx4 v[18:21], v[20:21], off nt
	s_nop 0
	global_load_dwordx4 v[10:13], v[42:43], off nt
	global_load_dwordx4 v[2:5], v[44:45], off nt
	v_mov_b32_e32 v42, v198
	s_waitcnt vmcnt(23)
	s_waitcnt vmcnt(22)
	s_waitcnt vmcnt(21)
	s_waitcnt vmcnt(20)
	s_waitcnt vmcnt(19)
	s_waitcnt vmcnt(18)
	s_waitcnt vmcnt(17)
	s_waitcnt vmcnt(16)
	ds_read_b32 v42, v187
	s_waitcnt lgkmcnt(0)
	v_pk_fma_f32 v[44:45], v[42:43], v[74:75], 0 op_sel_hi:[0,1,0] neg_lo:[1,0,0] neg_hi:[1,0,0]
	v_pk_fma_f32 v[42:43], v[42:43], v[76:77], 0 op_sel_hi:[0,1,0] neg_lo:[1,0,0] neg_hi:[1,0,0]
	v_cvt_pk_bf16_f32 v44, v44, v45
	v_cvt_pk_bf16_f32 v45, v42, v43
	ds_write_b64 v186, v[44:45]
	ds_read_b32 v42, v187 offset:8
	s_waitcnt lgkmcnt(0)
	v_pk_fma_f32 v[44:45], v[42:43], v[62:63], 0 op_sel_hi:[0,1,0] neg_lo:[1,0,0] neg_hi:[1,0,0]
	v_pk_fma_f32 v[42:43], v[42:43], v[64:65], 0 op_sel_hi:[0,1,0] neg_lo:[1,0,0] neg_hi:[1,0,0]
	v_cvt_pk_bf16_f32 v44, v44, v45
	v_cvt_pk_bf16_f32 v45, v42, v43
	ds_write_b64 v186, v[44:45] offset:544
	ds_read_b32 v42, v187 offset:16
	s_waitcnt lgkmcnt(0)
	v_pk_fma_f32 v[44:45], v[42:43], v[58:59], 0 op_sel_hi:[0,1,0] neg_lo:[1,0,0] neg_hi:[1,0,0]
	v_pk_fma_f32 v[42:43], v[42:43], v[60:61], 0 op_sel_hi:[0,1,0] neg_lo:[1,0,0] neg_hi:[1,0,0]
	v_cvt_pk_bf16_f32 v44, v44, v45
	v_cvt_pk_bf16_f32 v45, v42, v43
	ds_write_b64 v186, v[44:45] offset:1088
	ds_read_b32 v42, v187 offset:24
	s_waitcnt lgkmcnt(0)
	v_pk_fma_f32 v[44:45], v[42:43], v[46:47], 0 op_sel_hi:[0,1,0] neg_lo:[1,0,0] neg_hi:[1,0,0]
	v_pk_fma_f32 v[42:43], v[42:43], v[48:49], 0 op_sel_hi:[0,1,0] neg_lo:[1,0,0] neg_hi:[1,0,0]
	v_cvt_pk_bf16_f32 v44, v44, v45
	v_cvt_pk_bf16_f32 v45, v42, v43
	ds_write_b64 v186, v[44:45] offset:1632
	ds_read_b32 v42, v187 offset:32
	s_waitcnt lgkmcnt(0)
	v_pk_fma_f32 v[44:45], v[42:43], v[50:51], 0 op_sel_hi:[0,1,0] neg_lo:[1,0,0] neg_hi:[1,0,0]
	v_pk_fma_f32 v[42:43], v[42:43], v[52:53], 0 op_sel_hi:[0,1,0] neg_lo:[1,0,0] neg_hi:[1,0,0]
	v_cvt_pk_bf16_f32 v44, v44, v45
	v_cvt_pk_bf16_f32 v45, v42, v43
	ds_write_b64 v186, v[44:45] offset:2176
	ds_read_b32 v42, v187 offset:40
	s_waitcnt lgkmcnt(0)
	v_pk_fma_f32 v[30:31], v[42:43], v[30:31], 0 op_sel_hi:[0,1,0] neg_lo:[1,0,0] neg_hi:[1,0,0]
	v_pk_fma_f32 v[32:33], v[42:43], v[32:33], 0 op_sel_hi:[0,1,0] neg_lo:[1,0,0] neg_hi:[1,0,0]
	v_cvt_pk_bf16_f32 v30, v30, v31
	v_cvt_pk_bf16_f32 v31, v32, v33
	ds_write_b64 v186, v[30:31] offset:2720
	ds_read_b32 v30, v187 offset:48
	s_waitcnt lgkmcnt(0)
	v_pk_fma_f32 v[32:33], v[30:31], v[34:35], 0 op_sel_hi:[0,1,0] neg_lo:[1,0,0] neg_hi:[1,0,0]
	v_pk_fma_f32 v[30:31], v[30:31], v[36:37], 0 op_sel_hi:[0,1,0] neg_lo:[1,0,0] neg_hi:[1,0,0]
	v_cvt_pk_bf16_f32 v32, v32, v33
	v_cvt_pk_bf16_f32 v33, v30, v31
	ds_write_b64 v186, v[32:33] offset:3264
	ds_read_b32 v30, v187 offset:56
	s_waitcnt lgkmcnt(0)
	v_pk_fma_f32 v[22:23], v[30:31], v[22:23], 0 op_sel_hi:[0,1,0] neg_lo:[1,0,0] neg_hi:[1,0,0]
	v_pk_fma_f32 v[24:25], v[30:31], v[24:25], 0 op_sel_hi:[0,1,0] neg_lo:[1,0,0] neg_hi:[1,0,0]
	v_cvt_pk_bf16_f32 v22, v22, v23
	v_cvt_pk_bf16_f32 v23, v24, v25
	ds_write_b64 v186, v[22:23] offset:3808
	ds_read_b128 a[0:3], v1
	ds_read_b128 a[4:7], v1 offset:64
	ds_read_b128 a[8:11], v1 offset:128
	ds_read_b128 a[12:15], v1 offset:192
	v_lshl_add_u64 v[22:23], v[130:131], 0, s[28:29]
	v_add_co_u32_e32 v24, vcc, s7, v22
	s_nop 1
	v_addc_co_u32_e32 v25, vcc, 0, v23, vcc
	global_load_dwordx4 v[102:105], v[22:23], off nt
	global_load_dwordx4 v[86:89], v[24:25], off nt
	v_add_co_u32_e32 v24, vcc, s36, v22
	s_nop 1
	v_addc_co_u32_e32 v25, vcc, 0, v23, vcc
	v_add_co_u32_e32 v30, vcc, s37, v22
	s_nop 1
	v_addc_co_u32_e32 v31, vcc, 0, v23, vcc
	global_load_dwordx4 v[74:77], v[24:25], off nt
	global_load_dwordx4 v[62:65], v[30:31], off nt
	v_add_co_u32_e32 v24, vcc, s38, v22
	s_nop 1
	v_addc_co_u32_e32 v25, vcc, 0, v23, vcc
	v_add_co_u32_e32 v30, vcc, s39, v22
	s_nop 1
	v_addc_co_u32_e32 v31, vcc, 0, v23, vcc
	global_load_dwordx4 v[58:61], v[24:25], off nt
	global_load_dwordx4 v[46:49], v[30:31], off nt
	v_add_co_u32_e32 v24, vcc, s41, v22
	s_nop 1
	v_addc_co_u32_e32 v25, vcc, 0, v23, vcc
	v_add_co_u32_e32 v22, vcc, s42, v22
	s_nop 1
	v_addc_co_u32_e32 v23, vcc, 0, v23, vcc
	global_load_dwordx4 v[42:45], v[24:25], off nt
	global_load_dwordx4 v[30:33], v[22:23], off nt
	v_mov_b32_e32 v22, v198
	s_waitcnt vmcnt(23)
	s_waitcnt vmcnt(22)
	s_waitcnt vmcnt(21)
	s_waitcnt vmcnt(20)
	s_waitcnt vmcnt(19)
	s_waitcnt vmcnt(18)
	s_waitcnt vmcnt(17)
	s_waitcnt vmcnt(16)
	ds_read_b32 v22, v187 offset:64
	s_waitcnt lgkmcnt(0)
	v_pk_fma_f32 v[24:25], v[22:23], v[94:95], 0 op_sel_hi:[0,1,0] neg_lo:[1,0,0] neg_hi:[1,0,0]
	v_pk_fma_f32 v[22:23], v[22:23], v[96:97], 0 op_sel_hi:[0,1,0] neg_lo:[1,0,0] neg_hi:[1,0,0]
	v_cvt_pk_bf16_f32 v24, v24, v25
	v_cvt_pk_bf16_f32 v25, v22, v23
	ds_write_b64 v186, v[24:25]
	ds_read_b32 v22, v187 offset:72
	s_waitcnt lgkmcnt(0)
	v_pk_fma_f32 v[24:25], v[22:23], v[90:91], 0 op_sel_hi:[0,1,0] neg_lo:[1,0,0] neg_hi:[1,0,0]
	v_pk_fma_f32 v[22:23], v[22:23], v[92:93], 0 op_sel_hi:[0,1,0] neg_lo:[1,0,0] neg_hi:[1,0,0]
	v_cvt_pk_bf16_f32 v24, v24, v25
	v_cvt_pk_bf16_f32 v25, v22, v23
	ds_write_b64 v186, v[24:25] offset:544
	ds_read_b32 v22, v187 offset:80
	s_waitcnt lgkmcnt(0)
	v_pk_fma_f32 v[24:25], v[22:23], v[82:83], 0 op_sel_hi:[0,1,0] neg_lo:[1,0,0] neg_hi:[1,0,0]
	v_pk_fma_f32 v[22:23], v[22:23], v[84:85], 0 op_sel_hi:[0,1,0] neg_lo:[1,0,0] neg_hi:[1,0,0]
	v_cvt_pk_bf16_f32 v24, v24, v25
	v_cvt_pk_bf16_f32 v25, v22, v23
	ds_write_b64 v186, v[24:25] offset:1088
	ds_read_b32 v22, v187 offset:88
	s_waitcnt lgkmcnt(0)
	v_pk_fma_f32 v[24:25], v[22:23], v[70:71], 0 op_sel_hi:[0,1,0] neg_lo:[1,0,0] neg_hi:[1,0,0]
	v_pk_fma_f32 v[22:23], v[22:23], v[72:73], 0 op_sel_hi:[0,1,0] neg_lo:[1,0,0] neg_hi:[1,0,0]
	v_cvt_pk_bf16_f32 v24, v24, v25
	v_cvt_pk_bf16_f32 v25, v22, v23
	ds_write_b64 v186, v[24:25] offset:1632
	ds_read_b32 v22, v187 offset:96
	s_waitcnt lgkmcnt(0)
	v_pk_fma_f32 v[24:25], v[22:23], v[54:55], 0 op_sel_hi:[0,1,0] neg_lo:[1,0,0] neg_hi:[1,0,0]
	v_pk_fma_f32 v[22:23], v[22:23], v[56:57], 0 op_sel_hi:[0,1,0] neg_lo:[1,0,0] neg_hi:[1,0,0]
	v_cvt_pk_bf16_f32 v24, v24, v25
	v_cvt_pk_bf16_f32 v25, v22, v23
	ds_write_b64 v186, v[24:25] offset:2176
	ds_read_b32 v22, v187 offset:104
	s_waitcnt lgkmcnt(0)
	v_pk_fma_f32 v[24:25], v[22:23], v[26:27], 0 op_sel_hi:[0,1,0] neg_lo:[1,0,0] neg_hi:[1,0,0]
	v_pk_fma_f32 v[22:23], v[22:23], v[28:29], 0 op_sel_hi:[0,1,0] neg_lo:[1,0,0] neg_hi:[1,0,0]
	v_cvt_pk_bf16_f32 v24, v24, v25
	v_cvt_pk_bf16_f32 v25, v22, v23
	ds_write_b64 v186, v[24:25] offset:2720
	ds_read_b32 v22, v187 offset:112
	s_waitcnt lgkmcnt(0)
	v_pk_fma_f32 v[14:15], v[22:23], v[14:15], 0 op_sel_hi:[0,1,0] neg_lo:[1,0,0] neg_hi:[1,0,0]
	v_pk_fma_f32 v[16:17], v[22:23], v[16:17], 0 op_sel_hi:[0,1,0] neg_lo:[1,0,0] neg_hi:[1,0,0]
	v_cvt_pk_bf16_f32 v14, v14, v15
	v_cvt_pk_bf16_f32 v15, v16, v17
	ds_write_b64 v186, v[14:15] offset:3264
	ds_read_b32 v14, v187 offset:120
	s_waitcnt lgkmcnt(0)
	v_pk_fma_f32 v[6:7], v[14:15], v[6:7], 0 op_sel_hi:[0,1,0] neg_lo:[1,0,0] neg_hi:[1,0,0]
	v_pk_fma_f32 v[8:9], v[14:15], v[8:9], 0 op_sel_hi:[0,1,0] neg_lo:[1,0,0] neg_hi:[1,0,0]
	v_cvt_pk_bf16_f32 v6, v6, v7
	v_cvt_pk_bf16_f32 v7, v8, v9
	ds_write_b64 v186, v[6:7] offset:3808
	ds_read_b128 a[16:19], v1
	ds_read_b128 a[20:23], v1 offset:64
	ds_read_b128 a[24:27], v1 offset:128
	ds_read_b128 a[28:31], v1 offset:192
	v_lshl_add_u64 v[6:7], v[150:151], 0, s[28:29]
	v_lshl_add_u64 v[8:9], v[152:153], 0, s[28:29]
	v_lshl_add_u64 v[14:15], v[156:157], 0, s[28:29]
	v_lshl_add_u64 v[16:17], v[158:159], 0, s[28:29]
	v_lshl_add_u64 v[22:23], v[160:161], 0, s[28:29]
	v_lshl_add_u64 v[24:25], v[162:163], 0, s[28:29]
	v_lshl_add_u64 v[26:27], v[164:165], 0, s[28:29]
	v_lshl_add_u64 v[28:29], v[166:167], 0, s[28:29]
	global_load_dwordx4 v[110:113], v[6:7], off nt
	global_load_dwordx4 v[90:93], v[8:9], off nt
	global_load_dwordx4 v[70:73], v[14:15], off nt
	global_load_dwordx4 v[50:53], v[16:17], off nt
	global_load_dwordx4 v[34:37], v[22:23], off nt
	s_nop 0
	global_load_dwordx4 v[22:25], v[24:25], off nt
	s_nop 0
	global_load_dwordx4 v[14:17], v[26:27], off nt
	global_load_dwordx4 v[6:9], v[28:29], off nt
	s_waitcnt vmcnt(23)
	s_waitcnt vmcnt(22)
	s_waitcnt vmcnt(21)
	s_waitcnt vmcnt(20)
	s_waitcnt vmcnt(19)
	s_waitcnt vmcnt(18)
	s_waitcnt vmcnt(17)
	s_waitcnt vmcnt(16)
	ds_read_b32 v26, v187 offset:128
	s_waitcnt lgkmcnt(0)
	v_pk_fma_f32 v[28:29], v[26:27], v[106:107], 0 op_sel_hi:[0,1,0] neg_lo:[1,0,0] neg_hi:[1,0,0]
	v_pk_fma_f32 v[26:27], v[26:27], v[108:109], 0 op_sel_hi:[0,1,0] neg_lo:[1,0,0] neg_hi:[1,0,0]
	v_cvt_pk_bf16_f32 v28, v28, v29
	v_cvt_pk_bf16_f32 v29, v26, v27
	ds_write_b64 v186, v[28:29]
	ds_read_b32 v26, v187 offset:136
	s_waitcnt lgkmcnt(0)
	v_pk_fma_f32 v[28:29], v[26:27], v[98:99], 0 op_sel_hi:[0,1,0] neg_lo:[1,0,0] neg_hi:[1,0,0]
	v_pk_fma_f32 v[26:27], v[26:27], v[100:101], 0 op_sel_hi:[0,1,0] neg_lo:[1,0,0] neg_hi:[1,0,0]
	v_cvt_pk_bf16_f32 v28, v28, v29
	v_cvt_pk_bf16_f32 v29, v26, v27
	ds_write_b64 v186, v[28:29] offset:544
	ds_read_b32 v26, v187 offset:144
	s_waitcnt lgkmcnt(0)
	v_pk_fma_f32 v[28:29], v[26:27], v[78:79], 0 op_sel_hi:[0,1,0] neg_lo:[1,0,0] neg_hi:[1,0,0]
	v_pk_fma_f32 v[26:27], v[26:27], v[80:81], 0 op_sel_hi:[0,1,0] neg_lo:[1,0,0] neg_hi:[1,0,0]
	v_cvt_pk_bf16_f32 v28, v28, v29
	v_cvt_pk_bf16_f32 v29, v26, v27
	ds_write_b64 v186, v[28:29] offset:1088
	ds_read_b32 v26, v187 offset:152
	s_waitcnt lgkmcnt(0)
	v_pk_fma_f32 v[28:29], v[26:27], v[66:67], 0 op_sel_hi:[0,1,0] neg_lo:[1,0,0] neg_hi:[1,0,0]
	v_pk_fma_f32 v[26:27], v[26:27], v[68:69], 0 op_sel_hi:[0,1,0] neg_lo:[1,0,0] neg_hi:[1,0,0]
	v_cvt_pk_bf16_f32 v28, v28, v29
	v_cvt_pk_bf16_f32 v29, v26, v27
	ds_write_b64 v186, v[28:29] offset:1632
	ds_read_b32 v26, v187 offset:160
	s_waitcnt lgkmcnt(0)
	v_pk_fma_f32 v[28:29], v[26:27], v[38:39], 0 op_sel_hi:[0,1,0] neg_lo:[1,0,0] neg_hi:[1,0,0]
	v_pk_fma_f32 v[26:27], v[26:27], v[40:41], 0 op_sel_hi:[0,1,0] neg_lo:[1,0,0] neg_hi:[1,0,0]
	v_cvt_pk_bf16_f32 v28, v28, v29
	v_cvt_pk_bf16_f32 v29, v26, v27
	ds_write_b64 v186, v[28:29] offset:2176
	ds_read_b32 v26, v187 offset:168
	s_waitcnt lgkmcnt(0)
	v_pk_fma_f32 v[18:19], v[26:27], v[18:19], 0 op_sel_hi:[0,1,0] neg_lo:[1,0,0] neg_hi:[1,0,0]
	v_pk_fma_f32 v[20:21], v[26:27], v[20:21], 0 op_sel_hi:[0,1,0] neg_lo:[1,0,0] neg_hi:[1,0,0]
	v_cvt_pk_bf16_f32 v18, v18, v19
	v_cvt_pk_bf16_f32 v19, v20, v21
	ds_write_b64 v186, v[18:19] offset:2720
	ds_read_b32 v18, v187 offset:176
	s_waitcnt lgkmcnt(0)
	v_pk_fma_f32 v[10:11], v[18:19], v[10:11], 0 op_sel_hi:[0,1,0] neg_lo:[1,0,0] neg_hi:[1,0,0]
	v_pk_fma_f32 v[12:13], v[18:19], v[12:13], 0 op_sel_hi:[0,1,0] neg_lo:[1,0,0] neg_hi:[1,0,0]
	v_cvt_pk_bf16_f32 v10, v10, v11
	v_cvt_pk_bf16_f32 v11, v12, v13
	ds_write_b64 v186, v[10:11] offset:3264
	ds_read_b32 v10, v187 offset:184
	s_waitcnt lgkmcnt(0)
	v_pk_fma_f32 v[2:3], v[10:11], v[2:3], 0 op_sel_hi:[0,1,0] neg_lo:[1,0,0] neg_hi:[1,0,0]
	v_pk_fma_f32 v[4:5], v[10:11], v[4:5], 0 op_sel_hi:[0,1,0] neg_lo:[1,0,0] neg_hi:[1,0,0]
	v_cvt_pk_bf16_f32 v2, v2, v3
	v_cvt_pk_bf16_f32 v3, v4, v5
	ds_write_b64 v186, v[2:3] offset:3808
	ds_read_b128 a[32:35], v1
	ds_read_b128 a[36:39], v1 offset:64
	ds_read_b128 a[40:43], v1 offset:128
	ds_read_b128 a[44:47], v1 offset:192
	v_lshl_add_u64 v[2:3], v[168:169], 0, s[28:29]
	v_lshl_add_u64 v[4:5], v[170:171], 0, s[28:29]
	v_lshl_add_u64 v[10:11], v[172:173], 0, s[28:29]
	v_lshl_add_u64 v[12:13], v[174:175], 0, s[28:29]
	v_lshl_add_u64 v[18:19], v[176:177], 0, s[28:29]
	v_lshl_add_u64 v[20:21], v[178:179], 0, s[28:29]
	v_lshl_add_u64 v[26:27], v[180:181], 0, s[28:29]
	v_lshl_add_u64 v[28:29], v[182:183], 0, s[28:29]
	global_load_dwordx4 v[106:109], v[2:3], off nt
	global_load_dwordx4 v[94:97], v[4:5], off nt
	global_load_dwordx4 v[66:69], v[10:11], off nt
	global_load_dwordx4 v[54:57], v[12:13], off nt
	global_load_dwordx4 v[38:41], v[18:19], off nt
	s_nop 0
	global_load_dwordx4 v[18:21], v[20:21], off nt
	s_nop 0
	global_load_dwordx4 v[10:13], v[26:27], off nt
	global_load_dwordx4 v[2:5], v[28:29], off nt
	v_mov_b32_e32 v26, v197
	s_waitcnt vmcnt(23)
	s_waitcnt vmcnt(22)
	s_waitcnt vmcnt(21)
	s_waitcnt vmcnt(20)
	s_waitcnt vmcnt(19)
	s_waitcnt vmcnt(18)
	s_waitcnt vmcnt(17)
	s_waitcnt vmcnt(16)
	ds_read_b32 v26, v187
	s_waitcnt lgkmcnt(0)
	v_pk_fma_f32 v[28:29], v[26:27], v[102:103], 0 op_sel_hi:[0,1,0] neg_lo:[1,0,0] neg_hi:[1,0,0]
	v_pk_fma_f32 v[26:27], v[26:27], v[104:105], 0 op_sel_hi:[0,1,0] neg_lo:[1,0,0] neg_hi:[1,0,0]
	v_cvt_pk_bf16_f32 v28, v28, v29
	v_cvt_pk_bf16_f32 v29, v26, v27
	ds_write_b64 v186, v[28:29]
	ds_read_b32 v26, v187 offset:8
	s_waitcnt lgkmcnt(0)
	v_pk_fma_f32 v[28:29], v[26:27], v[86:87], 0 op_sel_hi:[0,1,0] neg_lo:[1,0,0] neg_hi:[1,0,0]
	v_pk_fma_f32 v[26:27], v[26:27], v[88:89], 0 op_sel_hi:[0,1,0] neg_lo:[1,0,0] neg_hi:[1,0,0]
	v_cvt_pk_bf16_f32 v28, v28, v29
	v_cvt_pk_bf16_f32 v29, v26, v27
	ds_write_b64 v186, v[28:29] offset:544
	ds_read_b32 v26, v187 offset:16
	s_waitcnt lgkmcnt(0)
	v_pk_fma_f32 v[28:29], v[26:27], v[74:75], 0 op_sel_hi:[0,1,0] neg_lo:[1,0,0] neg_hi:[1,0,0]
	v_pk_fma_f32 v[26:27], v[26:27], v[76:77], 0 op_sel_hi:[0,1,0] neg_lo:[1,0,0] neg_hi:[1,0,0]
	v_cvt_pk_bf16_f32 v28, v28, v29
	v_cvt_pk_bf16_f32 v29, v26, v27
	ds_write_b64 v186, v[28:29] offset:1088
	ds_read_b32 v26, v187 offset:24
	s_waitcnt lgkmcnt(0)
	v_pk_fma_f32 v[28:29], v[26:27], v[62:63], 0 op_sel_hi:[0,1,0] neg_lo:[1,0,0] neg_hi:[1,0,0]
	v_pk_fma_f32 v[26:27], v[26:27], v[64:65], 0 op_sel_hi:[0,1,0] neg_lo:[1,0,0] neg_hi:[1,0,0]
	v_cvt_pk_bf16_f32 v28, v28, v29
	v_cvt_pk_bf16_f32 v29, v26, v27
	ds_write_b64 v186, v[28:29] offset:1632
	ds_read_b32 v26, v187 offset:32
	s_waitcnt lgkmcnt(0)
	v_pk_fma_f32 v[28:29], v[26:27], v[58:59], 0 op_sel_hi:[0,1,0] neg_lo:[1,0,0] neg_hi:[1,0,0]
	v_pk_fma_f32 v[26:27], v[26:27], v[60:61], 0 op_sel_hi:[0,1,0] neg_lo:[1,0,0] neg_hi:[1,0,0]
	v_cvt_pk_bf16_f32 v28, v28, v29
	v_cvt_pk_bf16_f32 v29, v26, v27
	ds_write_b64 v186, v[28:29] offset:2176
	ds_read_b32 v26, v187 offset:40
	s_waitcnt lgkmcnt(0)
	v_pk_fma_f32 v[28:29], v[26:27], v[46:47], 0 op_sel_hi:[0,1,0] neg_lo:[1,0,0] neg_hi:[1,0,0]
	v_pk_fma_f32 v[26:27], v[26:27], v[48:49], 0 op_sel_hi:[0,1,0] neg_lo:[1,0,0] neg_hi:[1,0,0]
	v_cvt_pk_bf16_f32 v28, v28, v29
	v_cvt_pk_bf16_f32 v29, v26, v27
	ds_write_b64 v186, v[28:29] offset:2720
	ds_read_b32 v26, v187 offset:48
	s_waitcnt lgkmcnt(0)
	v_pk_fma_f32 v[28:29], v[26:27], v[42:43], 0 op_sel_hi:[0,1,0] neg_lo:[1,0,0] neg_hi:[1,0,0]
	v_pk_fma_f32 v[26:27], v[26:27], v[44:45], 0 op_sel_hi:[0,1,0] neg_lo:[1,0,0] neg_hi:[1,0,0]
	v_cvt_pk_bf16_f32 v28, v28, v29
	v_cvt_pk_bf16_f32 v29, v26, v27
	ds_write_b64 v186, v[28:29] offset:3264
	ds_read_b32 v26, v187 offset:56
	s_waitcnt lgkmcnt(0)
	v_pk_fma_f32 v[28:29], v[26:27], v[30:31], 0 op_sel_hi:[0,1,0] neg_lo:[1,0,0] neg_hi:[1,0,0]
	v_pk_fma_f32 v[26:27], v[26:27], v[32:33], 0 op_sel_hi:[0,1,0] neg_lo:[1,0,0] neg_hi:[1,0,0]
	v_cvt_pk_bf16_f32 v28, v28, v29
	v_cvt_pk_bf16_f32 v29, v26, v27
	ds_write_b64 v186, v[28:29] offset:3808
	ds_read_b128 a[48:51], v1
	ds_read_b128 a[52:55], v1 offset:64
	ds_read_b128 a[56:59], v1 offset:128
	ds_read_b128 a[60:63], v1 offset:192
	v_lshl_add_u64 v[26:27], v[130:131], 0, s[26:27]
	v_add_co_u32_e32 v28, vcc, s7, v26
	s_nop 1
	v_addc_co_u32_e32 v29, vcc, 0, v27, vcc
	global_load_dwordx4 v[86:89], v[26:27], off nt
	global_load_dwordx4 v[82:85], v[28:29], off nt
	v_add_co_u32_e32 v28, vcc, s36, v26
	s_nop 1
	v_addc_co_u32_e32 v29, vcc, 0, v27, vcc
	v_add_co_u32_e32 v30, vcc, s37, v26
	s_nop 1
	v_addc_co_u32_e32 v31, vcc, 0, v27, vcc
	global_load_dwordx4 v[78:81], v[28:29], off nt
	global_load_dwordx4 v[58:61], v[30:31], off nt
	v_add_co_u32_e32 v28, vcc, s38, v26
	s_nop 1
	v_addc_co_u32_e32 v29, vcc, 0, v27, vcc
	v_add_co_u32_e32 v30, vcc, s39, v26
	s_nop 1
	v_addc_co_u32_e32 v31, vcc, 0, v27, vcc
	global_load_dwordx4 v[46:49], v[28:29], off nt
	global_load_dwordx4 v[42:45], v[30:31], off nt
	v_add_co_u32_e32 v28, vcc, s41, v26
	s_nop 1
	v_addc_co_u32_e32 v29, vcc, 0, v27, vcc
	v_add_co_u32_e32 v26, vcc, s42, v26
	s_nop 1
	v_addc_co_u32_e32 v27, vcc, 0, v27, vcc
	global_load_dwordx4 v[30:33], v[28:29], off nt
	s_nop 0
	global_load_dwordx4 v[26:29], v[26:27], off nt
	v_mov_b32_e32 v62, v197
	s_waitcnt vmcnt(23)
	s_waitcnt vmcnt(22)
	s_waitcnt vmcnt(21)
	s_waitcnt vmcnt(20)
	s_waitcnt vmcnt(19)
	s_waitcnt vmcnt(18)
	s_waitcnt vmcnt(17)
	s_waitcnt vmcnt(16)
	ds_read_b32 v62, v187 offset:64
	s_waitcnt lgkmcnt(0)
	v_pk_fma_f32 v[64:65], v[62:63], v[110:111], 0 op_sel_hi:[0,1,0] neg_lo:[1,0,0] neg_hi:[1,0,0]
	v_pk_fma_f32 v[62:63], v[62:63], v[112:113], 0 op_sel_hi:[0,1,0] neg_lo:[1,0,0] neg_hi:[1,0,0]
	v_cvt_pk_bf16_f32 v64, v64, v65
	v_cvt_pk_bf16_f32 v65, v62, v63
	ds_write_b64 v186, v[64:65]
	ds_read_b32 v62, v187 offset:72
	s_waitcnt lgkmcnt(0)
	v_pk_fma_f32 v[64:65], v[62:63], v[90:91], 0 op_sel_hi:[0,1,0] neg_lo:[1,0,0] neg_hi:[1,0,0]
	v_pk_fma_f32 v[62:63], v[62:63], v[92:93], 0 op_sel_hi:[0,1,0] neg_lo:[1,0,0] neg_hi:[1,0,0]
	v_cvt_pk_bf16_f32 v64, v64, v65
	v_cvt_pk_bf16_f32 v65, v62, v63
	ds_write_b64 v186, v[64:65] offset:544
	ds_read_b32 v62, v187 offset:80
	s_waitcnt lgkmcnt(0)
	v_pk_fma_f32 v[64:65], v[62:63], v[70:71], 0 op_sel_hi:[0,1,0] neg_lo:[1,0,0] neg_hi:[1,0,0]
	v_pk_fma_f32 v[62:63], v[62:63], v[72:73], 0 op_sel_hi:[0,1,0] neg_lo:[1,0,0] neg_hi:[1,0,0]
	v_cvt_pk_bf16_f32 v64, v64, v65
	v_cvt_pk_bf16_f32 v65, v62, v63
	ds_write_b64 v186, v[64:65] offset:1088
	ds_read_b32 v62, v187 offset:88
	s_waitcnt lgkmcnt(0)
	v_pk_fma_f32 v[50:51], v[62:63], v[50:51], 0 op_sel_hi:[0,1,0] neg_lo:[1,0,0] neg_hi:[1,0,0]
	v_pk_fma_f32 v[52:53], v[62:63], v[52:53], 0 op_sel_hi:[0,1,0] neg_lo:[1,0,0] neg_hi:[1,0,0]
	v_cvt_pk_bf16_f32 v50, v50, v51
	v_cvt_pk_bf16_f32 v51, v52, v53
	ds_write_b64 v186, v[50:51] offset:1632
	ds_read_b32 v50, v187 offset:96
	s_waitcnt lgkmcnt(0)
	v_pk_fma_f32 v[34:35], v[50:51], v[34:35], 0 op_sel_hi:[0,1,0] neg_lo:[1,0,0] neg_hi:[1,0,0]
	v_pk_fma_f32 v[36:37], v[50:51], v[36:37], 0 op_sel_hi:[0,1,0] neg_lo:[1,0,0] neg_hi:[1,0,0]
	v_cvt_pk_bf16_f32 v34, v34, v35
	v_cvt_pk_bf16_f32 v35, v36, v37
	ds_write_b64 v186, v[34:35] offset:2176
	ds_read_b32 v34, v187 offset:104
	s_waitcnt lgkmcnt(0)
	v_pk_fma_f32 v[22:23], v[34:35], v[22:23], 0 op_sel_hi:[0,1,0] neg_lo:[1,0,0] neg_hi:[1,0,0]
	v_pk_fma_f32 v[24:25], v[34:35], v[24:25], 0 op_sel_hi:[0,1,0] neg_lo:[1,0,0] neg_hi:[1,0,0]
	v_cvt_pk_bf16_f32 v22, v22, v23
	v_cvt_pk_bf16_f32 v23, v24, v25
	ds_write_b64 v186, v[22:23] offset:2720
	ds_read_b32 v22, v187 offset:112
	s_waitcnt lgkmcnt(0)
	v_pk_fma_f32 v[14:15], v[22:23], v[14:15], 0 op_sel_hi:[0,1,0] neg_lo:[1,0,0] neg_hi:[1,0,0]
	v_pk_fma_f32 v[16:17], v[22:23], v[16:17], 0 op_sel_hi:[0,1,0] neg_lo:[1,0,0] neg_hi:[1,0,0]
	v_cvt_pk_bf16_f32 v14, v14, v15
	v_cvt_pk_bf16_f32 v15, v16, v17
	ds_write_b64 v186, v[14:15] offset:3264
	ds_read_b32 v14, v187 offset:120
	s_waitcnt lgkmcnt(0)
	v_pk_fma_f32 v[6:7], v[14:15], v[6:7], 0 op_sel_hi:[0,1,0] neg_lo:[1,0,0] neg_hi:[1,0,0]
	v_pk_fma_f32 v[8:9], v[14:15], v[8:9], 0 op_sel_hi:[0,1,0] neg_lo:[1,0,0] neg_hi:[1,0,0]
	v_cvt_pk_bf16_f32 v6, v6, v7
	v_cvt_pk_bf16_f32 v7, v8, v9
	ds_write_b64 v186, v[6:7] offset:3808
	ds_read_b128 a[64:67], v1
	ds_read_b128 a[68:71], v1 offset:64
	ds_read_b128 a[72:75], v1 offset:128
	ds_read_b128 a[76:79], v1 offset:192
	v_lshl_add_u64 v[6:7], v[150:151], 0, s[26:27]
	v_lshl_add_u64 v[8:9], v[152:153], 0, s[26:27]
	v_lshl_add_u64 v[14:15], v[156:157], 0, s[26:27]
	v_lshl_add_u64 v[16:17], v[158:159], 0, s[26:27]
	v_lshl_add_u64 v[22:23], v[160:161], 0, s[26:27]
	v_lshl_add_u64 v[24:25], v[162:163], 0, s[26:27]
	v_lshl_add_u64 v[70:71], v[164:165], 0, s[26:27]
	v_lshl_add_u64 v[72:73], v[166:167], 0, s[26:27]
	global_load_dwordx4 v[110:113], v[6:7], off nt
	global_load_dwordx4 v[98:101], v[8:9], off nt
	global_load_dwordx4 v[62:65], v[14:15], off nt
	global_load_dwordx4 v[50:53], v[16:17], off nt
	global_load_dwordx4 v[34:37], v[22:23], off nt
	s_nop 0
	global_load_dwordx4 v[22:25], v[24:25], off nt
	s_nop 0
	global_load_dwordx4 v[14:17], v[70:71], off nt
	global_load_dwordx4 v[6:9], v[72:73], off nt
	s_waitcnt vmcnt(23)
	s_waitcnt vmcnt(22)
	s_waitcnt vmcnt(21)
	s_waitcnt vmcnt(20)
	s_waitcnt vmcnt(19)
	s_waitcnt vmcnt(18)
	s_waitcnt vmcnt(17)
	s_waitcnt vmcnt(16)
	ds_read_b32 v70, v187 offset:128
	s_waitcnt lgkmcnt(0)
	v_pk_fma_f32 v[72:73], v[70:71], v[106:107], 0 op_sel_hi:[0,1,0] neg_lo:[1,0,0] neg_hi:[1,0,0]
	v_pk_fma_f32 v[70:71], v[70:71], v[108:109], 0 op_sel_hi:[0,1,0] neg_lo:[1,0,0] neg_hi:[1,0,0]
	v_cvt_pk_bf16_f32 v72, v72, v73
	v_cvt_pk_bf16_f32 v73, v70, v71
	ds_write_b64 v186, v[72:73]
	ds_read_b32 v70, v187 offset:136
	s_waitcnt lgkmcnt(0)
	v_pk_fma_f32 v[72:73], v[70:71], v[94:95], 0 op_sel_hi:[0,1,0] neg_lo:[1,0,0] neg_hi:[1,0,0]
	v_pk_fma_f32 v[70:71], v[70:71], v[96:97], 0 op_sel_hi:[0,1,0] neg_lo:[1,0,0] neg_hi:[1,0,0]
	v_cvt_pk_bf16_f32 v72, v72, v73
	v_cvt_pk_bf16_f32 v73, v70, v71
	ds_write_b64 v186, v[72:73] offset:544
	ds_read_b32 v70, v187 offset:144
	s_waitcnt lgkmcnt(0)
	v_pk_fma_f32 v[66:67], v[70:71], v[66:67], 0 op_sel_hi:[0,1,0] neg_lo:[1,0,0] neg_hi:[1,0,0]
	v_pk_fma_f32 v[68:69], v[70:71], v[68:69], 0 op_sel_hi:[0,1,0] neg_lo:[1,0,0] neg_hi:[1,0,0]
	v_cvt_pk_bf16_f32 v66, v66, v67
	v_cvt_pk_bf16_f32 v67, v68, v69
	ds_write_b64 v186, v[66:67] offset:1088
	ds_read_b32 v66, v187 offset:152
	s_waitcnt lgkmcnt(0)
	v_pk_fma_f32 v[54:55], v[66:67], v[54:55], 0 op_sel_hi:[0,1,0] neg_lo:[1,0,0] neg_hi:[1,0,0]
	v_pk_fma_f32 v[56:57], v[66:67], v[56:57], 0 op_sel_hi:[0,1,0] neg_lo:[1,0,0] neg_hi:[1,0,0]
	v_cvt_pk_bf16_f32 v54, v54, v55
	v_cvt_pk_bf16_f32 v55, v56, v57
	ds_write_b64 v186, v[54:55] offset:1632
	ds_read_b32 v54, v187 offset:160
	s_waitcnt lgkmcnt(0)
	v_pk_fma_f32 v[38:39], v[54:55], v[38:39], 0 op_sel_hi:[0,1,0] neg_lo:[1,0,0] neg_hi:[1,0,0]
	v_pk_fma_f32 v[40:41], v[54:55], v[40:41], 0 op_sel_hi:[0,1,0] neg_lo:[1,0,0] neg_hi:[1,0,0]
	v_cvt_pk_bf16_f32 v38, v38, v39
	v_cvt_pk_bf16_f32 v39, v40, v41
	ds_write_b64 v186, v[38:39] offset:2176
	ds_read_b32 v38, v187 offset:168
	s_waitcnt lgkmcnt(0)
	v_pk_fma_f32 v[18:19], v[38:39], v[18:19], 0 op_sel_hi:[0,1,0] neg_lo:[1,0,0] neg_hi:[1,0,0]
	v_pk_fma_f32 v[20:21], v[38:39], v[20:21], 0 op_sel_hi:[0,1,0] neg_lo:[1,0,0] neg_hi:[1,0,0]
	v_cvt_pk_bf16_f32 v18, v18, v19
	v_cvt_pk_bf16_f32 v19, v20, v21
	ds_write_b64 v186, v[18:19] offset:2720
	ds_read_b32 v18, v187 offset:176
	s_waitcnt lgkmcnt(0)
	v_pk_fma_f32 v[10:11], v[18:19], v[10:11], 0 op_sel_hi:[0,1,0] neg_lo:[1,0,0] neg_hi:[1,0,0]
	v_pk_fma_f32 v[12:13], v[18:19], v[12:13], 0 op_sel_hi:[0,1,0] neg_lo:[1,0,0] neg_hi:[1,0,0]
	v_cvt_pk_bf16_f32 v10, v10, v11
	v_cvt_pk_bf16_f32 v11, v12, v13
	ds_write_b64 v186, v[10:11] offset:3264
	ds_read_b32 v10, v187 offset:184
	s_waitcnt lgkmcnt(0)
	v_pk_fma_f32 v[2:3], v[10:11], v[2:3], 0 op_sel_hi:[0,1,0] neg_lo:[1,0,0] neg_hi:[1,0,0]
	v_pk_fma_f32 v[4:5], v[10:11], v[4:5], 0 op_sel_hi:[0,1,0] neg_lo:[1,0,0] neg_hi:[1,0,0]
	v_cvt_pk_bf16_f32 v2, v2, v3
	v_cvt_pk_bf16_f32 v3, v4, v5
	ds_write_b64 v186, v[2:3] offset:3808
	ds_read_b128 a[80:83], v1
	ds_read_b128 a[84:87], v1 offset:64
	ds_read_b128 a[88:91], v1 offset:128
	ds_read_b128 a[92:95], v1 offset:192
	v_lshl_add_u64 v[2:3], v[168:169], 0, s[26:27]
	v_lshl_add_u64 v[4:5], v[170:171], 0, s[26:27]
	v_lshl_add_u64 v[10:11], v[172:173], 0, s[26:27]
	v_lshl_add_u64 v[12:13], v[174:175], 0, s[26:27]
	v_lshl_add_u64 v[18:19], v[176:177], 0, s[26:27]
	v_lshl_add_u64 v[20:21], v[178:179], 0, s[26:27]
	v_lshl_add_u64 v[66:67], v[180:181], 0, s[26:27]
	v_lshl_add_u64 v[68:69], v[182:183], 0, s[26:27]
	global_load_dwordx4 v[106:109], v[2:3], off nt
	global_load_dwordx4 v[94:97], v[4:5], off nt
	global_load_dwordx4 v[74:77], v[10:11], off nt
	global_load_dwordx4 v[54:57], v[12:13], off nt
	global_load_dwordx4 v[38:41], v[18:19], off nt
	s_nop 0
	global_load_dwordx4 v[18:21], v[20:21], off nt
	s_nop 0
	global_load_dwordx4 v[10:13], v[66:67], off nt
	global_load_dwordx4 v[2:5], v[68:69], off nt
	v_mov_b32_e32 v66, v196
	s_waitcnt vmcnt(23)
	s_waitcnt vmcnt(22)
	s_waitcnt vmcnt(21)
	s_waitcnt vmcnt(20)
	s_waitcnt vmcnt(19)
	s_waitcnt vmcnt(18)
	s_waitcnt vmcnt(17)
	s_waitcnt vmcnt(16)
	ds_read_b32 v66, v187
	s_waitcnt lgkmcnt(0)
	v_pk_fma_f32 v[68:69], v[66:67], v[86:87], 0 op_sel_hi:[0,1,0] neg_lo:[1,0,0] neg_hi:[1,0,0]
	v_pk_fma_f32 v[66:67], v[66:67], v[88:89], 0 op_sel_hi:[0,1,0] neg_lo:[1,0,0] neg_hi:[1,0,0]
	v_cvt_pk_bf16_f32 v68, v68, v69
	v_cvt_pk_bf16_f32 v69, v66, v67
	ds_write_b64 v186, v[68:69]
	ds_read_b32 v66, v187 offset:8
	s_waitcnt lgkmcnt(0)
	v_pk_fma_f32 v[68:69], v[66:67], v[82:83], 0 op_sel_hi:[0,1,0] neg_lo:[1,0,0] neg_hi:[1,0,0]
	v_pk_fma_f32 v[66:67], v[66:67], v[84:85], 0 op_sel_hi:[0,1,0] neg_lo:[1,0,0] neg_hi:[1,0,0]
	v_cvt_pk_bf16_f32 v68, v68, v69
	v_cvt_pk_bf16_f32 v69, v66, v67
	ds_write_b64 v186, v[68:69] offset:544
	ds_read_b32 v66, v187 offset:16
	s_waitcnt lgkmcnt(0)
	v_pk_fma_f32 v[68:69], v[66:67], v[78:79], 0 op_sel_hi:[0,1,0] neg_lo:[1,0,0] neg_hi:[1,0,0]
	v_pk_fma_f32 v[66:67], v[66:67], v[80:81], 0 op_sel_hi:[0,1,0] neg_lo:[1,0,0] neg_hi:[1,0,0]
	v_cvt_pk_bf16_f32 v68, v68, v69
	v_cvt_pk_bf16_f32 v69, v66, v67
	ds_write_b64 v186, v[68:69] offset:1088
	ds_read_b32 v66, v187 offset:24
	s_waitcnt lgkmcnt(0)
	v_pk_fma_f32 v[58:59], v[66:67], v[58:59], 0 op_sel_hi:[0,1,0] neg_lo:[1,0,0] neg_hi:[1,0,0]
	v_pk_fma_f32 v[60:61], v[66:67], v[60:61], 0 op_sel_hi:[0,1,0] neg_lo:[1,0,0] neg_hi:[1,0,0]
	v_cvt_pk_bf16_f32 v58, v58, v59
	v_cvt_pk_bf16_f32 v59, v60, v61
	ds_write_b64 v186, v[58:59] offset:1632
	ds_read_b32 v58, v187 offset:32
	s_waitcnt lgkmcnt(0)
	v_pk_fma_f32 v[46:47], v[58:59], v[46:47], 0 op_sel_hi:[0,1,0] neg_lo:[1,0,0] neg_hi:[1,0,0]
	v_pk_fma_f32 v[48:49], v[58:59], v[48:49], 0 op_sel_hi:[0,1,0] neg_lo:[1,0,0] neg_hi:[1,0,0]
	v_cvt_pk_bf16_f32 v46, v46, v47
	v_cvt_pk_bf16_f32 v47, v48, v49
	ds_write_b64 v186, v[46:47] offset:2176
	ds_read_b32 v46, v187 offset:40
	s_waitcnt lgkmcnt(0)
	v_pk_fma_f32 v[42:43], v[46:47], v[42:43], 0 op_sel_hi:[0,1,0] neg_lo:[1,0,0] neg_hi:[1,0,0]
	v_pk_fma_f32 v[44:45], v[46:47], v[44:45], 0 op_sel_hi:[0,1,0] neg_lo:[1,0,0] neg_hi:[1,0,0]
	v_cvt_pk_bf16_f32 v42, v42, v43
	v_cvt_pk_bf16_f32 v43, v44, v45
	ds_write_b64 v186, v[42:43] offset:2720
	ds_read_b32 v42, v187 offset:48
	s_waitcnt lgkmcnt(0)
	v_pk_fma_f32 v[30:31], v[42:43], v[30:31], 0 op_sel_hi:[0,1,0] neg_lo:[1,0,0] neg_hi:[1,0,0]
	v_pk_fma_f32 v[32:33], v[42:43], v[32:33], 0 op_sel_hi:[0,1,0] neg_lo:[1,0,0] neg_hi:[1,0,0]
	v_cvt_pk_bf16_f32 v30, v30, v31
	v_cvt_pk_bf16_f32 v31, v32, v33
	ds_write_b64 v186, v[30:31] offset:3264
	ds_read_b32 v30, v187 offset:56
	s_waitcnt lgkmcnt(0)
	v_pk_fma_f32 v[26:27], v[30:31], v[26:27], 0 op_sel_hi:[0,1,0] neg_lo:[1,0,0] neg_hi:[1,0,0]
	v_pk_fma_f32 v[28:29], v[30:31], v[28:29], 0 op_sel_hi:[0,1,0] neg_lo:[1,0,0] neg_hi:[1,0,0]
	v_cvt_pk_bf16_f32 v26, v26, v27
	v_cvt_pk_bf16_f32 v27, v28, v29
	ds_write_b64 v186, v[26:27] offset:3808
	ds_read_b128 a[96:99], v1
	ds_read_b128 a[100:103], v1 offset:64
	ds_read_b128 a[104:107], v1 offset:128
	ds_read_b128 a[108:111], v1 offset:192
	v_lshl_add_u64 v[26:27], v[130:131], 0, s[24:25]
	v_add_co_u32_e32 v28, vcc, s7, v26
	s_nop 1
	v_addc_co_u32_e32 v29, vcc, 0, v27, vcc
	global_load_dwordx4 v[102:105], v[26:27], off nt
	global_load_dwordx4 v[90:93], v[28:29], off nt
	v_add_co_u32_e32 v28, vcc, s36, v26
	s_nop 1
	v_addc_co_u32_e32 v29, vcc, 0, v27, vcc
	v_add_co_u32_e32 v30, vcc, s37, v26
	s_nop 1
	v_addc_co_u32_e32 v31, vcc, 0, v27, vcc
	global_load_dwordx4 v[86:89], v[28:29], off nt
	global_load_dwordx4 v[70:73], v[30:31], off nt
	v_add_co_u32_e32 v28, vcc, s38, v26
	s_nop 1
	v_addc_co_u32_e32 v29, vcc, 0, v27, vcc
	v_add_co_u32_e32 v30, vcc, s39, v26
	s_nop 1
	v_addc_co_u32_e32 v31, vcc, 0, v27, vcc
	global_load_dwordx4 v[66:69], v[28:29], off nt
	global_load_dwordx4 v[46:49], v[30:31], off nt
	v_add_co_u32_e32 v28, vcc, s41, v26
	s_nop 1
	v_addc_co_u32_e32 v29, vcc, 0, v27, vcc
	v_add_co_u32_e32 v26, vcc, s42, v26
	s_nop 1
	v_addc_co_u32_e32 v27, vcc, 0, v27, vcc
	global_load_dwordx4 v[42:45], v[28:29], off nt
	global_load_dwordx4 v[30:33], v[26:27], off nt
	v_mov_b32_e32 v26, v196
	s_waitcnt vmcnt(23)
	s_waitcnt vmcnt(22)
	s_waitcnt vmcnt(21)
	s_waitcnt vmcnt(20)
	s_waitcnt vmcnt(19)
	s_waitcnt vmcnt(18)
	s_waitcnt vmcnt(17)
	s_waitcnt vmcnt(16)
	ds_read_b32 v26, v187 offset:64
	s_waitcnt lgkmcnt(0)
	v_pk_fma_f32 v[28:29], v[26:27], v[110:111], 0 op_sel_hi:[0,1,0] neg_lo:[1,0,0] neg_hi:[1,0,0]
	v_pk_fma_f32 v[26:27], v[26:27], v[112:113], 0 op_sel_hi:[0,1,0] neg_lo:[1,0,0] neg_hi:[1,0,0]
	v_cvt_pk_bf16_f32 v28, v28, v29
	v_cvt_pk_bf16_f32 v29, v26, v27
	ds_write_b64 v186, v[28:29]
	ds_read_b32 v26, v187 offset:72
	s_waitcnt lgkmcnt(0)
	v_pk_fma_f32 v[28:29], v[26:27], v[98:99], 0 op_sel_hi:[0,1,0] neg_lo:[1,0,0] neg_hi:[1,0,0]
	v_pk_fma_f32 v[26:27], v[26:27], v[100:101], 0 op_sel_hi:[0,1,0] neg_lo:[1,0,0] neg_hi:[1,0,0]
	v_cvt_pk_bf16_f32 v28, v28, v29
	v_cvt_pk_bf16_f32 v29, v26, v27
	ds_write_b64 v186, v[28:29] offset:544
	ds_read_b32 v26, v187 offset:80
	s_waitcnt lgkmcnt(0)
	v_pk_fma_f32 v[28:29], v[26:27], v[62:63], 0 op_sel_hi:[0,1,0] neg_lo:[1,0,0] neg_hi:[1,0,0]
	v_pk_fma_f32 v[26:27], v[26:27], v[64:65], 0 op_sel_hi:[0,1,0] neg_lo:[1,0,0] neg_hi:[1,0,0]
	v_cvt_pk_bf16_f32 v28, v28, v29
	v_cvt_pk_bf16_f32 v29, v26, v27
	ds_write_b64 v186, v[28:29] offset:1088
	ds_read_b32 v26, v187 offset:88
	s_waitcnt lgkmcnt(0)
	v_pk_fma_f32 v[28:29], v[26:27], v[50:51], 0 op_sel_hi:[0,1,0] neg_lo:[1,0,0] neg_hi:[1,0,0]
	v_pk_fma_f32 v[26:27], v[26:27], v[52:53], 0 op_sel_hi:[0,1,0] neg_lo:[1,0,0] neg_hi:[1,0,0]
	v_cvt_pk_bf16_f32 v28, v28, v29
	v_cvt_pk_bf16_f32 v29, v26, v27
	ds_write_b64 v186, v[28:29] offset:1632
	ds_read_b32 v26, v187 offset:96
	s_waitcnt lgkmcnt(0)
	v_pk_fma_f32 v[28:29], v[26:27], v[34:35], 0 op_sel_hi:[0,1,0] neg_lo:[1,0,0] neg_hi:[1,0,0]
	v_pk_fma_f32 v[26:27], v[26:27], v[36:37], 0 op_sel_hi:[0,1,0] neg_lo:[1,0,0] neg_hi:[1,0,0]
	v_cvt_pk_bf16_f32 v28, v28, v29
	v_cvt_pk_bf16_f32 v29, v26, v27
	ds_write_b64 v186, v[28:29] offset:2176
	ds_read_b32 v26, v187 offset:104
	s_waitcnt lgkmcnt(0)
	v_pk_fma_f32 v[22:23], v[26:27], v[22:23], 0 op_sel_hi:[0,1,0] neg_lo:[1,0,0] neg_hi:[1,0,0]
	v_pk_fma_f32 v[24:25], v[26:27], v[24:25], 0 op_sel_hi:[0,1,0] neg_lo:[1,0,0] neg_hi:[1,0,0]
	v_cvt_pk_bf16_f32 v22, v22, v23
	v_cvt_pk_bf16_f32 v23, v24, v25
	ds_write_b64 v186, v[22:23] offset:2720
	ds_read_b32 v22, v187 offset:112
	s_waitcnt lgkmcnt(0)
	v_pk_fma_f32 v[14:15], v[22:23], v[14:15], 0 op_sel_hi:[0,1,0] neg_lo:[1,0,0] neg_hi:[1,0,0]
	v_pk_fma_f32 v[16:17], v[22:23], v[16:17], 0 op_sel_hi:[0,1,0] neg_lo:[1,0,0] neg_hi:[1,0,0]
	v_cvt_pk_bf16_f32 v14, v14, v15
	v_cvt_pk_bf16_f32 v15, v16, v17
	ds_write_b64 v186, v[14:15] offset:3264
	ds_read_b32 v14, v187 offset:120
	s_waitcnt lgkmcnt(0)
	v_pk_fma_f32 v[6:7], v[14:15], v[6:7], 0 op_sel_hi:[0,1,0] neg_lo:[1,0,0] neg_hi:[1,0,0]
	v_pk_fma_f32 v[8:9], v[14:15], v[8:9], 0 op_sel_hi:[0,1,0] neg_lo:[1,0,0] neg_hi:[1,0,0]
	v_cvt_pk_bf16_f32 v6, v6, v7
	v_cvt_pk_bf16_f32 v7, v8, v9
	ds_write_b64 v186, v[6:7] offset:3808
	ds_read_b128 a[112:115], v1
	ds_read_b128 a[116:119], v1 offset:64
	ds_read_b128 a[120:123], v1 offset:128
	ds_read_b128 a[124:127], v1 offset:192
	v_lshl_add_u64 v[6:7], v[150:151], 0, s[24:25]
	v_lshl_add_u64 v[8:9], v[152:153], 0, s[24:25]
	v_lshl_add_u64 v[14:15], v[156:157], 0, s[24:25]
	v_lshl_add_u64 v[16:17], v[158:159], 0, s[24:25]
	v_lshl_add_u64 v[22:23], v[160:161], 0, s[24:25]
	v_lshl_add_u64 v[24:25], v[162:163], 0, s[24:25]
	v_lshl_add_u64 v[26:27], v[164:165], 0, s[24:25]
	v_lshl_add_u64 v[28:29], v[166:167], 0, s[24:25]
	global_load_dwordx4 v[110:113], v[6:7], off nt
	global_load_dwordx4 v[98:101], v[8:9], off nt
	global_load_dwordx4 v[78:81], v[14:15], off nt
	global_load_dwordx4 v[58:61], v[16:17], off nt
	global_load_dwordx4 v[34:37], v[22:23], off nt
	s_nop 0
	global_load_dwordx4 v[22:25], v[24:25], off nt
	s_nop 0
	global_load_dwordx4 v[14:17], v[26:27], off nt
	global_load_dwordx4 v[6:9], v[28:29], off nt
	s_waitcnt vmcnt(23)
	s_waitcnt vmcnt(22)
	s_waitcnt vmcnt(21)
	s_waitcnt vmcnt(20)
	s_waitcnt vmcnt(19)
	s_waitcnt vmcnt(18)
	s_waitcnt vmcnt(17)
	s_waitcnt vmcnt(16)
	ds_read_b32 v26, v187 offset:128
	s_waitcnt lgkmcnt(0)
	v_pk_fma_f32 v[28:29], v[26:27], v[106:107], 0 op_sel_hi:[0,1,0] neg_lo:[1,0,0] neg_hi:[1,0,0]
	v_pk_fma_f32 v[26:27], v[26:27], v[108:109], 0 op_sel_hi:[0,1,0] neg_lo:[1,0,0] neg_hi:[1,0,0]
	v_cvt_pk_bf16_f32 v28, v28, v29
	v_cvt_pk_bf16_f32 v29, v26, v27
	ds_write_b64 v186, v[28:29]
	ds_read_b32 v26, v187 offset:136
	s_waitcnt lgkmcnt(0)
	v_pk_fma_f32 v[28:29], v[26:27], v[94:95], 0 op_sel_hi:[0,1,0] neg_lo:[1,0,0] neg_hi:[1,0,0]
	v_pk_fma_f32 v[26:27], v[26:27], v[96:97], 0 op_sel_hi:[0,1,0] neg_lo:[1,0,0] neg_hi:[1,0,0]
	v_cvt_pk_bf16_f32 v28, v28, v29
	v_cvt_pk_bf16_f32 v29, v26, v27
	ds_write_b64 v186, v[28:29] offset:544
	ds_read_b32 v26, v187 offset:144
	s_waitcnt lgkmcnt(0)
	v_pk_fma_f32 v[28:29], v[26:27], v[74:75], 0 op_sel_hi:[0,1,0] neg_lo:[1,0,0] neg_hi:[1,0,0]
	v_pk_fma_f32 v[26:27], v[26:27], v[76:77], 0 op_sel_hi:[0,1,0] neg_lo:[1,0,0] neg_hi:[1,0,0]
	v_cvt_pk_bf16_f32 v28, v28, v29
	v_cvt_pk_bf16_f32 v29, v26, v27
	ds_write_b64 v186, v[28:29] offset:1088
	ds_read_b32 v26, v187 offset:152
	s_waitcnt lgkmcnt(0)
	v_pk_fma_f32 v[28:29], v[26:27], v[54:55], 0 op_sel_hi:[0,1,0] neg_lo:[1,0,0] neg_hi:[1,0,0]
	v_pk_fma_f32 v[26:27], v[26:27], v[56:57], 0 op_sel_hi:[0,1,0] neg_lo:[1,0,0] neg_hi:[1,0,0]
	v_cvt_pk_bf16_f32 v28, v28, v29
	v_cvt_pk_bf16_f32 v29, v26, v27
	ds_write_b64 v186, v[28:29] offset:1632
	ds_read_b32 v26, v187 offset:160
	s_waitcnt lgkmcnt(0)
	v_pk_fma_f32 v[28:29], v[26:27], v[38:39], 0 op_sel_hi:[0,1,0] neg_lo:[1,0,0] neg_hi:[1,0,0]
	v_pk_fma_f32 v[26:27], v[26:27], v[40:41], 0 op_sel_hi:[0,1,0] neg_lo:[1,0,0] neg_hi:[1,0,0]
	v_cvt_pk_bf16_f32 v28, v28, v29
	v_cvt_pk_bf16_f32 v29, v26, v27
	ds_write_b64 v186, v[28:29] offset:2176
	ds_read_b32 v26, v187 offset:168
	s_waitcnt lgkmcnt(0)
	v_pk_fma_f32 v[18:19], v[26:27], v[18:19], 0 op_sel_hi:[0,1,0] neg_lo:[1,0,0] neg_hi:[1,0,0]
	v_pk_fma_f32 v[20:21], v[26:27], v[20:21], 0 op_sel_hi:[0,1,0] neg_lo:[1,0,0] neg_hi:[1,0,0]
	v_cvt_pk_bf16_f32 v18, v18, v19
	v_cvt_pk_bf16_f32 v19, v20, v21
	ds_write_b64 v186, v[18:19] offset:2720
	ds_read_b32 v18, v187 offset:176
	s_waitcnt lgkmcnt(0)
	v_pk_fma_f32 v[10:11], v[18:19], v[10:11], 0 op_sel_hi:[0,1,0] neg_lo:[1,0,0] neg_hi:[1,0,0]
	v_pk_fma_f32 v[12:13], v[18:19], v[12:13], 0 op_sel_hi:[0,1,0] neg_lo:[1,0,0] neg_hi:[1,0,0]
	v_cvt_pk_bf16_f32 v10, v10, v11
	v_cvt_pk_bf16_f32 v11, v12, v13
	ds_write_b64 v186, v[10:11] offset:3264
	ds_read_b32 v10, v187 offset:184
	s_waitcnt lgkmcnt(0)
	v_pk_fma_f32 v[2:3], v[10:11], v[2:3], 0 op_sel_hi:[0,1,0] neg_lo:[1,0,0] neg_hi:[1,0,0]
	v_pk_fma_f32 v[4:5], v[10:11], v[4:5], 0 op_sel_hi:[0,1,0] neg_lo:[1,0,0] neg_hi:[1,0,0]
	v_cvt_pk_bf16_f32 v2, v2, v3
	v_cvt_pk_bf16_f32 v3, v4, v5
	ds_write_b64 v186, v[2:3] offset:3808
	ds_read_b128 a[128:131], v1
	ds_read_b128 a[132:135], v1 offset:64
	ds_read_b128 a[136:139], v1 offset:128
	ds_read_b128 a[140:143], v1 offset:192
	v_lshl_add_u64 v[2:3], v[168:169], 0, s[24:25]
	v_lshl_add_u64 v[4:5], v[170:171], 0, s[24:25]
	v_lshl_add_u64 v[10:11], v[172:173], 0, s[24:25]
	v_lshl_add_u64 v[12:13], v[174:175], 0, s[24:25]
	v_lshl_add_u64 v[18:19], v[176:177], 0, s[24:25]
	v_lshl_add_u64 v[20:21], v[178:179], 0, s[24:25]
	v_lshl_add_u64 v[50:51], v[180:181], 0, s[24:25]
	v_lshl_add_u64 v[52:53], v[182:183], 0, s[24:25]
	global_load_dwordx4 v[114:117], v[2:3], off nt
	global_load_dwordx4 v[94:97], v[4:5], off nt
	global_load_dwordx4 v[82:85], v[10:11], off nt
	global_load_dwordx4 v[62:65], v[12:13], off nt
	global_load_dwordx4 v[38:41], v[18:19], off nt
	global_load_dwordx4 v[26:29], v[20:21], off nt
	s_nop 0
	global_load_dwordx4 v[10:13], v[50:51], off nt
	global_load_dwordx4 v[2:5], v[52:53], off nt
	v_mov_b32_e32 v18, v195
	s_waitcnt vmcnt(23)
	s_waitcnt vmcnt(22)
	s_waitcnt vmcnt(21)
	s_waitcnt vmcnt(20)
	s_waitcnt vmcnt(19)
	s_waitcnt vmcnt(18)
	s_waitcnt vmcnt(17)
	s_waitcnt vmcnt(16)
	ds_read_b32 v18, v187
	s_waitcnt lgkmcnt(0)
	v_pk_fma_f32 v[20:21], v[18:19], v[102:103], 0 op_sel_hi:[0,1,0] neg_lo:[1,0,0] neg_hi:[1,0,0]
	v_pk_fma_f32 v[18:19], v[18:19], v[104:105], 0 op_sel_hi:[0,1,0] neg_lo:[1,0,0] neg_hi:[1,0,0]
	v_cvt_pk_bf16_f32 v20, v20, v21
	v_cvt_pk_bf16_f32 v21, v18, v19
	ds_write_b64 v186, v[20:21]
	ds_read_b32 v18, v187 offset:8
	s_waitcnt lgkmcnt(0)
	v_pk_fma_f32 v[20:21], v[18:19], v[90:91], 0 op_sel_hi:[0,1,0] neg_lo:[1,0,0] neg_hi:[1,0,0]
	v_pk_fma_f32 v[18:19], v[18:19], v[92:93], 0 op_sel_hi:[0,1,0] neg_lo:[1,0,0] neg_hi:[1,0,0]
	v_cvt_pk_bf16_f32 v20, v20, v21
	v_cvt_pk_bf16_f32 v21, v18, v19
	ds_write_b64 v186, v[20:21] offset:544
	ds_read_b32 v18, v187 offset:16
	s_waitcnt lgkmcnt(0)
	v_pk_fma_f32 v[20:21], v[18:19], v[86:87], 0 op_sel_hi:[0,1,0] neg_lo:[1,0,0] neg_hi:[1,0,0]
	v_pk_fma_f32 v[18:19], v[18:19], v[88:89], 0 op_sel_hi:[0,1,0] neg_lo:[1,0,0] neg_hi:[1,0,0]
	v_cvt_pk_bf16_f32 v20, v20, v21
	v_cvt_pk_bf16_f32 v21, v18, v19
	ds_write_b64 v186, v[20:21] offset:1088
	ds_read_b32 v18, v187 offset:24
	s_waitcnt lgkmcnt(0)
	v_pk_fma_f32 v[20:21], v[18:19], v[70:71], 0 op_sel_hi:[0,1,0] neg_lo:[1,0,0] neg_hi:[1,0,0]
	v_pk_fma_f32 v[18:19], v[18:19], v[72:73], 0 op_sel_hi:[0,1,0] neg_lo:[1,0,0] neg_hi:[1,0,0]
	v_cvt_pk_bf16_f32 v20, v20, v21
	v_cvt_pk_bf16_f32 v21, v18, v19
	ds_write_b64 v186, v[20:21] offset:1632
	ds_read_b32 v18, v187 offset:32
	s_waitcnt lgkmcnt(0)
	v_pk_fma_f32 v[20:21], v[18:19], v[66:67], 0 op_sel_hi:[0,1,0] neg_lo:[1,0,0] neg_hi:[1,0,0]
	v_pk_fma_f32 v[18:19], v[18:19], v[68:69], 0 op_sel_hi:[0,1,0] neg_lo:[1,0,0] neg_hi:[1,0,0]
	v_cvt_pk_bf16_f32 v20, v20, v21
	v_cvt_pk_bf16_f32 v21, v18, v19
	ds_write_b64 v186, v[20:21] offset:2176
	ds_read_b32 v18, v187 offset:40
	s_waitcnt lgkmcnt(0)
	v_pk_fma_f32 v[20:21], v[18:19], v[46:47], 0 op_sel_hi:[0,1,0] neg_lo:[1,0,0] neg_hi:[1,0,0]
	v_pk_fma_f32 v[18:19], v[18:19], v[48:49], 0 op_sel_hi:[0,1,0] neg_lo:[1,0,0] neg_hi:[1,0,0]
	v_cvt_pk_bf16_f32 v20, v20, v21
	v_cvt_pk_bf16_f32 v21, v18, v19
	ds_write_b64 v186, v[20:21] offset:2720
	ds_read_b32 v18, v187 offset:48
	s_waitcnt lgkmcnt(0)
	v_pk_fma_f32 v[20:21], v[18:19], v[42:43], 0 op_sel_hi:[0,1,0] neg_lo:[1,0,0] neg_hi:[1,0,0]
	v_pk_fma_f32 v[18:19], v[18:19], v[44:45], 0 op_sel_hi:[0,1,0] neg_lo:[1,0,0] neg_hi:[1,0,0]
	v_cvt_pk_bf16_f32 v20, v20, v21
	v_cvt_pk_bf16_f32 v21, v18, v19
	ds_write_b64 v186, v[20:21] offset:3264
	ds_read_b32 v18, v187 offset:56
	s_waitcnt lgkmcnt(0)
	v_pk_fma_f32 v[20:21], v[18:19], v[30:31], 0 op_sel_hi:[0,1,0] neg_lo:[1,0,0] neg_hi:[1,0,0]
	v_pk_fma_f32 v[18:19], v[18:19], v[32:33], 0 op_sel_hi:[0,1,0] neg_lo:[1,0,0] neg_hi:[1,0,0]
	v_cvt_pk_bf16_f32 v20, v20, v21
	v_cvt_pk_bf16_f32 v21, v18, v19
	ds_write_b64 v186, v[20:21] offset:3808
	ds_read_b128 a[144:147], v1
	ds_read_b128 a[148:151], v1 offset:64
	ds_read_b128 a[152:155], v1 offset:128
	ds_read_b128 a[156:159], v1 offset:192
	v_lshl_add_u64 v[18:19], v[130:131], 0, s[22:23]
	v_add_co_u32_e32 v20, vcc, s7, v18
	s_nop 1
	v_addc_co_u32_e32 v21, vcc, 0, v19, vcc
	global_load_dwordx4 v[106:109], v[18:19], off nt
	global_load_dwordx4 v[90:93], v[20:21], off nt
	v_add_co_u32_e32 v20, vcc, s36, v18
	s_nop 1
	v_addc_co_u32_e32 v21, vcc, 0, v19, vcc
	v_add_co_u32_e32 v30, vcc, s37, v18
	s_nop 1
	v_addc_co_u32_e32 v31, vcc, 0, v19, vcc
	global_load_dwordx4 v[86:89], v[20:21], off nt
	global_load_dwordx4 v[74:77], v[30:31], off nt
	v_add_co_u32_e32 v20, vcc, s38, v18
	s_nop 1
	v_addc_co_u32_e32 v21, vcc, 0, v19, vcc
	v_add_co_u32_e32 v30, vcc, s39, v18
	s_nop 1
	v_addc_co_u32_e32 v31, vcc, 0, v19, vcc
	global_load_dwordx4 v[70:73], v[20:21], off nt
	global_load_dwordx4 v[54:57], v[30:31], off nt
	v_add_co_u32_e32 v20, vcc, s41, v18
	s_nop 1
	v_addc_co_u32_e32 v21, vcc, 0, v19, vcc
	v_add_co_u32_e32 v18, vcc, s42, v18
	s_nop 1
	v_addc_co_u32_e32 v19, vcc, 0, v19, vcc
	global_load_dwordx4 v[50:53], v[20:21], off nt
	global_load_dwordx4 v[46:49], v[18:19], off nt
	v_mov_b32_e32 v18, v195
	s_waitcnt vmcnt(23)
	s_waitcnt vmcnt(22)
	s_waitcnt vmcnt(21)
	s_waitcnt vmcnt(20)
	s_waitcnt vmcnt(19)
	s_waitcnt vmcnt(18)
	s_waitcnt vmcnt(17)
	s_waitcnt vmcnt(16)
	ds_read_b32 v18, v187 offset:64
	s_waitcnt lgkmcnt(0)
	v_pk_fma_f32 v[20:21], v[18:19], v[110:111], 0 op_sel_hi:[0,1,0] neg_lo:[1,0,0] neg_hi:[1,0,0]
	v_pk_fma_f32 v[18:19], v[18:19], v[112:113], 0 op_sel_hi:[0,1,0] neg_lo:[1,0,0] neg_hi:[1,0,0]
	v_cvt_pk_bf16_f32 v20, v20, v21
	v_cvt_pk_bf16_f32 v21, v18, v19
	ds_write_b64 v186, v[20:21]
	ds_read_b32 v18, v187 offset:72
	s_waitcnt lgkmcnt(0)
	v_pk_fma_f32 v[20:21], v[18:19], v[98:99], 0 op_sel_hi:[0,1,0] neg_lo:[1,0,0] neg_hi:[1,0,0]
	v_pk_fma_f32 v[18:19], v[18:19], v[100:101], 0 op_sel_hi:[0,1,0] neg_lo:[1,0,0] neg_hi:[1,0,0]
	v_cvt_pk_bf16_f32 v20, v20, v21
	v_cvt_pk_bf16_f32 v21, v18, v19
	ds_write_b64 v186, v[20:21] offset:544
	ds_read_b32 v18, v187 offset:80
	s_waitcnt lgkmcnt(0)
	v_pk_fma_f32 v[20:21], v[18:19], v[78:79], 0 op_sel_hi:[0,1,0] neg_lo:[1,0,0] neg_hi:[1,0,0]
	v_pk_fma_f32 v[18:19], v[18:19], v[80:81], 0 op_sel_hi:[0,1,0] neg_lo:[1,0,0] neg_hi:[1,0,0]
	v_cvt_pk_bf16_f32 v20, v20, v21
	v_cvt_pk_bf16_f32 v21, v18, v19
	ds_write_b64 v186, v[20:21] offset:1088
	ds_read_b32 v18, v187 offset:88
	s_waitcnt lgkmcnt(0)
	v_pk_fma_f32 v[20:21], v[18:19], v[58:59], 0 op_sel_hi:[0,1,0] neg_lo:[1,0,0] neg_hi:[1,0,0]
	v_pk_fma_f32 v[18:19], v[18:19], v[60:61], 0 op_sel_hi:[0,1,0] neg_lo:[1,0,0] neg_hi:[1,0,0]
	v_cvt_pk_bf16_f32 v20, v20, v21
	v_cvt_pk_bf16_f32 v21, v18, v19
	ds_write_b64 v186, v[20:21] offset:1632
	ds_read_b32 v18, v187 offset:96
	s_waitcnt lgkmcnt(0)
	v_pk_fma_f32 v[20:21], v[18:19], v[34:35], 0 op_sel_hi:[0,1,0] neg_lo:[1,0,0] neg_hi:[1,0,0]
	v_pk_fma_f32 v[18:19], v[18:19], v[36:37], 0 op_sel_hi:[0,1,0] neg_lo:[1,0,0] neg_hi:[1,0,0]
	v_cvt_pk_bf16_f32 v20, v20, v21
	v_cvt_pk_bf16_f32 v21, v18, v19
	ds_write_b64 v186, v[20:21] offset:2176
	ds_read_b32 v18, v187 offset:104
	s_waitcnt lgkmcnt(0)
	v_pk_fma_f32 v[20:21], v[18:19], v[22:23], 0 op_sel_hi:[0,1,0] neg_lo:[1,0,0] neg_hi:[1,0,0]
	v_pk_fma_f32 v[18:19], v[18:19], v[24:25], 0 op_sel_hi:[0,1,0] neg_lo:[1,0,0] neg_hi:[1,0,0]
	v_cvt_pk_bf16_f32 v20, v20, v21
	v_cvt_pk_bf16_f32 v21, v18, v19
	ds_write_b64 v186, v[20:21] offset:2720
	ds_read_b32 v18, v187 offset:112
	s_waitcnt lgkmcnt(0)
	v_pk_fma_f32 v[14:15], v[18:19], v[14:15], 0 op_sel_hi:[0,1,0] neg_lo:[1,0,0] neg_hi:[1,0,0]
	v_pk_fma_f32 v[16:17], v[18:19], v[16:17], 0 op_sel_hi:[0,1,0] neg_lo:[1,0,0] neg_hi:[1,0,0]
	v_cvt_pk_bf16_f32 v14, v14, v15
	v_cvt_pk_bf16_f32 v15, v16, v17
	ds_write_b64 v186, v[14:15] offset:3264
	ds_read_b32 v14, v187 offset:120
	s_waitcnt lgkmcnt(0)
	v_pk_fma_f32 v[6:7], v[14:15], v[6:7], 0 op_sel_hi:[0,1,0] neg_lo:[1,0,0] neg_hi:[1,0,0]
	v_pk_fma_f32 v[8:9], v[14:15], v[8:9], 0 op_sel_hi:[0,1,0] neg_lo:[1,0,0] neg_hi:[1,0,0]
	v_cvt_pk_bf16_f32 v6, v6, v7
	v_cvt_pk_bf16_f32 v7, v8, v9
	ds_write_b64 v186, v[6:7] offset:3808
	ds_read_b128 a[160:163], v1
	ds_read_b128 a[164:167], v1 offset:64
	ds_read_b128 a[168:171], v1 offset:128
	ds_read_b128 a[172:175], v1 offset:192
	v_lshl_add_u64 v[6:7], v[150:151], 0, s[22:23]
	v_lshl_add_u64 v[18:19], v[160:161], 0, s[22:23]
	v_lshl_add_u64 v[20:21], v[162:163], 0, s[22:23]
	v_lshl_add_u64 v[22:23], v[164:165], 0, s[22:23]
	v_lshl_add_u64 v[8:9], v[152:153], 0, s[22:23]
	v_lshl_add_u64 v[14:15], v[156:157], 0, s[22:23]
	v_lshl_add_u64 v[16:17], v[158:159], 0, s[22:23]
	v_lshl_add_u64 v[34:35], v[166:167], 0, s[22:23]
	global_load_dwordx4 v[110:113], v[6:7], off nt
	global_load_dwordx4 v[98:101], v[8:9], off nt
	global_load_dwordx4 v[78:81], v[14:15], off nt
	global_load_dwordx4 v[66:69], v[16:17], off nt
	global_load_dwordx4 v[58:61], v[18:19], off nt
	global_load_dwordx4 v[30:33], v[20:21], off nt
	s_nop 0
	global_load_dwordx4 v[22:25], v[22:23], off nt
	s_nop 0
	global_load_dwordx4 v[18:21], v[34:35], off nt
	s_waitcnt vmcnt(23)
	s_waitcnt vmcnt(22)
	s_waitcnt vmcnt(21)
	s_waitcnt vmcnt(20)
	s_waitcnt vmcnt(19)
	s_waitcnt vmcnt(18)
	s_waitcnt vmcnt(17)
	s_waitcnt vmcnt(16)
	ds_read_b32 v6, v187 offset:128
	s_waitcnt lgkmcnt(0)
	v_pk_fma_f32 v[8:9], v[6:7], v[114:115], 0 op_sel_hi:[0,1,0] neg_lo:[1,0,0] neg_hi:[1,0,0]
	v_pk_fma_f32 v[6:7], v[6:7], v[116:117], 0 op_sel_hi:[0,1,0] neg_lo:[1,0,0] neg_hi:[1,0,0]
	v_cvt_pk_bf16_f32 v8, v8, v9
	v_cvt_pk_bf16_f32 v9, v6, v7
	ds_write_b64 v186, v[8:9]
	ds_read_b32 v6, v187 offset:136
	s_waitcnt lgkmcnt(0)
	v_pk_fma_f32 v[8:9], v[6:7], v[94:95], 0 op_sel_hi:[0,1,0] neg_lo:[1,0,0] neg_hi:[1,0,0]
	v_pk_fma_f32 v[6:7], v[6:7], v[96:97], 0 op_sel_hi:[0,1,0] neg_lo:[1,0,0] neg_hi:[1,0,0]
	v_cvt_pk_bf16_f32 v8, v8, v9
	v_cvt_pk_bf16_f32 v9, v6, v7
	ds_write_b64 v186, v[8:9] offset:544
	ds_read_b32 v6, v187 offset:144
	s_waitcnt lgkmcnt(0)
	v_pk_fma_f32 v[8:9], v[6:7], v[82:83], 0 op_sel_hi:[0,1,0] neg_lo:[1,0,0] neg_hi:[1,0,0]
	v_pk_fma_f32 v[6:7], v[6:7], v[84:85], 0 op_sel_hi:[0,1,0] neg_lo:[1,0,0] neg_hi:[1,0,0]
	v_cvt_pk_bf16_f32 v8, v8, v9
	v_cvt_pk_bf16_f32 v9, v6, v7
	ds_write_b64 v186, v[8:9] offset:1088
	ds_read_b32 v6, v187 offset:152
	s_waitcnt lgkmcnt(0)
	v_pk_fma_f32 v[8:9], v[6:7], v[62:63], 0 op_sel_hi:[0,1,0] neg_lo:[1,0,0] neg_hi:[1,0,0]
	v_pk_fma_f32 v[6:7], v[6:7], v[64:65], 0 op_sel_hi:[0,1,0] neg_lo:[1,0,0] neg_hi:[1,0,0]
	v_cvt_pk_bf16_f32 v8, v8, v9
	v_cvt_pk_bf16_f32 v9, v6, v7
	ds_write_b64 v186, v[8:9] offset:1632
	ds_read_b32 v6, v187 offset:160
	s_waitcnt lgkmcnt(0)
	v_pk_fma_f32 v[8:9], v[6:7], v[38:39], 0 op_sel_hi:[0,1,0] neg_lo:[1,0,0] neg_hi:[1,0,0]
	v_pk_fma_f32 v[6:7], v[6:7], v[40:41], 0 op_sel_hi:[0,1,0] neg_lo:[1,0,0] neg_hi:[1,0,0]
	v_cvt_pk_bf16_f32 v8, v8, v9
	v_cvt_pk_bf16_f32 v9, v6, v7
	ds_write_b64 v186, v[8:9] offset:2176
	ds_read_b32 v6, v187 offset:168
	s_waitcnt lgkmcnt(0)
	v_pk_fma_f32 v[8:9], v[6:7], v[26:27], 0 op_sel_hi:[0,1,0] neg_lo:[1,0,0] neg_hi:[1,0,0]
	v_pk_fma_f32 v[6:7], v[6:7], v[28:29], 0 op_sel_hi:[0,1,0] neg_lo:[1,0,0] neg_hi:[1,0,0]
	v_cvt_pk_bf16_f32 v8, v8, v9
	v_cvt_pk_bf16_f32 v9, v6, v7
	ds_write_b64 v186, v[8:9] offset:2720
	ds_read_b32 v6, v187 offset:176
	s_waitcnt lgkmcnt(0)
	v_pk_fma_f32 v[8:9], v[6:7], v[10:11], 0 op_sel_hi:[0,1,0] neg_lo:[1,0,0] neg_hi:[1,0,0]
	v_pk_fma_f32 v[6:7], v[6:7], v[12:13], 0 op_sel_hi:[0,1,0] neg_lo:[1,0,0] neg_hi:[1,0,0]
	v_cvt_pk_bf16_f32 v8, v8, v9
	v_cvt_pk_bf16_f32 v9, v6, v7
	ds_write_b64 v186, v[8:9] offset:3264
	ds_read_b32 v6, v187 offset:184
	s_waitcnt lgkmcnt(0)
	v_pk_fma_f32 v[2:3], v[6:7], v[2:3], 0 op_sel_hi:[0,1,0] neg_lo:[1,0,0] neg_hi:[1,0,0]
	v_pk_fma_f32 v[4:5], v[6:7], v[4:5], 0 op_sel_hi:[0,1,0] neg_lo:[1,0,0] neg_hi:[1,0,0]
	v_cvt_pk_bf16_f32 v2, v2, v3
	v_cvt_pk_bf16_f32 v3, v4, v5
	ds_write_b64 v186, v[2:3] offset:3808
	ds_read_b128 a[176:179], v1
	ds_read_b128 a[180:183], v1 offset:64
	ds_read_b128 a[184:187], v1 offset:128
	ds_read_b128 a[188:191], v1 offset:192
	v_lshl_add_u64 v[2:3], v[168:169], 0, s[22:23]
	v_lshl_add_u64 v[4:5], v[170:171], 0, s[22:23]
	v_lshl_add_u64 v[6:7], v[172:173], 0, s[22:23]
	v_lshl_add_u64 v[8:9], v[174:175], 0, s[22:23]
	v_lshl_add_u64 v[10:11], v[176:177], 0, s[22:23]
	v_lshl_add_u64 v[12:13], v[178:179], 0, s[22:23]
	v_lshl_add_u64 v[14:15], v[180:181], 0, s[22:23]
	v_lshl_add_u64 v[16:17], v[182:183], 0, s[22:23]
	global_load_dwordx4 v[114:117], v[2:3], off nt
	global_load_dwordx4 v[102:105], v[4:5], off nt
	global_load_dwordx4 v[94:97], v[6:7], off nt
	global_load_dwordx4 v[82:85], v[8:9], off nt
	global_load_dwordx4 v[62:65], v[10:11], off nt
	global_load_dwordx4 v[42:45], v[12:13], off nt
	global_load_dwordx4 v[38:41], v[14:15], off nt
	global_load_dwordx4 v[34:37], v[16:17], off nt
	v_mov_b32_e32 v2, v194
	s_waitcnt vmcnt(23)
	s_waitcnt vmcnt(22)
	s_waitcnt vmcnt(21)
	s_waitcnt vmcnt(20)
	s_waitcnt vmcnt(19)
	s_waitcnt vmcnt(18)
	s_waitcnt vmcnt(17)
	s_waitcnt vmcnt(16)
	ds_read_b32 v2, v187
	s_waitcnt lgkmcnt(0)
	v_pk_fma_f32 v[4:5], v[2:3], v[106:107], 0 op_sel_hi:[0,1,0] neg_lo:[1,0,0] neg_hi:[1,0,0]
	v_pk_fma_f32 v[2:3], v[2:3], v[108:109], 0 op_sel_hi:[0,1,0] neg_lo:[1,0,0] neg_hi:[1,0,0]
	v_cvt_pk_bf16_f32 v4, v4, v5
	v_cvt_pk_bf16_f32 v5, v2, v3
	ds_write_b64 v186, v[4:5]
	ds_read_b32 v2, v187 offset:8
	s_waitcnt lgkmcnt(0)
	v_pk_fma_f32 v[4:5], v[2:3], v[90:91], 0 op_sel_hi:[0,1,0] neg_lo:[1,0,0] neg_hi:[1,0,0]
	v_pk_fma_f32 v[2:3], v[2:3], v[92:93], 0 op_sel_hi:[0,1,0] neg_lo:[1,0,0] neg_hi:[1,0,0]
	v_cvt_pk_bf16_f32 v4, v4, v5
	v_cvt_pk_bf16_f32 v5, v2, v3
	ds_write_b64 v186, v[4:5] offset:544
	ds_read_b32 v2, v187 offset:16
	s_waitcnt lgkmcnt(0)
	v_pk_fma_f32 v[4:5], v[2:3], v[86:87], 0 op_sel_hi:[0,1,0] neg_lo:[1,0,0] neg_hi:[1,0,0]
	v_pk_fma_f32 v[2:3], v[2:3], v[88:89], 0 op_sel_hi:[0,1,0] neg_lo:[1,0,0] neg_hi:[1,0,0]
	v_cvt_pk_bf16_f32 v4, v4, v5
	v_cvt_pk_bf16_f32 v5, v2, v3
	ds_write_b64 v186, v[4:5] offset:1088
	ds_read_b32 v2, v187 offset:24
	s_waitcnt lgkmcnt(0)
	v_pk_fma_f32 v[4:5], v[2:3], v[74:75], 0 op_sel_hi:[0,1,0] neg_lo:[1,0,0] neg_hi:[1,0,0]
	v_pk_fma_f32 v[2:3], v[2:3], v[76:77], 0 op_sel_hi:[0,1,0] neg_lo:[1,0,0] neg_hi:[1,0,0]
	v_cvt_pk_bf16_f32 v4, v4, v5
	v_cvt_pk_bf16_f32 v5, v2, v3
	ds_write_b64 v186, v[4:5] offset:1632
	ds_read_b32 v2, v187 offset:32
	s_waitcnt lgkmcnt(0)
	v_pk_fma_f32 v[4:5], v[2:3], v[70:71], 0 op_sel_hi:[0,1,0] neg_lo:[1,0,0] neg_hi:[1,0,0]
	v_pk_fma_f32 v[2:3], v[2:3], v[72:73], 0 op_sel_hi:[0,1,0] neg_lo:[1,0,0] neg_hi:[1,0,0]
	v_cvt_pk_bf16_f32 v4, v4, v5
	v_cvt_pk_bf16_f32 v5, v2, v3
	ds_write_b64 v186, v[4:5] offset:2176
	ds_read_b32 v2, v187 offset:40
	s_waitcnt lgkmcnt(0)
	v_pk_fma_f32 v[4:5], v[2:3], v[54:55], 0 op_sel_hi:[0,1,0] neg_lo:[1,0,0] neg_hi:[1,0,0]
	v_pk_fma_f32 v[2:3], v[2:3], v[56:57], 0 op_sel_hi:[0,1,0] neg_lo:[1,0,0] neg_hi:[1,0,0]
	v_cvt_pk_bf16_f32 v4, v4, v5
	v_cvt_pk_bf16_f32 v5, v2, v3
	ds_write_b64 v186, v[4:5] offset:2720
	ds_read_b32 v2, v187 offset:48
	s_waitcnt lgkmcnt(0)
	v_pk_fma_f32 v[4:5], v[2:3], v[50:51], 0 op_sel_hi:[0,1,0] neg_lo:[1,0,0] neg_hi:[1,0,0]
	v_pk_fma_f32 v[2:3], v[2:3], v[52:53], 0 op_sel_hi:[0,1,0] neg_lo:[1,0,0] neg_hi:[1,0,0]
	v_cvt_pk_bf16_f32 v4, v4, v5
	v_cvt_pk_bf16_f32 v5, v2, v3
	ds_write_b64 v186, v[4:5] offset:3264
	ds_read_b32 v2, v187 offset:56
	s_waitcnt lgkmcnt(0)
	v_pk_fma_f32 v[4:5], v[2:3], v[46:47], 0 op_sel_hi:[0,1,0] neg_lo:[1,0,0] neg_hi:[1,0,0]
	v_pk_fma_f32 v[2:3], v[2:3], v[48:49], 0 op_sel_hi:[0,1,0] neg_lo:[1,0,0] neg_hi:[1,0,0]
	v_cvt_pk_bf16_f32 v4, v4, v5
	v_cvt_pk_bf16_f32 v5, v2, v3
	ds_write_b64 v186, v[4:5] offset:3808
	ds_read_b128 a[192:195], v1
	ds_read_b128 a[196:199], v1 offset:64
	ds_read_b128 a[200:203], v1 offset:128
	ds_read_b128 a[204:207], v1 offset:192
	v_lshl_add_u64 v[118:119], v[130:131], 0, s[20:21]
	v_add_co_u32_e32 v126, vcc, s7, v118
	s_nop 1
	v_addc_co_u32_e32 v127, vcc, 0, v119, vcc
	v_add_co_u32_e32 v128, vcc, s36, v118
	global_load_dwordx4 v[90:93], v[118:119], off nt
	global_load_dwordx4 v[86:89], v[126:127], off nt
	v_addc_co_u32_e32 v129, vcc, 0, v119, vcc
	v_add_co_u32_e32 v134, vcc, s37, v118
	s_nop 1
	v_addc_co_u32_e32 v135, vcc, 0, v119, vcc
	v_add_co_u32_e32 v136, vcc, s38, v118
	global_load_dwordx4 v[54:57], v[128:129], off nt
	global_load_dwordx4 v[50:53], v[134:135], off nt
	v_addc_co_u32_e32 v137, vcc, 0, v119, vcc
	v_add_co_u32_e32 v138, vcc, s39, v118
	s_nop 1
	v_addc_co_u32_e32 v139, vcc, 0, v119, vcc
	v_add_co_u32_e32 v140, vcc, s41, v118
	global_load_dwordx4 v[14:17], v[136:137], off nt
	global_load_dwordx4 v[10:13], v[138:139], off nt
	v_addc_co_u32_e32 v141, vcc, 0, v119, vcc
	v_add_co_u32_e32 v142, vcc, s42, v118
	s_nop 1
	v_addc_co_u32_e32 v143, vcc, 0, v119, vcc
	global_load_dwordx4 v[6:9], v[140:141], off nt
	global_load_dwordx4 v[2:5], v[142:143], off nt
	v_mov_b32_e32 v26, v194
	s_waitcnt vmcnt(23)
	s_waitcnt vmcnt(22)
	s_waitcnt vmcnt(21)
	s_waitcnt vmcnt(20)
	s_waitcnt vmcnt(19)
	s_waitcnt vmcnt(18)
	s_waitcnt vmcnt(17)
	s_waitcnt vmcnt(16)
	ds_read_b32 v26, v187 offset:64
	s_waitcnt lgkmcnt(0)
	v_pk_fma_f32 v[28:29], v[26:27], v[110:111], 0 op_sel_hi:[0,1,0] neg_lo:[1,0,0] neg_hi:[1,0,0]
	v_pk_fma_f32 v[26:27], v[26:27], v[112:113], 0 op_sel_hi:[0,1,0] neg_lo:[1,0,0] neg_hi:[1,0,0]
	v_cvt_pk_bf16_f32 v28, v28, v29
	v_cvt_pk_bf16_f32 v29, v26, v27
	ds_write_b64 v186, v[28:29]
	ds_read_b32 v26, v187 offset:72
	s_waitcnt lgkmcnt(0)
	v_pk_fma_f32 v[28:29], v[26:27], v[98:99], 0 op_sel_hi:[0,1,0] neg_lo:[1,0,0] neg_hi:[1,0,0]
	v_pk_fma_f32 v[26:27], v[26:27], v[100:101], 0 op_sel_hi:[0,1,0] neg_lo:[1,0,0] neg_hi:[1,0,0]
	v_cvt_pk_bf16_f32 v28, v28, v29
	v_cvt_pk_bf16_f32 v29, v26, v27
	ds_write_b64 v186, v[28:29] offset:544
	ds_read_b32 v26, v187 offset:80
	s_waitcnt lgkmcnt(0)
	v_pk_fma_f32 v[28:29], v[26:27], v[78:79], 0 op_sel_hi:[0,1,0] neg_lo:[1,0,0] neg_hi:[1,0,0]
	v_pk_fma_f32 v[26:27], v[26:27], v[80:81], 0 op_sel_hi:[0,1,0] neg_lo:[1,0,0] neg_hi:[1,0,0]
	v_cvt_pk_bf16_f32 v28, v28, v29
	v_cvt_pk_bf16_f32 v29, v26, v27
	ds_write_b64 v186, v[28:29] offset:1088
	ds_read_b32 v26, v187 offset:88
	s_waitcnt lgkmcnt(0)
	v_pk_fma_f32 v[28:29], v[26:27], v[66:67], 0 op_sel_hi:[0,1,0] neg_lo:[1,0,0] neg_hi:[1,0,0]
	v_pk_fma_f32 v[26:27], v[26:27], v[68:69], 0 op_sel_hi:[0,1,0] neg_lo:[1,0,0] neg_hi:[1,0,0]
	v_cvt_pk_bf16_f32 v28, v28, v29
	v_cvt_pk_bf16_f32 v29, v26, v27
	ds_write_b64 v186, v[28:29] offset:1632
	ds_read_b32 v26, v187 offset:96
	s_waitcnt lgkmcnt(0)
	v_pk_fma_f32 v[28:29], v[26:27], v[58:59], 0 op_sel_hi:[0,1,0] neg_lo:[1,0,0] neg_hi:[1,0,0]
	v_pk_fma_f32 v[26:27], v[26:27], v[60:61], 0 op_sel_hi:[0,1,0] neg_lo:[1,0,0] neg_hi:[1,0,0]
	v_cvt_pk_bf16_f32 v28, v28, v29
	v_cvt_pk_bf16_f32 v29, v26, v27
	ds_write_b64 v186, v[28:29] offset:2176
	ds_read_b32 v26, v187 offset:104
	s_waitcnt lgkmcnt(0)
	v_pk_fma_f32 v[28:29], v[26:27], v[30:31], 0 op_sel_hi:[0,1,0] neg_lo:[1,0,0] neg_hi:[1,0,0]
	v_pk_fma_f32 v[26:27], v[26:27], v[32:33], 0 op_sel_hi:[0,1,0] neg_lo:[1,0,0] neg_hi:[1,0,0]
	v_cvt_pk_bf16_f32 v28, v28, v29
	v_cvt_pk_bf16_f32 v29, v26, v27
	ds_write_b64 v186, v[28:29] offset:2720
	ds_read_b32 v26, v187 offset:112
	s_waitcnt lgkmcnt(0)
	v_pk_fma_f32 v[22:23], v[26:27], v[22:23], 0 op_sel_hi:[0,1,0] neg_lo:[1,0,0] neg_hi:[1,0,0]
	v_pk_fma_f32 v[24:25], v[26:27], v[24:25], 0 op_sel_hi:[0,1,0] neg_lo:[1,0,0] neg_hi:[1,0,0]
	v_cvt_pk_bf16_f32 v22, v22, v23
	v_cvt_pk_bf16_f32 v23, v24, v25
	ds_write_b64 v186, v[22:23] offset:3264
	ds_read_b32 v22, v187 offset:120
	s_waitcnt lgkmcnt(0)
	v_pk_fma_f32 v[18:19], v[22:23], v[18:19], 0 op_sel_hi:[0,1,0] neg_lo:[1,0,0] neg_hi:[1,0,0]
	v_pk_fma_f32 v[20:21], v[22:23], v[20:21], 0 op_sel_hi:[0,1,0] neg_lo:[1,0,0] neg_hi:[1,0,0]
	v_cvt_pk_bf16_f32 v18, v18, v19
	v_cvt_pk_bf16_f32 v19, v20, v21
	ds_write_b64 v186, v[18:19] offset:3808
	ds_read_b128 a[208:211], v1
	ds_read_b128 a[212:215], v1 offset:64
	ds_read_b128 a[216:219], v1 offset:128
	ds_read_b128 a[220:223], v1 offset:192
	v_lshl_add_u64 v[18:19], v[150:151], 0, s[20:21]
	v_lshl_add_u64 v[20:21], v[152:153], 0, s[20:21]
	v_lshl_add_u64 v[22:23], v[156:157], 0, s[20:21]
	v_lshl_add_u64 v[24:25], v[158:159], 0, s[20:21]
	v_lshl_add_u64 v[26:27], v[160:161], 0, s[20:21]
	v_lshl_add_u64 v[28:29], v[162:163], 0, s[20:21]
	v_lshl_add_u64 v[46:47], v[164:165], 0, s[20:21]
	v_lshl_add_u64 v[48:49], v[166:167], 0, s[20:21]
	global_load_dwordx4 v[78:81], v[18:19], off nt
	global_load_dwordx4 v[74:77], v[20:21], off nt
	global_load_dwordx4 v[70:73], v[22:23], off nt
	global_load_dwordx4 v[66:69], v[24:25], off nt
	global_load_dwordx4 v[30:33], v[26:27], off nt
	s_nop 0
	global_load_dwordx4 v[26:29], v[28:29], off nt
	s_nop 0
	global_load_dwordx4 v[22:25], v[46:47], off nt
	global_load_dwordx4 v[18:21], v[48:49], off nt
	s_waitcnt vmcnt(23)
	s_waitcnt vmcnt(22)
	s_waitcnt vmcnt(21)
	s_waitcnt vmcnt(20)
	s_waitcnt vmcnt(19)
	s_waitcnt vmcnt(18)
	s_waitcnt vmcnt(17)
	s_waitcnt vmcnt(16)
	ds_read_b32 v46, v187 offset:128
	s_waitcnt lgkmcnt(0)
	v_pk_fma_f32 v[48:49], v[46:47], v[114:115], 0 op_sel_hi:[0,1,0] neg_lo:[1,0,0] neg_hi:[1,0,0]
	v_pk_fma_f32 v[46:47], v[46:47], v[116:117], 0 op_sel_hi:[0,1,0] neg_lo:[1,0,0] neg_hi:[1,0,0]
	v_cvt_pk_bf16_f32 v48, v48, v49
	v_cvt_pk_bf16_f32 v49, v46, v47
	ds_write_b64 v186, v[48:49]
	ds_read_b32 v46, v187 offset:136
	s_waitcnt lgkmcnt(0)
	v_pk_fma_f32 v[48:49], v[46:47], v[102:103], 0 op_sel_hi:[0,1,0] neg_lo:[1,0,0] neg_hi:[1,0,0]
	v_pk_fma_f32 v[46:47], v[46:47], v[104:105], 0 op_sel_hi:[0,1,0] neg_lo:[1,0,0] neg_hi:[1,0,0]
	v_cvt_pk_bf16_f32 v48, v48, v49
	v_cvt_pk_bf16_f32 v49, v46, v47
	ds_write_b64 v186, v[48:49] offset:544
	ds_read_b32 v46, v187 offset:144
	s_waitcnt lgkmcnt(0)
	v_pk_fma_f32 v[48:49], v[46:47], v[94:95], 0 op_sel_hi:[0,1,0] neg_lo:[1,0,0] neg_hi:[1,0,0]
	v_pk_fma_f32 v[46:47], v[46:47], v[96:97], 0 op_sel_hi:[0,1,0] neg_lo:[1,0,0] neg_hi:[1,0,0]
	v_cvt_pk_bf16_f32 v48, v48, v49
	v_cvt_pk_bf16_f32 v49, v46, v47
	ds_write_b64 v186, v[48:49] offset:1088
	ds_read_b32 v46, v187 offset:152
	s_waitcnt lgkmcnt(0)
	v_pk_fma_f32 v[48:49], v[46:47], v[82:83], 0 op_sel_hi:[0,1,0] neg_lo:[1,0,0] neg_hi:[1,0,0]
	v_pk_fma_f32 v[46:47], v[46:47], v[84:85], 0 op_sel_hi:[0,1,0] neg_lo:[1,0,0] neg_hi:[1,0,0]
	v_cvt_pk_bf16_f32 v48, v48, v49
	v_cvt_pk_bf16_f32 v49, v46, v47
	ds_write_b64 v186, v[48:49] offset:1632
	ds_read_b32 v46, v187 offset:160
	s_waitcnt lgkmcnt(0)
	v_pk_fma_f32 v[48:49], v[46:47], v[62:63], 0 op_sel_hi:[0,1,0] neg_lo:[1,0,0] neg_hi:[1,0,0]
	v_pk_fma_f32 v[46:47], v[46:47], v[64:65], 0 op_sel_hi:[0,1,0] neg_lo:[1,0,0] neg_hi:[1,0,0]
	v_cvt_pk_bf16_f32 v48, v48, v49
	v_cvt_pk_bf16_f32 v49, v46, v47
	ds_write_b64 v186, v[48:49] offset:2176
	ds_read_b32 v46, v187 offset:168
	s_waitcnt lgkmcnt(0)
	v_pk_fma_f32 v[42:43], v[46:47], v[42:43], 0 op_sel_hi:[0,1,0] neg_lo:[1,0,0] neg_hi:[1,0,0]
	v_pk_fma_f32 v[44:45], v[46:47], v[44:45], 0 op_sel_hi:[0,1,0] neg_lo:[1,0,0] neg_hi:[1,0,0]
	v_cvt_pk_bf16_f32 v42, v42, v43
	v_cvt_pk_bf16_f32 v43, v44, v45
	ds_write_b64 v186, v[42:43] offset:2720
	ds_read_b32 v42, v187 offset:176
	s_waitcnt lgkmcnt(0)
	v_pk_fma_f32 v[38:39], v[42:43], v[38:39], 0 op_sel_hi:[0,1,0] neg_lo:[1,0,0] neg_hi:[1,0,0]
	v_pk_fma_f32 v[40:41], v[42:43], v[40:41], 0 op_sel_hi:[0,1,0] neg_lo:[1,0,0] neg_hi:[1,0,0]
	v_cvt_pk_bf16_f32 v38, v38, v39
	v_cvt_pk_bf16_f32 v39, v40, v41
	ds_write_b64 v186, v[38:39] offset:3264
	ds_read_b32 v38, v187 offset:184
	s_waitcnt lgkmcnt(0)
	v_pk_fma_f32 v[34:35], v[38:39], v[34:35], 0 op_sel_hi:[0,1,0] neg_lo:[1,0,0] neg_hi:[1,0,0]
	v_pk_fma_f32 v[36:37], v[38:39], v[36:37], 0 op_sel_hi:[0,1,0] neg_lo:[1,0,0] neg_hi:[1,0,0]
	v_cvt_pk_bf16_f32 v34, v34, v35
	v_cvt_pk_bf16_f32 v35, v36, v37
	ds_write_b64 v186, v[34:35] offset:3808
	ds_read_b128 a[224:227], v1
	ds_read_b128 a[228:231], v1 offset:64
	ds_read_b128 a[232:235], v1 offset:128
	ds_read_b128 a[236:239], v1 offset:192
	v_lshl_add_u64 v[34:35], v[168:169], 0, s[20:21]
	v_lshl_add_u64 v[36:37], v[170:171], 0, s[20:21]
	v_lshl_add_u64 v[38:39], v[172:173], 0, s[20:21]
	v_lshl_add_u64 v[40:41], v[174:175], 0, s[20:21]
	v_lshl_add_u64 v[42:43], v[176:177], 0, s[20:21]
	v_lshl_add_u64 v[44:45], v[178:179], 0, s[20:21]
	v_lshl_add_u64 v[58:59], v[180:181], 0, s[20:21]
	v_lshl_add_u64 v[60:61], v[182:183], 0, s[20:21]
	global_load_dwordx4 v[122:125], v[34:35], off nt
	global_load_dwordx4 v[106:109], v[36:37], off nt
	global_load_dwordx4 v[94:97], v[38:39], off nt
	global_load_dwordx4 v[82:85], v[40:41], off nt
	global_load_dwordx4 v[46:49], v[42:43], off nt
	s_nop 0
	global_load_dwordx4 v[42:45], v[44:45], off nt
	s_nop 0
	global_load_dwordx4 v[38:41], v[58:59], off nt
	global_load_dwordx4 v[34:37], v[60:61], off nt
	v_mov_b32_e32 v98, v133
	s_waitcnt vmcnt(23)
	s_waitcnt vmcnt(22)
	s_waitcnt vmcnt(21)
	s_waitcnt vmcnt(20)
	s_waitcnt vmcnt(19)
	s_waitcnt vmcnt(18)
	s_waitcnt vmcnt(17)
	s_waitcnt vmcnt(16)
	ds_read_b32 v58, v187
	v_add_u32_e32 v99, 1, v98
	v_cmp_eq_u32_e32 vcc, v98, v132
	s_nop 1
	v_cndmask_b32_e64 v60, 0, 1.0, vcc
	v_cmp_eq_u32_e32 vcc, v99, v132
	s_nop 1
	v_cndmask_b32_e64 v61, 0, 1.0, vcc
	s_waitcnt lgkmcnt(0)
	v_pk_fma_f32 v[62:63], v[58:59], v[90:91], v[60:61] op_sel_hi:[0,1,1] neg_lo:[1,0,0] neg_hi:[1,0,0]
	v_add_u32_e32 v90, 3, v98
	v_add_u32_e32 v91, 2, v98
	v_cmp_eq_u32_e32 vcc, v90, v132
	v_cvt_pk_bf16_f32 v62, v62, v63
	s_nop 0
	v_cndmask_b32_e64 v65, 0, 1.0, vcc
	v_cmp_eq_u32_e32 vcc, v91, v132
	s_nop 1
	v_cndmask_b32_e64 v64, 0, 1.0, vcc
	v_pk_fma_f32 v[58:59], v[58:59], v[92:93], v[64:65] op_sel_hi:[0,1,1] neg_lo:[1,0,0] neg_hi:[1,0,0]
	v_cvt_pk_bf16_f32 v63, v58, v59
	ds_write_b64 v186, v[62:63]
	ds_read_b32 v58, v187 offset:8
	v_cmp_eq_u32_e32 vcc, v98, v193
	s_nop 1
	v_cndmask_b32_e64 v62, 0, 1.0, vcc
	v_cmp_eq_u32_e32 vcc, v99, v193
	s_nop 1
	v_cndmask_b32_e64 v63, 0, 1.0, vcc
	v_cmp_eq_u32_e32 vcc, v90, v193
	s_waitcnt lgkmcnt(0)
	v_pk_fma_f32 v[62:63], v[58:59], v[86:87], v[62:63] op_sel_hi:[0,1,1] neg_lo:[1,0,0] neg_hi:[1,0,0]
	v_cvt_pk_bf16_f32 v62, v62, v63
	v_cndmask_b32_e64 v61, 0, 1.0, vcc
	v_pk_fma_f32 v[58:59], v[58:59], v[88:89], v[60:61] op_sel_hi:[0,1,1] neg_lo:[1,0,0] neg_hi:[1,0,0]
	v_cvt_pk_bf16_f32 v63, v58, v59
	ds_write_b64 v186, v[62:63] offset:544
	ds_read_b32 v58, v187 offset:16
	v_cmp_eq_u32_e32 vcc, v98, v192
	s_nop 1
	v_cndmask_b32_e64 v60, 0, 1.0, vcc
	v_cmp_eq_u32_e32 vcc, v99, v192
	s_nop 1
	v_cndmask_b32_e64 v61, 0, 1.0, vcc
	v_cmp_eq_u32_e32 vcc, v90, v192
	s_waitcnt lgkmcnt(0)
	v_pk_fma_f32 v[54:55], v[58:59], v[54:55], v[60:61] op_sel_hi:[0,1,1] neg_lo:[1,0,0] neg_hi:[1,0,0]
	v_cvt_pk_bf16_f32 v54, v54, v55
	v_cndmask_b32_e64 v61, 0, 1.0, vcc
	v_cmp_eq_u32_e32 vcc, v91, v192
	s_nop 1
	v_cndmask_b32_e64 v60, 0, 1.0, vcc
	v_pk_fma_f32 v[56:57], v[58:59], v[56:57], v[60:61] op_sel_hi:[0,1,1] neg_lo:[1,0,0] neg_hi:[1,0,0]
	v_cvt_pk_bf16_f32 v55, v56, v57
	ds_write_b64 v186, v[54:55] offset:1088
	ds_read_b32 v54, v187 offset:24
	v_cmp_eq_u32_e32 vcc, v98, v190
	s_nop 1
	v_cndmask_b32_e64 v56, 0, 1.0, vcc
	v_cmp_eq_u32_e32 vcc, v99, v190
	s_nop 1
	v_cndmask_b32_e64 v57, 0, 1.0, vcc
	v_cmp_eq_u32_e32 vcc, v90, v190
	s_waitcnt lgkmcnt(0)
	v_pk_fma_f32 v[50:51], v[54:55], v[50:51], v[56:57] op_sel_hi:[0,1,1] neg_lo:[1,0,0] neg_hi:[1,0,0]
	v_cvt_pk_bf16_f32 v50, v50, v51
	v_cndmask_b32_e64 v57, 0, 1.0, vcc
	v_cmp_eq_u32_e32 vcc, v91, v190
	s_nop 1
	v_cndmask_b32_e64 v56, 0, 1.0, vcc
	v_pk_fma_f32 v[52:53], v[54:55], v[52:53], v[56:57] op_sel_hi:[0,1,1] neg_lo:[1,0,0] neg_hi:[1,0,0]
	v_cvt_pk_bf16_f32 v51, v52, v53
	ds_write_b64 v186, v[50:51] offset:1632
	ds_read_b32 v50, v187 offset:32
	v_cmp_eq_u32_e32 vcc, v98, v149
	s_nop 1
	v_cndmask_b32_e64 v52, 0, 1.0, vcc
	v_cmp_eq_u32_e32 vcc, v99, v149
	s_nop 1
	v_cndmask_b32_e64 v53, 0, 1.0, vcc
	v_cmp_eq_u32_e32 vcc, v90, v149
	s_waitcnt lgkmcnt(0)
	v_pk_fma_f32 v[14:15], v[50:51], v[14:15], v[52:53] op_sel_hi:[0,1,1] neg_lo:[1,0,0] neg_hi:[1,0,0]
	v_cvt_pk_bf16_f32 v14, v14, v15
	v_cndmask_b32_e64 v53, 0, 1.0, vcc
	v_cmp_eq_u32_e32 vcc, v91, v149
	s_nop 1
	v_cndmask_b32_e64 v52, 0, 1.0, vcc
	v_pk_fma_f32 v[16:17], v[50:51], v[16:17], v[52:53] op_sel_hi:[0,1,1] neg_lo:[1,0,0] neg_hi:[1,0,0]
	v_cvt_pk_bf16_f32 v15, v16, v17
	ds_write_b64 v186, v[14:15] offset:2176
	ds_read_b32 v14, v187 offset:40
	v_cmp_eq_u32_e32 vcc, v98, v148
	s_nop 1
	v_cndmask_b32_e64 v16, 0, 1.0, vcc
	v_cmp_eq_u32_e32 vcc, v99, v148
	s_nop 1
	v_cndmask_b32_e64 v17, 0, 1.0, vcc
	v_cmp_eq_u32_e32 vcc, v90, v148
	s_waitcnt lgkmcnt(0)
	v_pk_fma_f32 v[10:11], v[14:15], v[10:11], v[16:17] op_sel_hi:[0,1,1] neg_lo:[1,0,0] neg_hi:[1,0,0]
	v_cvt_pk_bf16_f32 v10, v10, v11
	v_cndmask_b32_e64 v17, 0, 1.0, vcc
	v_cmp_eq_u32_e32 vcc, v91, v148
	s_nop 1
	v_cndmask_b32_e64 v16, 0, 1.0, vcc
	v_pk_fma_f32 v[12:13], v[14:15], v[12:13], v[16:17] op_sel_hi:[0,1,1] neg_lo:[1,0,0] neg_hi:[1,0,0]
	v_cvt_pk_bf16_f32 v11, v12, v13
	ds_write_b64 v186, v[10:11] offset:2720
	ds_read_b32 v10, v187 offset:48
	v_cmp_eq_u32_e32 vcc, v98, v147
	s_nop 1
	v_cndmask_b32_e64 v12, 0, 1.0, vcc
	v_cmp_eq_u32_e32 vcc, v99, v147
	s_nop 1
	v_cndmask_b32_e64 v13, 0, 1.0, vcc
	v_cmp_eq_u32_e32 vcc, v90, v147
	s_waitcnt lgkmcnt(0)
	v_pk_fma_f32 v[6:7], v[10:11], v[6:7], v[12:13] op_sel_hi:[0,1,1] neg_lo:[1,0,0] neg_hi:[1,0,0]
	v_cvt_pk_bf16_f32 v6, v6, v7
	v_cndmask_b32_e64 v13, 0, 1.0, vcc
	v_cmp_eq_u32_e32 vcc, v91, v147
	s_nop 1
	v_cndmask_b32_e64 v12, 0, 1.0, vcc
	v_pk_fma_f32 v[8:9], v[10:11], v[8:9], v[12:13] op_sel_hi:[0,1,1] neg_lo:[1,0,0] neg_hi:[1,0,0]
	v_cvt_pk_bf16_f32 v7, v8, v9
	ds_write_b64 v186, v[6:7] offset:3264
	ds_read_b32 v6, v187 offset:56
	v_cmp_eq_u32_e32 vcc, v98, v146
	s_nop 1
	v_cndmask_b32_e64 v8, 0, 1.0, vcc
	v_cmp_eq_u32_e32 vcc, v99, v146
	s_nop 1
	v_cndmask_b32_e64 v9, 0, 1.0, vcc
	v_cmp_eq_u32_e32 vcc, v90, v146
	s_waitcnt lgkmcnt(0)
	v_pk_fma_f32 v[2:3], v[6:7], v[2:3], v[8:9] op_sel_hi:[0,1,1] neg_lo:[1,0,0] neg_hi:[1,0,0]
	v_cvt_pk_bf16_f32 v2, v2, v3
	v_cndmask_b32_e64 v9, 0, 1.0, vcc
	v_cmp_eq_u32_e32 vcc, v91, v146
	s_nop 1
	v_cndmask_b32_e64 v8, 0, 1.0, vcc
	v_pk_fma_f32 v[4:5], v[6:7], v[4:5], v[8:9] op_sel_hi:[0,1,1] neg_lo:[1,0,0] neg_hi:[1,0,0]
	v_cvt_pk_bf16_f32 v3, v4, v5
	ds_write_b64 v186, v[2:3] offset:3808
	ds_read_b128 v[2:5], v1
	ds_read_b128 v[6:9], v1 offset:64
	ds_read_b128 v[10:13], v1 offset:128
	ds_read_b128 v[14:17], v1 offset:192
	global_load_dwordx4 v[118:121], v[118:119], off offset:512 nt
	s_nop 0
	global_load_dwordx4 v[110:113], v[126:127], off offset:512 nt
	global_load_dwordx4 v[98:101], v[128:129], off offset:512 nt
	global_load_dwordx4 v[86:89], v[134:135], off offset:512 nt
	global_load_dwordx4 v[62:65], v[136:137], off offset:512 nt
	global_load_dwordx4 v[58:61], v[138:139], off offset:512 nt
	global_load_dwordx4 v[54:57], v[140:141], off offset:512 nt
	global_load_dwordx4 v[50:53], v[142:143], off offset:512 nt
	v_mov_b32_e32 v91, v133
	s_waitcnt vmcnt(23)
	s_waitcnt vmcnt(22)
	s_waitcnt vmcnt(21)
	s_waitcnt vmcnt(20)
	s_waitcnt vmcnt(19)
	s_waitcnt vmcnt(18)
	s_waitcnt vmcnt(17)
	s_waitcnt vmcnt(16)
	ds_read_b32 v90, v187 offset:64
	v_or_b32_e32 v138, 16, v132
	v_add_u32_e32 v102, 1, v91
	v_cmp_eq_u32_e32 vcc, v91, v138
	v_add_u32_e32 v103, 3, v91
	v_add_u32_e32 v104, 2, v91
	v_cndmask_b32_e64 v92, 0, 1.0, vcc
	v_cmp_eq_u32_e32 vcc, v102, v138
	v_or_b32_e32 v139, 18, v132
	v_or_b32_e32 v140, 20, v132
	v_cndmask_b32_e64 v93, 0, 1.0, vcc
	v_cmp_eq_u32_e32 vcc, v103, v138
	s_waitcnt lgkmcnt(0)
	v_pk_fma_f32 v[78:79], v[90:91], v[78:79], v[92:93] op_sel_hi:[0,1,1] neg_lo:[1,0,0] neg_hi:[1,0,0]
	v_cvt_pk_bf16_f32 v78, v78, v79
	v_cndmask_b32_e64 v93, 0, 1.0, vcc
	v_cmp_eq_u32_e32 vcc, v104, v138
	v_or_b32_e32 v141, 22, v132
	v_or_b32_e32 v142, 24, v132
	v_cndmask_b32_e64 v92, 0, 1.0, vcc
	v_pk_fma_f32 v[80:81], v[90:91], v[80:81], v[92:93] op_sel_hi:[0,1,1] neg_lo:[1,0,0] neg_hi:[1,0,0]
	v_cvt_pk_bf16_f32 v79, v80, v81
	ds_write_b64 v186, v[78:79]
	ds_read_b32 v78, v187 offset:72
	v_cmp_eq_u32_e32 vcc, v91, v139
	v_or_b32_e32 v143, 26, v132
	v_or_b32_e32 v144, 28, v132
	v_cndmask_b32_e64 v80, 0, 1.0, vcc
	v_cmp_eq_u32_e32 vcc, v102, v139
	v_or_b32_e32 v145, 30, v132
	s_nop 0
	v_cndmask_b32_e64 v81, 0, 1.0, vcc
	v_cmp_eq_u32_e32 vcc, v103, v139
	s_waitcnt lgkmcnt(0)
	v_pk_fma_f32 v[74:75], v[78:79], v[74:75], v[80:81] op_sel_hi:[0,1,1] neg_lo:[1,0,0] neg_hi:[1,0,0]
	v_cvt_pk_bf16_f32 v74, v74, v75
	v_cndmask_b32_e64 v81, 0, 1.0, vcc
	v_cmp_eq_u32_e32 vcc, v104, v139
	s_nop 1
	v_cndmask_b32_e64 v80, 0, 1.0, vcc
	v_pk_fma_f32 v[76:77], v[78:79], v[76:77], v[80:81] op_sel_hi:[0,1,1] neg_lo:[1,0,0] neg_hi:[1,0,0]
	v_cvt_pk_bf16_f32 v75, v76, v77
	ds_write_b64 v186, v[74:75] offset:544
	ds_read_b32 v74, v187 offset:80
	v_cmp_eq_u32_e32 vcc, v91, v140
	s_nop 1
	v_cndmask_b32_e64 v76, 0, 1.0, vcc
	v_cmp_eq_u32_e32 vcc, v102, v140
	s_nop 1
	v_cndmask_b32_e64 v77, 0, 1.0, vcc
	v_cmp_eq_u32_e32 vcc, v103, v140
	s_waitcnt lgkmcnt(0)
	v_pk_fma_f32 v[70:71], v[74:75], v[70:71], v[76:77] op_sel_hi:[0,1,1] neg_lo:[1,0,0] neg_hi:[1,0,0]
	v_cvt_pk_bf16_f32 v70, v70, v71
	v_cndmask_b32_e64 v77, 0, 1.0, vcc
	v_cmp_eq_u32_e32 vcc, v104, v140
	s_nop 1
	v_cndmask_b32_e64 v76, 0, 1.0, vcc
	v_pk_fma_f32 v[72:73], v[74:75], v[72:73], v[76:77] op_sel_hi:[0,1,1] neg_lo:[1,0,0] neg_hi:[1,0,0]
	v_cvt_pk_bf16_f32 v71, v72, v73
	ds_write_b64 v186, v[70:71] offset:1088
	ds_read_b32 v70, v187 offset:88
	v_cmp_eq_u32_e32 vcc, v91, v141
	s_nop 1
	v_cndmask_b32_e64 v72, 0, 1.0, vcc
	v_cmp_eq_u32_e32 vcc, v102, v141
	s_nop 1
	v_cndmask_b32_e64 v73, 0, 1.0, vcc
	v_cmp_eq_u32_e32 vcc, v103, v141
	s_waitcnt lgkmcnt(0)
	v_pk_fma_f32 v[66:67], v[70:71], v[66:67], v[72:73] op_sel_hi:[0,1,1] neg_lo:[1,0,0] neg_hi:[1,0,0]
	v_cvt_pk_bf16_f32 v66, v66, v67
	v_cndmask_b32_e64 v73, 0, 1.0, vcc
	v_cmp_eq_u32_e32 vcc, v104, v141
	s_nop 1
	v_cndmask_b32_e64 v72, 0, 1.0, vcc
	v_pk_fma_f32 v[68:69], v[70:71], v[68:69], v[72:73] op_sel_hi:[0,1,1] neg_lo:[1,0,0] neg_hi:[1,0,0]
	v_cvt_pk_bf16_f32 v67, v68, v69
	ds_write_b64 v186, v[66:67] offset:1632
	ds_read_b32 v66, v187 offset:96
	v_cmp_eq_u32_e32 vcc, v91, v142
	s_nop 1
	v_cndmask_b32_e64 v68, 0, 1.0, vcc
	v_cmp_eq_u32_e32 vcc, v102, v142
	s_nop 1
	v_cndmask_b32_e64 v69, 0, 1.0, vcc
	v_cmp_eq_u32_e32 vcc, v103, v142
	s_waitcnt lgkmcnt(0)
	v_pk_fma_f32 v[30:31], v[66:67], v[30:31], v[68:69] op_sel_hi:[0,1,1] neg_lo:[1,0,0] neg_hi:[1,0,0]
	v_cvt_pk_bf16_f32 v30, v30, v31
	v_cndmask_b32_e64 v69, 0, 1.0, vcc
	v_cmp_eq_u32_e32 vcc, v104, v142
	s_nop 1
	v_cndmask_b32_e64 v68, 0, 1.0, vcc
	v_pk_fma_f32 v[32:33], v[66:67], v[32:33], v[68:69] op_sel_hi:[0,1,1] neg_lo:[1,0,0] neg_hi:[1,0,0]
	v_cvt_pk_bf16_f32 v31, v32, v33
	ds_write_b64 v186, v[30:31] offset:2176
	ds_read_b32 v30, v187 offset:104
	v_cmp_eq_u32_e32 vcc, v91, v143
	s_nop 1
	v_cndmask_b32_e64 v32, 0, 1.0, vcc
	v_cmp_eq_u32_e32 vcc, v102, v143
	s_nop 1
	v_cndmask_b32_e64 v33, 0, 1.0, vcc
	v_cmp_eq_u32_e32 vcc, v103, v143
	s_waitcnt lgkmcnt(0)
	v_pk_fma_f32 v[26:27], v[30:31], v[26:27], v[32:33] op_sel_hi:[0,1,1] neg_lo:[1,0,0] neg_hi:[1,0,0]
	v_cvt_pk_bf16_f32 v26, v26, v27
	v_cndmask_b32_e64 v33, 0, 1.0, vcc
	v_cmp_eq_u32_e32 vcc, v104, v143
	s_nop 1
	v_cndmask_b32_e64 v32, 0, 1.0, vcc
	v_pk_fma_f32 v[28:29], v[30:31], v[28:29], v[32:33] op_sel_hi:[0,1,1] neg_lo:[1,0,0] neg_hi:[1,0,0]
	v_cvt_pk_bf16_f32 v27, v28, v29
	ds_write_b64 v186, v[26:27] offset:2720
	ds_read_b32 v26, v187 offset:112
	v_cmp_eq_u32_e32 vcc, v91, v144
	s_nop 1
	v_cndmask_b32_e64 v28, 0, 1.0, vcc
	v_cmp_eq_u32_e32 vcc, v102, v144
	s_nop 1
	v_cndmask_b32_e64 v29, 0, 1.0, vcc
	v_cmp_eq_u32_e32 vcc, v103, v144
	s_waitcnt lgkmcnt(0)
	v_pk_fma_f32 v[22:23], v[26:27], v[22:23], v[28:29] op_sel_hi:[0,1,1] neg_lo:[1,0,0] neg_hi:[1,0,0]
	v_cvt_pk_bf16_f32 v22, v22, v23
	v_cndmask_b32_e64 v29, 0, 1.0, vcc
	v_cmp_eq_u32_e32 vcc, v104, v144
	s_nop 1
	v_cndmask_b32_e64 v28, 0, 1.0, vcc
	v_pk_fma_f32 v[24:25], v[26:27], v[24:25], v[28:29] op_sel_hi:[0,1,1] neg_lo:[1,0,0] neg_hi:[1,0,0]
	v_cvt_pk_bf16_f32 v23, v24, v25
	ds_write_b64 v186, v[22:23] offset:3264
	ds_read_b32 v22, v187 offset:120
	v_cmp_eq_u32_e32 vcc, v91, v145
	s_nop 1
	v_cndmask_b32_e64 v24, 0, 1.0, vcc
	v_cmp_eq_u32_e32 vcc, v102, v145
	s_nop 1
	v_cndmask_b32_e64 v25, 0, 1.0, vcc
	v_cmp_eq_u32_e32 vcc, v103, v145
	s_waitcnt lgkmcnt(0)
	v_pk_fma_f32 v[18:19], v[22:23], v[18:19], v[24:25] op_sel_hi:[0,1,1] neg_lo:[1,0,0] neg_hi:[1,0,0]
	v_cvt_pk_bf16_f32 v18, v18, v19
	v_cndmask_b32_e64 v25, 0, 1.0, vcc
	v_cmp_eq_u32_e32 vcc, v104, v145
	s_nop 1
	v_cndmask_b32_e64 v24, 0, 1.0, vcc
	v_pk_fma_f32 v[20:21], v[22:23], v[20:21], v[24:25] op_sel_hi:[0,1,1] neg_lo:[1,0,0] neg_hi:[1,0,0]
	v_cvt_pk_bf16_f32 v19, v20, v21
	ds_write_b64 v186, v[18:19] offset:3808
	ds_read_b128 v[18:21], v1
	ds_read_b128 v[22:25], v1 offset:64
	ds_read_b128 v[26:29], v1 offset:128
	ds_read_b128 v[30:33], v1 offset:192
	v_lshl_add_u64 v[66:67], v[150:151], 0, s[8:9]
	v_lshl_add_u64 v[68:69], v[152:153], 0, s[8:9]
	v_lshl_add_u64 v[70:71], v[156:157], 0, s[8:9]
	v_lshl_add_u64 v[72:73], v[158:159], 0, s[8:9]
	v_lshl_add_u64 v[74:75], v[160:161], 0, s[8:9]
	v_lshl_add_u64 v[76:77], v[162:163], 0, s[8:9]
	v_lshl_add_u64 v[134:135], v[164:165], 0, s[8:9]
	v_lshl_add_u64 v[136:137], v[166:167], 0, s[8:9]
	global_load_dwordx4 v[126:129], v[66:67], off nt
	global_load_dwordx4 v[114:117], v[68:69], off nt
	global_load_dwordx4 v[102:105], v[70:71], off nt
	global_load_dwordx4 v[90:93], v[72:73], off nt
	global_load_dwordx4 v[78:81], v[74:75], off nt
	s_nop 0
	global_load_dwordx4 v[74:77], v[76:77], off nt
	s_nop 0
	global_load_dwordx4 v[70:73], v[134:135], off nt
	global_load_dwordx4 v[66:69], v[136:137], off nt
	s_waitcnt vmcnt(23)
	s_waitcnt vmcnt(22)
	s_waitcnt vmcnt(21)
	s_waitcnt vmcnt(20)
	s_waitcnt vmcnt(19)
	s_waitcnt vmcnt(18)
	s_waitcnt vmcnt(17)
	s_waitcnt vmcnt(16)
	ds_read_b32 v134, v187 offset:128
	v_or_b32_e32 v194, 32, v132
	v_add_u32_e32 v135, 1, v133
	v_cmp_eq_u32_e32 vcc, v133, v194
	v_add_u32_e32 v202, 3, v133
	v_add_u32_e32 v203, 2, v133
	v_cndmask_b32_e64 v136, 0, 1.0, vcc
	v_cmp_eq_u32_e32 vcc, v135, v194
	v_or_b32_e32 v195, 34, v132
	v_or_b32_e32 v196, 36, v132
	v_cndmask_b32_e64 v137, 0, 1.0, vcc
	v_cmp_eq_u32_e32 vcc, v202, v194
	s_waitcnt lgkmcnt(0)
	v_pk_fma_f32 v[122:123], v[134:135], v[122:123], v[136:137] op_sel_hi:[0,1,1] neg_lo:[1,0,0] neg_hi:[1,0,0]
	v_cvt_pk_bf16_f32 v122, v122, v123
	v_cndmask_b32_e64 v137, 0, 1.0, vcc
	v_cmp_eq_u32_e32 vcc, v203, v194
	v_or_b32_e32 v197, 38, v132
	v_or_b32_e32 v198, 40, v132
	v_cndmask_b32_e64 v136, 0, 1.0, vcc
	v_pk_fma_f32 v[124:125], v[134:135], v[124:125], v[136:137] op_sel_hi:[0,1,1] neg_lo:[1,0,0] neg_hi:[1,0,0]
	v_cvt_pk_bf16_f32 v123, v124, v125
	ds_write_b64 v186, v[122:123]
	ds_read_b32 v122, v187 offset:136
	v_cmp_eq_u32_e32 vcc, v133, v195
	v_or_b32_e32 v199, 42, v132
	v_or_b32_e32 v200, 44, v132
	v_cndmask_b32_e64 v124, 0, 1.0, vcc
	v_cmp_eq_u32_e32 vcc, v135, v195
	v_or_b32_e32 v201, 46, v132
	s_nop 0
	v_cndmask_b32_e64 v125, 0, 1.0, vcc
	v_cmp_eq_u32_e32 vcc, v202, v195
	s_waitcnt lgkmcnt(0)
	v_pk_fma_f32 v[106:107], v[122:123], v[106:107], v[124:125] op_sel_hi:[0,1,1] neg_lo:[1,0,0] neg_hi:[1,0,0]
	v_cvt_pk_bf16_f32 v106, v106, v107
	v_cndmask_b32_e64 v125, 0, 1.0, vcc
	v_cmp_eq_u32_e32 vcc, v203, v195
	s_nop 1
	v_cndmask_b32_e64 v124, 0, 1.0, vcc
	v_pk_fma_f32 v[108:109], v[122:123], v[108:109], v[124:125] op_sel_hi:[0,1,1] neg_lo:[1,0,0] neg_hi:[1,0,0]
	v_cvt_pk_bf16_f32 v107, v108, v109
	ds_write_b64 v186, v[106:107] offset:544
	ds_read_b32 v106, v187 offset:144
	v_cmp_eq_u32_e32 vcc, v133, v196
	s_nop 1
	v_cndmask_b32_e64 v108, 0, 1.0, vcc
	v_cmp_eq_u32_e32 vcc, v135, v196
	s_nop 1
	v_cndmask_b32_e64 v109, 0, 1.0, vcc
	v_cmp_eq_u32_e32 vcc, v202, v196
	s_waitcnt lgkmcnt(0)
	v_pk_fma_f32 v[94:95], v[106:107], v[94:95], v[108:109] op_sel_hi:[0,1,1] neg_lo:[1,0,0] neg_hi:[1,0,0]
	v_cvt_pk_bf16_f32 v94, v94, v95
	v_cndmask_b32_e64 v109, 0, 1.0, vcc
	v_cmp_eq_u32_e32 vcc, v203, v196
	s_nop 1
	v_cndmask_b32_e64 v108, 0, 1.0, vcc
	v_pk_fma_f32 v[96:97], v[106:107], v[96:97], v[108:109] op_sel_hi:[0,1,1] neg_lo:[1,0,0] neg_hi:[1,0,0]
	v_cvt_pk_bf16_f32 v95, v96, v97
	ds_write_b64 v186, v[94:95] offset:1088
	ds_read_b32 v94, v187 offset:152
	v_cmp_eq_u32_e32 vcc, v133, v197
	s_nop 1
	v_cndmask_b32_e64 v96, 0, 1.0, vcc
	v_cmp_eq_u32_e32 vcc, v135, v197
	s_nop 1
	v_cndmask_b32_e64 v97, 0, 1.0, vcc
	v_cmp_eq_u32_e32 vcc, v202, v197
	s_waitcnt lgkmcnt(0)
	v_pk_fma_f32 v[82:83], v[94:95], v[82:83], v[96:97] op_sel_hi:[0,1,1] neg_lo:[1,0,0] neg_hi:[1,0,0]
	v_cvt_pk_bf16_f32 v82, v82, v83
	v_cndmask_b32_e64 v97, 0, 1.0, vcc
	v_cmp_eq_u32_e32 vcc, v203, v197
	s_nop 1
	v_cndmask_b32_e64 v96, 0, 1.0, vcc
	v_pk_fma_f32 v[84:85], v[94:95], v[84:85], v[96:97] op_sel_hi:[0,1,1] neg_lo:[1,0,0] neg_hi:[1,0,0]
	v_cvt_pk_bf16_f32 v83, v84, v85
	ds_write_b64 v186, v[82:83] offset:1632
	ds_read_b32 v82, v187 offset:160
	v_cmp_eq_u32_e32 vcc, v133, v198
	s_nop 1
	v_cndmask_b32_e64 v84, 0, 1.0, vcc
	v_cmp_eq_u32_e32 vcc, v135, v198
	s_nop 1
	v_cndmask_b32_e64 v85, 0, 1.0, vcc
	v_cmp_eq_u32_e32 vcc, v202, v198
	s_waitcnt lgkmcnt(0)
	v_pk_fma_f32 v[46:47], v[82:83], v[46:47], v[84:85] op_sel_hi:[0,1,1] neg_lo:[1,0,0] neg_hi:[1,0,0]
	v_cvt_pk_bf16_f32 v46, v46, v47
	v_cndmask_b32_e64 v85, 0, 1.0, vcc
	v_cmp_eq_u32_e32 vcc, v203, v198
	s_nop 1
	v_cndmask_b32_e64 v84, 0, 1.0, vcc
	v_pk_fma_f32 v[48:49], v[82:83], v[48:49], v[84:85] op_sel_hi:[0,1,1] neg_lo:[1,0,0] neg_hi:[1,0,0]
	v_cvt_pk_bf16_f32 v47, v48, v49
	ds_write_b64 v186, v[46:47] offset:2176
	ds_read_b32 v46, v187 offset:168
	v_cmp_eq_u32_e32 vcc, v133, v199
	s_nop 1
	v_cndmask_b32_e64 v48, 0, 1.0, vcc
	v_cmp_eq_u32_e32 vcc, v135, v199
	s_nop 1
	v_cndmask_b32_e64 v49, 0, 1.0, vcc
	v_cmp_eq_u32_e32 vcc, v202, v199
	s_waitcnt lgkmcnt(0)
	v_pk_fma_f32 v[42:43], v[46:47], v[42:43], v[48:49] op_sel_hi:[0,1,1] neg_lo:[1,0,0] neg_hi:[1,0,0]
	v_cvt_pk_bf16_f32 v42, v42, v43
	v_cndmask_b32_e64 v49, 0, 1.0, vcc
	v_cmp_eq_u32_e32 vcc, v203, v199
	s_nop 1
	v_cndmask_b32_e64 v48, 0, 1.0, vcc
	v_pk_fma_f32 v[44:45], v[46:47], v[44:45], v[48:49] op_sel_hi:[0,1,1] neg_lo:[1,0,0] neg_hi:[1,0,0]
	v_cvt_pk_bf16_f32 v43, v44, v45
	ds_write_b64 v186, v[42:43] offset:2720
	ds_read_b32 v42, v187 offset:176
	v_cmp_eq_u32_e32 vcc, v133, v200
	s_nop 1
	v_cndmask_b32_e64 v44, 0, 1.0, vcc
	v_cmp_eq_u32_e32 vcc, v135, v200
	s_nop 1
	v_cndmask_b32_e64 v45, 0, 1.0, vcc
	v_cmp_eq_u32_e32 vcc, v202, v200
	s_waitcnt lgkmcnt(0)
	v_pk_fma_f32 v[38:39], v[42:43], v[38:39], v[44:45] op_sel_hi:[0,1,1] neg_lo:[1,0,0] neg_hi:[1,0,0]
	v_cvt_pk_bf16_f32 v38, v38, v39
	v_cndmask_b32_e64 v45, 0, 1.0, vcc
	v_cmp_eq_u32_e32 vcc, v203, v200
	s_nop 1
	v_cndmask_b32_e64 v44, 0, 1.0, vcc
	v_pk_fma_f32 v[40:41], v[42:43], v[40:41], v[44:45] op_sel_hi:[0,1,1] neg_lo:[1,0,0] neg_hi:[1,0,0]
	v_cvt_pk_bf16_f32 v39, v40, v41
	ds_write_b64 v186, v[38:39] offset:3264
	ds_read_b32 v38, v187 offset:184
	v_cmp_eq_u32_e32 vcc, v133, v201
	s_nop 1
	v_cndmask_b32_e64 v40, 0, 1.0, vcc
	v_cmp_eq_u32_e32 vcc, v135, v201
	s_nop 1
	v_cndmask_b32_e64 v41, 0, 1.0, vcc
	v_cmp_eq_u32_e32 vcc, v202, v201
	s_waitcnt lgkmcnt(0)
	v_pk_fma_f32 v[34:35], v[38:39], v[34:35], v[40:41] op_sel_hi:[0,1,1] neg_lo:[1,0,0] neg_hi:[1,0,0]
	v_cvt_pk_bf16_f32 v34, v34, v35
	v_cndmask_b32_e64 v41, 0, 1.0, vcc
	v_cmp_eq_u32_e32 vcc, v203, v201
	s_nop 1
	v_cndmask_b32_e64 v40, 0, 1.0, vcc
	v_pk_fma_f32 v[36:37], v[38:39], v[36:37], v[40:41] op_sel_hi:[0,1,1] neg_lo:[1,0,0] neg_hi:[1,0,0]
	v_cvt_pk_bf16_f32 v35, v36, v37
	ds_write_b64 v186, v[34:35] offset:3808
	ds_read_b128 v[34:37], v1
	ds_read_b128 v[38:41], v1 offset:64
	ds_read_b128 v[42:45], v1 offset:128
	ds_read_b128 v[46:49], v1 offset:192
	v_mov_b32_e32 v106, v189
	s_waitcnt vmcnt(15)
	s_waitcnt vmcnt(14)
	s_waitcnt vmcnt(13)
	s_waitcnt vmcnt(12)
	s_waitcnt vmcnt(11)
	s_waitcnt vmcnt(10)
	s_waitcnt vmcnt(9)
	s_waitcnt vmcnt(8)
	ds_read_b32 v82, v187
	v_add_u32_e32 v107, 1, v106
	v_cmp_eq_u32_e32 vcc, v106, v132
	v_add_u32_e32 v108, 3, v106
	v_add_u32_e32 v109, 2, v106
	v_cndmask_b32_e64 v84, 0, 1.0, vcc
	v_cmp_eq_u32_e32 vcc, v107, v132
	s_nop 1
	v_cndmask_b32_e64 v85, 0, 1.0, vcc
	v_cmp_eq_u32_e32 vcc, v108, v132
	s_waitcnt lgkmcnt(0)
	v_pk_fma_f32 v[94:95], v[82:83], v[118:119], v[84:85] op_sel_hi:[0,1,1] neg_lo:[1,0,0] neg_hi:[1,0,0]
	v_cvt_pk_bf16_f32 v94, v94, v95
	v_cndmask_b32_e64 v97, 0, 1.0, vcc
	v_cmp_eq_u32_e32 vcc, v109, v132
	s_nop 1
	v_cndmask_b32_e64 v96, 0, 1.0, vcc
	v_pk_fma_f32 v[82:83], v[82:83], v[120:121], v[96:97] op_sel_hi:[0,1,1] neg_lo:[1,0,0] neg_hi:[1,0,0]
	v_cvt_pk_bf16_f32 v95, v82, v83
	ds_write_b64 v186, v[94:95]
	ds_read_b32 v82, v187 offset:8
	v_cmp_eq_u32_e32 vcc, v106, v193
	s_nop 1
	v_cndmask_b32_e64 v94, 0, 1.0, vcc
	v_cmp_eq_u32_e32 vcc, v107, v193
	s_nop 1
	v_cndmask_b32_e64 v95, 0, 1.0, vcc
	v_cmp_eq_u32_e32 vcc, v108, v193
	s_waitcnt lgkmcnt(0)
	v_pk_fma_f32 v[94:95], v[82:83], v[110:111], v[94:95] op_sel_hi:[0,1,1] neg_lo:[1,0,0] neg_hi:[1,0,0]
	v_cvt_pk_bf16_f32 v94, v94, v95
	v_cndmask_b32_e64 v85, 0, 1.0, vcc
	v_pk_fma_f32 v[82:83], v[82:83], v[112:113], v[84:85] op_sel_hi:[0,1,1] neg_lo:[1,0,0] neg_hi:[1,0,0]
	v_cvt_pk_bf16_f32 v95, v82, v83
	ds_write_b64 v186, v[94:95] offset:544
	ds_read_b32 v82, v187 offset:16
	v_cmp_eq_u32_e32 vcc, v106, v192
	s_nop 1
	v_cndmask_b32_e64 v84, 0, 1.0, vcc
	v_cmp_eq_u32_e32 vcc, v107, v192
	s_nop 1
	v_cndmask_b32_e64 v85, 0, 1.0, vcc
	v_cmp_eq_u32_e32 vcc, v108, v192
	s_waitcnt lgkmcnt(0)
	v_pk_fma_f32 v[84:85], v[82:83], v[98:99], v[84:85] op_sel_hi:[0,1,1] neg_lo:[1,0,0] neg_hi:[1,0,0]
	v_cvt_pk_bf16_f32 v84, v84, v85
	v_cndmask_b32_e64 v95, 0, 1.0, vcc
	v_cmp_eq_u32_e32 vcc, v109, v192
	s_nop 1
	v_cndmask_b32_e64 v94, 0, 1.0, vcc
	v_pk_fma_f32 v[82:83], v[82:83], v[100:101], v[94:95] op_sel_hi:[0,1,1] neg_lo:[1,0,0] neg_hi:[1,0,0]
	v_cvt_pk_bf16_f32 v85, v82, v83
	ds_write_b64 v186, v[84:85] offset:1088
	ds_read_b32 v82, v187 offset:24
	v_cmp_eq_u32_e32 vcc, v106, v190
	s_nop 1
	v_cndmask_b32_e64 v84, 0, 1.0, vcc
	v_cmp_eq_u32_e32 vcc, v107, v190
	s_nop 1
	v_cndmask_b32_e64 v85, 0, 1.0, vcc
	v_cmp_eq_u32_e32 vcc, v108, v190
	s_waitcnt lgkmcnt(0)
	v_pk_fma_f32 v[84:85], v[82:83], v[86:87], v[84:85] op_sel_hi:[0,1,1] neg_lo:[1,0,0] neg_hi:[1,0,0]
	v_cvt_pk_bf16_f32 v84, v84, v85
	v_cndmask_b32_e64 v87, 0, 1.0, vcc
	v_cmp_eq_u32_e32 vcc, v109, v190
	s_nop 1
	v_cndmask_b32_e64 v86, 0, 1.0, vcc
	v_pk_fma_f32 v[82:83], v[82:83], v[88:89], v[86:87] op_sel_hi:[0,1,1] neg_lo:[1,0,0] neg_hi:[1,0,0]
	v_cvt_pk_bf16_f32 v85, v82, v83
	ds_write_b64 v186, v[84:85] offset:1632
	ds_read_b32 v82, v187 offset:32
	v_cmp_eq_u32_e32 vcc, v106, v149
	s_nop 1
	v_cndmask_b32_e64 v84, 0, 1.0, vcc
	v_cmp_eq_u32_e32 vcc, v107, v149
	s_nop 1
	v_cndmask_b32_e64 v85, 0, 1.0, vcc
	v_cmp_eq_u32_e32 vcc, v108, v149
	s_waitcnt lgkmcnt(0)
	v_pk_fma_f32 v[62:63], v[82:83], v[62:63], v[84:85] op_sel_hi:[0,1,1] neg_lo:[1,0,0] neg_hi:[1,0,0]
	v_cvt_pk_bf16_f32 v62, v62, v63
	v_cndmask_b32_e64 v85, 0, 1.0, vcc
	v_cmp_eq_u32_e32 vcc, v109, v149
	s_nop 1
	v_cndmask_b32_e64 v84, 0, 1.0, vcc
	v_pk_fma_f32 v[64:65], v[82:83], v[64:65], v[84:85] op_sel_hi:[0,1,1] neg_lo:[1,0,0] neg_hi:[1,0,0]
	v_cvt_pk_bf16_f32 v63, v64, v65
	ds_write_b64 v186, v[62:63] offset:2176
	ds_read_b32 v62, v187 offset:40
	v_cmp_eq_u32_e32 vcc, v106, v148
	s_nop 1
	v_cndmask_b32_e64 v64, 0, 1.0, vcc
	v_cmp_eq_u32_e32 vcc, v107, v148
	s_nop 1
	v_cndmask_b32_e64 v65, 0, 1.0, vcc
	v_cmp_eq_u32_e32 vcc, v108, v148
	s_waitcnt lgkmcnt(0)
	v_pk_fma_f32 v[58:59], v[62:63], v[58:59], v[64:65] op_sel_hi:[0,1,1] neg_lo:[1,0,0] neg_hi:[1,0,0]
	v_cvt_pk_bf16_f32 v58, v58, v59
	v_cndmask_b32_e64 v65, 0, 1.0, vcc
	v_cmp_eq_u32_e32 vcc, v109, v148
	s_nop 1
	v_cndmask_b32_e64 v64, 0, 1.0, vcc
	v_pk_fma_f32 v[60:61], v[62:63], v[60:61], v[64:65] op_sel_hi:[0,1,1] neg_lo:[1,0,0] neg_hi:[1,0,0]
	v_cvt_pk_bf16_f32 v59, v60, v61
	ds_write_b64 v186, v[58:59] offset:2720
	ds_read_b32 v58, v187 offset:48
	v_cmp_eq_u32_e32 vcc, v106, v147
	s_nop 1
	v_cndmask_b32_e64 v60, 0, 1.0, vcc
	v_cmp_eq_u32_e32 vcc, v107, v147
	s_nop 1
	v_cndmask_b32_e64 v61, 0, 1.0, vcc
	v_cmp_eq_u32_e32 vcc, v108, v147
	s_waitcnt lgkmcnt(0)
	v_pk_fma_f32 v[54:55], v[58:59], v[54:55], v[60:61] op_sel_hi:[0,1,1] neg_lo:[1,0,0] neg_hi:[1,0,0]
	v_cvt_pk_bf16_f32 v54, v54, v55
	v_cndmask_b32_e64 v61, 0, 1.0, vcc
	v_cmp_eq_u32_e32 vcc, v109, v147
	s_nop 1
	v_cndmask_b32_e64 v60, 0, 1.0, vcc
	v_pk_fma_f32 v[56:57], v[58:59], v[56:57], v[60:61] op_sel_hi:[0,1,1] neg_lo:[1,0,0] neg_hi:[1,0,0]
	v_cvt_pk_bf16_f32 v55, v56, v57
	ds_write_b64 v186, v[54:55] offset:3264
	ds_read_b32 v54, v187 offset:56
	v_cmp_eq_u32_e32 vcc, v106, v146
	s_nop 1
	v_cndmask_b32_e64 v56, 0, 1.0, vcc
	v_cmp_eq_u32_e32 vcc, v107, v146
	s_nop 1
	v_cndmask_b32_e64 v57, 0, 1.0, vcc
	v_cmp_eq_u32_e32 vcc, v108, v146
	s_waitcnt lgkmcnt(0)
	v_pk_fma_f32 v[50:51], v[54:55], v[50:51], v[56:57] op_sel_hi:[0,1,1] neg_lo:[1,0,0] neg_hi:[1,0,0]
	v_cvt_pk_bf16_f32 v50, v50, v51
	v_cndmask_b32_e64 v57, 0, 1.0, vcc
	v_cmp_eq_u32_e32 vcc, v109, v146
	s_nop 1
	v_cndmask_b32_e64 v56, 0, 1.0, vcc
	v_pk_fma_f32 v[52:53], v[54:55], v[52:53], v[56:57] op_sel_hi:[0,1,1] neg_lo:[1,0,0] neg_hi:[1,0,0]
	v_cvt_pk_bf16_f32 v51, v52, v53
	ds_write_b64 v186, v[50:51] offset:3808
	ds_read_b128 v[50:53], v1
	ds_read_b128 v[54:57], v1 offset:64
	ds_read_b128 v[58:61], v1 offset:128
	ds_read_b128 v[62:65], v1 offset:192
	v_lshl_add_u64 v[82:83], v[168:169], 0, s[8:9]
	v_lshl_add_u64 v[84:85], v[170:171], 0, s[8:9]
	v_lshl_add_u64 v[86:87], v[172:173], 0, s[8:9]
	v_lshl_add_u64 v[88:89], v[174:175], 0, s[8:9]
	v_lshl_add_u64 v[94:95], v[176:177], 0, s[8:9]
	v_lshl_add_u64 v[96:97], v[178:179], 0, s[8:9]
	v_lshl_add_u64 v[122:123], v[180:181], 0, s[8:9]
	v_lshl_add_u64 v[124:125], v[182:183], 0, s[8:9]
	global_load_dwordx4 v[134:137], v[82:83], off nt
	global_load_dwordx4 v[118:121], v[84:85], off nt
	global_load_dwordx4 v[110:113], v[86:87], off nt
	global_load_dwordx4 v[106:109], v[88:89], off nt
	global_load_dwordx4 v[98:101], v[94:95], off nt
	s_nop 0
	global_load_dwordx4 v[94:97], v[96:97], off nt
	s_nop 0
	global_load_dwordx4 v[86:89], v[122:123], off nt
	global_load_dwordx4 v[82:85], v[124:125], off nt
	v_mov_b32_e32 v132, v189
	s_waitcnt vmcnt(15)
	s_waitcnt vmcnt(14)
	s_waitcnt vmcnt(13)
	s_waitcnt vmcnt(12)
	s_waitcnt vmcnt(11)
	s_waitcnt vmcnt(10)
	s_waitcnt vmcnt(9)
	s_waitcnt vmcnt(8)
	ds_read_b32 v122, v187 offset:64
	v_add_u32_e32 v133, 1, v132
	v_cmp_eq_u32_e32 vcc, v132, v138
	v_add_u32_e32 v146, 3, v132
	v_add_u32_e32 v147, 2, v132
	v_cndmask_b32_e64 v124, 0, 1.0, vcc
	v_cmp_eq_u32_e32 vcc, v133, v138
	s_nop 1
	v_cndmask_b32_e64 v125, 0, 1.0, vcc
	v_cmp_eq_u32_e32 vcc, v146, v138
	s_waitcnt lgkmcnt(0)
	v_pk_fma_f32 v[124:125], v[122:123], v[126:127], v[124:125] op_sel_hi:[0,1,1] neg_lo:[1,0,0] neg_hi:[1,0,0]
	v_cvt_pk_bf16_f32 v124, v124, v125
	v_cndmask_b32_e64 v127, 0, 1.0, vcc
	v_cmp_eq_u32_e32 vcc, v147, v138
	s_nop 1
	v_cndmask_b32_e64 v126, 0, 1.0, vcc
	v_pk_fma_f32 v[122:123], v[122:123], v[128:129], v[126:127] op_sel_hi:[0,1,1] neg_lo:[1,0,0] neg_hi:[1,0,0]
	v_cvt_pk_bf16_f32 v125, v122, v123
	ds_write_b64 v186, v[124:125]
	ds_read_b32 v122, v187 offset:72
	v_cmp_eq_u32_e32 vcc, v132, v139
	s_nop 1
	v_cndmask_b32_e64 v124, 0, 1.0, vcc
	v_cmp_eq_u32_e32 vcc, v133, v139
	s_nop 1
	v_cndmask_b32_e64 v125, 0, 1.0, vcc
	v_cmp_eq_u32_e32 vcc, v146, v139
	s_waitcnt lgkmcnt(0)
	v_pk_fma_f32 v[114:115], v[122:123], v[114:115], v[124:125] op_sel_hi:[0,1,1] neg_lo:[1,0,0] neg_hi:[1,0,0]
	v_cvt_pk_bf16_f32 v114, v114, v115
	v_cndmask_b32_e64 v125, 0, 1.0, vcc
	v_cmp_eq_u32_e32 vcc, v147, v139
	s_nop 1
	v_cndmask_b32_e64 v124, 0, 1.0, vcc
	v_pk_fma_f32 v[116:117], v[122:123], v[116:117], v[124:125] op_sel_hi:[0,1,1] neg_lo:[1,0,0] neg_hi:[1,0,0]
	v_cvt_pk_bf16_f32 v115, v116, v117
	ds_write_b64 v186, v[114:115] offset:544
	ds_read_b32 v114, v187 offset:80
	v_cmp_eq_u32_e32 vcc, v132, v140
	s_nop 1
	v_cndmask_b32_e64 v116, 0, 1.0, vcc
	v_cmp_eq_u32_e32 vcc, v133, v140
	s_nop 1
	v_cndmask_b32_e64 v117, 0, 1.0, vcc
	v_cmp_eq_u32_e32 vcc, v146, v140
	s_waitcnt lgkmcnt(0)
	v_pk_fma_f32 v[102:103], v[114:115], v[102:103], v[116:117] op_sel_hi:[0,1,1] neg_lo:[1,0,0] neg_hi:[1,0,0]
	v_cvt_pk_bf16_f32 v102, v102, v103
	v_cndmask_b32_e64 v117, 0, 1.0, vcc
	v_cmp_eq_u32_e32 vcc, v147, v140
	s_nop 1
	v_cndmask_b32_e64 v116, 0, 1.0, vcc
	v_pk_fma_f32 v[104:105], v[114:115], v[104:105], v[116:117] op_sel_hi:[0,1,1] neg_lo:[1,0,0] neg_hi:[1,0,0]
	v_cvt_pk_bf16_f32 v103, v104, v105
	ds_write_b64 v186, v[102:103] offset:1088
	ds_read_b32 v102, v187 offset:88
	v_cmp_eq_u32_e32 vcc, v132, v141
	s_nop 1
	v_cndmask_b32_e64 v104, 0, 1.0, vcc
	v_cmp_eq_u32_e32 vcc, v133, v141
	s_nop 1
	v_cndmask_b32_e64 v105, 0, 1.0, vcc
	v_cmp_eq_u32_e32 vcc, v146, v141
	s_waitcnt lgkmcnt(0)
	v_pk_fma_f32 v[90:91], v[102:103], v[90:91], v[104:105] op_sel_hi:[0,1,1] neg_lo:[1,0,0] neg_hi:[1,0,0]
	v_cvt_pk_bf16_f32 v90, v90, v91
	v_cndmask_b32_e64 v105, 0, 1.0, vcc
	v_cmp_eq_u32_e32 vcc, v147, v141
	s_nop 1
	v_cndmask_b32_e64 v104, 0, 1.0, vcc
	v_pk_fma_f32 v[92:93], v[102:103], v[92:93], v[104:105] op_sel_hi:[0,1,1] neg_lo:[1,0,0] neg_hi:[1,0,0]
	v_cvt_pk_bf16_f32 v91, v92, v93
	ds_write_b64 v186, v[90:91] offset:1632
	ds_read_b32 v90, v187 offset:96
	v_cmp_eq_u32_e32 vcc, v132, v142
	s_nop 1
	v_cndmask_b32_e64 v92, 0, 1.0, vcc
	v_cmp_eq_u32_e32 vcc, v133, v142
	s_nop 1
	v_cndmask_b32_e64 v93, 0, 1.0, vcc
	v_cmp_eq_u32_e32 vcc, v146, v142
	s_waitcnt lgkmcnt(0)
	v_pk_fma_f32 v[78:79], v[90:91], v[78:79], v[92:93] op_sel_hi:[0,1,1] neg_lo:[1,0,0] neg_hi:[1,0,0]
	v_cvt_pk_bf16_f32 v78, v78, v79
	v_cndmask_b32_e64 v93, 0, 1.0, vcc
	v_cmp_eq_u32_e32 vcc, v147, v142
	s_nop 1
	v_cndmask_b32_e64 v92, 0, 1.0, vcc
	v_pk_fma_f32 v[80:81], v[90:91], v[80:81], v[92:93] op_sel_hi:[0,1,1] neg_lo:[1,0,0] neg_hi:[1,0,0]
	v_cvt_pk_bf16_f32 v79, v80, v81
	ds_write_b64 v186, v[78:79] offset:2176
	ds_read_b32 v78, v187 offset:104
	v_cmp_eq_u32_e32 vcc, v132, v143
	s_nop 1
	v_cndmask_b32_e64 v80, 0, 1.0, vcc
	v_cmp_eq_u32_e32 vcc, v133, v143
	s_nop 1
	v_cndmask_b32_e64 v81, 0, 1.0, vcc
	v_cmp_eq_u32_e32 vcc, v146, v143
	s_waitcnt lgkmcnt(0)
	v_pk_fma_f32 v[74:75], v[78:79], v[74:75], v[80:81] op_sel_hi:[0,1,1] neg_lo:[1,0,0] neg_hi:[1,0,0]
	v_cvt_pk_bf16_f32 v74, v74, v75
	v_cndmask_b32_e64 v81, 0, 1.0, vcc
	v_cmp_eq_u32_e32 vcc, v147, v143
	s_nop 1
	v_cndmask_b32_e64 v80, 0, 1.0, vcc
	v_pk_fma_f32 v[76:77], v[78:79], v[76:77], v[80:81] op_sel_hi:[0,1,1] neg_lo:[1,0,0] neg_hi:[1,0,0]
	v_cvt_pk_bf16_f32 v75, v76, v77
	ds_write_b64 v186, v[74:75] offset:2720
	ds_read_b32 v74, v187 offset:112
	v_cmp_eq_u32_e32 vcc, v132, v144
	s_nop 1
	v_cndmask_b32_e64 v76, 0, 1.0, vcc
	v_cmp_eq_u32_e32 vcc, v133, v144
	s_nop 1
	v_cndmask_b32_e64 v77, 0, 1.0, vcc
	v_cmp_eq_u32_e32 vcc, v146, v144
	s_waitcnt lgkmcnt(0)
	v_pk_fma_f32 v[70:71], v[74:75], v[70:71], v[76:77] op_sel_hi:[0,1,1] neg_lo:[1,0,0] neg_hi:[1,0,0]
	v_cvt_pk_bf16_f32 v70, v70, v71
	v_cndmask_b32_e64 v77, 0, 1.0, vcc
	v_cmp_eq_u32_e32 vcc, v147, v144
	s_nop 1
	v_cndmask_b32_e64 v76, 0, 1.0, vcc
	v_pk_fma_f32 v[72:73], v[74:75], v[72:73], v[76:77] op_sel_hi:[0,1,1] neg_lo:[1,0,0] neg_hi:[1,0,0]
	v_cvt_pk_bf16_f32 v71, v72, v73
	ds_write_b64 v186, v[70:71] offset:3264
	ds_read_b32 v70, v187 offset:120
	v_cmp_eq_u32_e32 vcc, v132, v145
	s_nop 1
	v_cndmask_b32_e64 v72, 0, 1.0, vcc
	v_cmp_eq_u32_e32 vcc, v133, v145
	s_nop 1
	v_cndmask_b32_e64 v73, 0, 1.0, vcc
	v_cmp_eq_u32_e32 vcc, v146, v145
	s_waitcnt lgkmcnt(0)
	v_pk_fma_f32 v[66:67], v[70:71], v[66:67], v[72:73] op_sel_hi:[0,1,1] neg_lo:[1,0,0] neg_hi:[1,0,0]
	v_cvt_pk_bf16_f32 v66, v66, v67
	v_cndmask_b32_e64 v73, 0, 1.0, vcc
	v_cmp_eq_u32_e32 vcc, v147, v145
	s_nop 1
	v_cndmask_b32_e64 v72, 0, 1.0, vcc
	v_pk_fma_f32 v[68:69], v[70:71], v[68:69], v[72:73] op_sel_hi:[0,1,1] neg_lo:[1,0,0] neg_hi:[1,0,0]
	v_cvt_pk_bf16_f32 v67, v68, v69
	ds_write_b64 v186, v[66:67] offset:3808
	ds_read_b128 v[66:69], v1
	ds_read_b128 v[70:73], v1 offset:64
	ds_read_b128 v[74:77], v1 offset:128
	ds_read_b128 v[78:81], v1 offset:192
	v_lshl_add_u64 v[90:91], v[130:131], 0, s[0:1]
	v_add_co_u32_e32 v92, vcc, s7, v90
	s_nop 1
	v_addc_co_u32_e32 v93, vcc, 0, v91, vcc
	global_load_dwordx4 v[146:149], v[90:91], off nt
	global_load_dwordx4 v[142:145], v[92:93], off nt
	v_add_co_u32_e32 v92, vcc, s36, v90
	s_nop 1
	v_addc_co_u32_e32 v93, vcc, 0, v91, vcc
	v_add_co_u32_e32 v102, vcc, s37, v90
	s_nop 1
	v_addc_co_u32_e32 v103, vcc, 0, v91, vcc
	global_load_dwordx4 v[138:141], v[92:93], off nt
	global_load_dwordx4 v[130:133], v[102:103], off nt
	v_add_co_u32_e32 v92, vcc, s38, v90
	s_nop 1
	v_addc_co_u32_e32 v93, vcc, 0, v91, vcc
	v_add_co_u32_e32 v102, vcc, s39, v90
	s_nop 1
	v_addc_co_u32_e32 v103, vcc, 0, v91, vcc
	global_load_dwordx4 v[126:129], v[92:93], off nt
	global_load_dwordx4 v[122:125], v[102:103], off nt
	v_add_co_u32_e32 v92, vcc, s41, v90
	s_nop 1
	v_addc_co_u32_e32 v93, vcc, 0, v91, vcc
	v_add_co_u32_e32 v90, vcc, s42, v90
	s_nop 1
	v_addc_co_u32_e32 v91, vcc, 0, v91, vcc
	global_load_dwordx4 v[114:117], v[92:93], off nt
	global_load_dwordx4 v[102:105], v[90:91], off nt
	s_waitcnt vmcnt(15)
	s_waitcnt vmcnt(14)
	s_waitcnt vmcnt(13)
	s_waitcnt vmcnt(12)
	s_waitcnt vmcnt(11)
	s_waitcnt vmcnt(10)
	s_waitcnt vmcnt(9)
	s_waitcnt vmcnt(8)
	ds_read_b32 v90, v187 offset:128
	v_add_u32_e32 v190, 1, v189
	v_cmp_eq_u32_e32 vcc, v189, v194
	v_add_u32_e32 v192, 3, v189
	v_add_u32_e32 v193, 2, v189
	v_cndmask_b32_e64 v92, 0, 1.0, vcc
	v_cmp_eq_u32_e32 vcc, v190, v194
	s_nop 1
	v_cndmask_b32_e64 v93, 0, 1.0, vcc
	v_cmp_eq_u32_e32 vcc, v192, v194
	s_waitcnt lgkmcnt(0)
	v_pk_fma_f32 v[92:93], v[90:91], v[134:135], v[92:93] op_sel_hi:[0,1,1] neg_lo:[1,0,0] neg_hi:[1,0,0]
	v_cvt_pk_bf16_f32 v92, v92, v93
	v_cndmask_b32_e64 v135, 0, 1.0, vcc
	v_cmp_eq_u32_e32 vcc, v193, v194
	s_nop 1
	v_cndmask_b32_e64 v134, 0, 1.0, vcc
	v_pk_fma_f32 v[90:91], v[90:91], v[136:137], v[134:135] op_sel_hi:[0,1,1] neg_lo:[1,0,0] neg_hi:[1,0,0]
	v_cvt_pk_bf16_f32 v93, v90, v91
	ds_write_b64 v186, v[92:93]
	ds_read_b32 v90, v187 offset:136
	v_cmp_eq_u32_e32 vcc, v189, v195
	s_nop 1
	v_cndmask_b32_e64 v92, 0, 1.0, vcc
	v_cmp_eq_u32_e32 vcc, v190, v195
	s_nop 1
	v_cndmask_b32_e64 v93, 0, 1.0, vcc
	v_cmp_eq_u32_e32 vcc, v192, v195
	s_waitcnt lgkmcnt(0)
	v_pk_fma_f32 v[92:93], v[90:91], v[118:119], v[92:93] op_sel_hi:[0,1,1] neg_lo:[1,0,0] neg_hi:[1,0,0]
	v_cvt_pk_bf16_f32 v92, v92, v93
	v_cndmask_b32_e64 v119, 0, 1.0, vcc
	v_cmp_eq_u32_e32 vcc, v193, v195
	s_nop 1
	v_cndmask_b32_e64 v118, 0, 1.0, vcc
	v_pk_fma_f32 v[90:91], v[90:91], v[120:121], v[118:119] op_sel_hi:[0,1,1] neg_lo:[1,0,0] neg_hi:[1,0,0]
	v_cvt_pk_bf16_f32 v93, v90, v91
	ds_write_b64 v186, v[92:93] offset:544
	ds_read_b32 v90, v187 offset:144
	v_cmp_eq_u32_e32 vcc, v189, v196
	s_nop 1
	v_cndmask_b32_e64 v92, 0, 1.0, vcc
	v_cmp_eq_u32_e32 vcc, v190, v196
	s_nop 1
	v_cndmask_b32_e64 v93, 0, 1.0, vcc
	v_cmp_eq_u32_e32 vcc, v192, v196
	s_waitcnt lgkmcnt(0)
	v_pk_fma_f32 v[92:93], v[90:91], v[110:111], v[92:93] op_sel_hi:[0,1,1] neg_lo:[1,0,0] neg_hi:[1,0,0]
	v_cvt_pk_bf16_f32 v92, v92, v93
	v_cndmask_b32_e64 v111, 0, 1.0, vcc
	v_cmp_eq_u32_e32 vcc, v193, v196
	s_nop 1
	v_cndmask_b32_e64 v110, 0, 1.0, vcc
	v_pk_fma_f32 v[90:91], v[90:91], v[112:113], v[110:111] op_sel_hi:[0,1,1] neg_lo:[1,0,0] neg_hi:[1,0,0]
	v_cvt_pk_bf16_f32 v93, v90, v91
	ds_write_b64 v186, v[92:93] offset:1088
	ds_read_b32 v90, v187 offset:152
	v_cmp_eq_u32_e32 vcc, v189, v197
	s_nop 1
	v_cndmask_b32_e64 v92, 0, 1.0, vcc
	v_cmp_eq_u32_e32 vcc, v190, v197
	s_nop 1
	v_cndmask_b32_e64 v93, 0, 1.0, vcc
	v_cmp_eq_u32_e32 vcc, v192, v197
	s_waitcnt lgkmcnt(0)
	v_pk_fma_f32 v[92:93], v[90:91], v[106:107], v[92:93] op_sel_hi:[0,1,1] neg_lo:[1,0,0] neg_hi:[1,0,0]
	v_cvt_pk_bf16_f32 v92, v92, v93
	v_cndmask_b32_e64 v107, 0, 1.0, vcc
	v_cmp_eq_u32_e32 vcc, v193, v197
	s_nop 1
	v_cndmask_b32_e64 v106, 0, 1.0, vcc
	v_pk_fma_f32 v[90:91], v[90:91], v[108:109], v[106:107] op_sel_hi:[0,1,1] neg_lo:[1,0,0] neg_hi:[1,0,0]
	v_cvt_pk_bf16_f32 v93, v90, v91
	ds_write_b64 v186, v[92:93] offset:1632
	ds_read_b32 v90, v187 offset:160
	v_cmp_eq_u32_e32 vcc, v189, v198
	s_nop 1
	v_cndmask_b32_e64 v92, 0, 1.0, vcc
	v_cmp_eq_u32_e32 vcc, v190, v198
	s_nop 1
	v_cndmask_b32_e64 v93, 0, 1.0, vcc
	v_cmp_eq_u32_e32 vcc, v192, v198
	s_waitcnt lgkmcnt(0)
	v_pk_fma_f32 v[92:93], v[90:91], v[98:99], v[92:93] op_sel_hi:[0,1,1] neg_lo:[1,0,0] neg_hi:[1,0,0]
	v_cvt_pk_bf16_f32 v92, v92, v93
	v_cndmask_b32_e64 v99, 0, 1.0, vcc
	v_cmp_eq_u32_e32 vcc, v193, v198
	s_nop 1
	v_cndmask_b32_e64 v98, 0, 1.0, vcc
	v_pk_fma_f32 v[90:91], v[90:91], v[100:101], v[98:99] op_sel_hi:[0,1,1] neg_lo:[1,0,0] neg_hi:[1,0,0]
	v_cvt_pk_bf16_f32 v93, v90, v91
	ds_write_b64 v186, v[92:93] offset:2176
	ds_read_b32 v90, v187 offset:168
	v_cmp_eq_u32_e32 vcc, v189, v199
	s_nop 1
	v_cndmask_b32_e64 v92, 0, 1.0, vcc
	v_cmp_eq_u32_e32 vcc, v190, v199
	s_nop 1
	v_cndmask_b32_e64 v93, 0, 1.0, vcc
	v_cmp_eq_u32_e32 vcc, v192, v199
	s_waitcnt lgkmcnt(0)
	v_pk_fma_f32 v[92:93], v[90:91], v[94:95], v[92:93] op_sel_hi:[0,1,1] neg_lo:[1,0,0] neg_hi:[1,0,0]
	v_cvt_pk_bf16_f32 v92, v92, v93
	v_cndmask_b32_e64 v95, 0, 1.0, vcc
	v_cmp_eq_u32_e32 vcc, v193, v199
	s_nop 1
	v_cndmask_b32_e64 v94, 0, 1.0, vcc
	v_pk_fma_f32 v[90:91], v[90:91], v[96:97], v[94:95] op_sel_hi:[0,1,1] neg_lo:[1,0,0] neg_hi:[1,0,0]
	v_cvt_pk_bf16_f32 v93, v90, v91
	ds_write_b64 v186, v[92:93] offset:2720
	ds_read_b32 v90, v187 offset:176
	v_cmp_eq_u32_e32 vcc, v189, v200
	s_nop 1
	v_cndmask_b32_e64 v92, 0, 1.0, vcc
	v_cmp_eq_u32_e32 vcc, v190, v200
	s_nop 1
	v_cndmask_b32_e64 v93, 0, 1.0, vcc
	v_cmp_eq_u32_e32 vcc, v192, v200
	s_waitcnt lgkmcnt(0)
	v_pk_fma_f32 v[86:87], v[90:91], v[86:87], v[92:93] op_sel_hi:[0,1,1] neg_lo:[1,0,0] neg_hi:[1,0,0]
	v_cvt_pk_bf16_f32 v86, v86, v87
	v_cndmask_b32_e64 v93, 0, 1.0, vcc
	v_cmp_eq_u32_e32 vcc, v193, v200
	s_nop 1
	v_cndmask_b32_e64 v92, 0, 1.0, vcc
	v_pk_fma_f32 v[88:89], v[90:91], v[88:89], v[92:93] op_sel_hi:[0,1,1] neg_lo:[1,0,0] neg_hi:[1,0,0]
	v_cvt_pk_bf16_f32 v87, v88, v89
	ds_write_b64 v186, v[86:87] offset:3264
	ds_read_b32 v86, v187 offset:184
	v_cmp_eq_u32_e32 vcc, v189, v201
	s_nop 1
	v_cndmask_b32_e64 v88, 0, 1.0, vcc
	v_cmp_eq_u32_e32 vcc, v190, v201
	s_nop 1
	v_cndmask_b32_e64 v89, 0, 1.0, vcc
	v_cmp_eq_u32_e32 vcc, v192, v201
	s_waitcnt lgkmcnt(0)
	v_pk_fma_f32 v[82:83], v[86:87], v[82:83], v[88:89] op_sel_hi:[0,1,1] neg_lo:[1,0,0] neg_hi:[1,0,0]
	v_cvt_pk_bf16_f32 v82, v82, v83
	v_cndmask_b32_e64 v89, 0, 1.0, vcc
	v_cmp_eq_u32_e32 vcc, v193, v201
	s_nop 1
	v_cndmask_b32_e64 v88, 0, 1.0, vcc
	v_pk_fma_f32 v[84:85], v[86:87], v[84:85], v[88:89] op_sel_hi:[0,1,1] neg_lo:[1,0,0] neg_hi:[1,0,0]
	v_cvt_pk_bf16_f32 v83, v84, v85
	ds_write_b64 v186, v[82:83] offset:3808
	ds_read_b128 v[82:85], v1
	ds_read_b128 v[86:89], v1 offset:64
	ds_read_b128 v[90:93], v1 offset:128
	ds_read_b128 v[94:97], v1 offset:192
	v_lshl_add_u64 v[98:99], v[150:151], 0, s[0:1]
	v_lshl_add_u64 v[192:193], v[164:165], 0, s[0:1]
	v_lshl_add_u64 v[196:197], v[166:167], 0, s[0:1]
	v_lshl_add_u64 v[100:101], v[152:153], 0, s[0:1]
	v_lshl_add_u64 v[106:107], v[156:157], 0, s[0:1]
	v_lshl_add_u64 v[108:109], v[158:159], 0, s[0:1]
	v_lshl_add_u64 v[110:111], v[160:161], 0, s[0:1]
	v_lshl_add_u64 v[112:113], v[162:163], 0, s[0:1]
	global_load_dwordx4 v[118:121], v[98:99], off nt
	global_load_dwordx4 v[134:137], v[100:101], off nt
	global_load_dwordx4 v[150:153], v[106:107], off nt
	global_load_dwordx4 v[156:159], v[108:109], off nt
	global_load_dwordx4 v[160:163], v[110:111], off nt
	global_load_dwordx4 v[164:167], v[112:113], off nt
	s_nop 0
	global_load_dwordx4 v[192:195], v[192:193], off nt
	s_nop 0
	global_load_dwordx4 v[196:199], v[196:197], off nt
	v_mov_b32_e32 v98, v188
	s_waitcnt vmcnt(15)
	s_waitcnt vmcnt(14)
	s_waitcnt vmcnt(13)
	s_waitcnt vmcnt(12)
	s_waitcnt vmcnt(11)
	s_waitcnt vmcnt(10)
	s_waitcnt vmcnt(9)
	s_waitcnt vmcnt(8)
	ds_read_b32 v98, v187
	s_waitcnt lgkmcnt(0)
	v_pk_fma_f32 v[100:101], v[98:99], v[146:147], 0 op_sel_hi:[0,1,0] neg_lo:[1,0,0] neg_hi:[1,0,0]
	v_pk_fma_f32 v[98:99], v[98:99], v[148:149], 0 op_sel_hi:[0,1,0] neg_lo:[1,0,0] neg_hi:[1,0,0]
	v_cvt_pk_bf16_f32 v100, v100, v101
	v_cvt_pk_bf16_f32 v101, v98, v99
	ds_write_b64 v186, v[100:101]
	ds_read_b32 v98, v187 offset:8
	s_waitcnt lgkmcnt(0)
	v_pk_fma_f32 v[100:101], v[98:99], v[142:143], 0 op_sel_hi:[0,1,0] neg_lo:[1,0,0] neg_hi:[1,0,0]
	v_pk_fma_f32 v[98:99], v[98:99], v[144:145], 0 op_sel_hi:[0,1,0] neg_lo:[1,0,0] neg_hi:[1,0,0]
	v_cvt_pk_bf16_f32 v100, v100, v101
	v_cvt_pk_bf16_f32 v101, v98, v99
	ds_write_b64 v186, v[100:101] offset:544
	ds_read_b32 v98, v187 offset:16
	s_waitcnt lgkmcnt(0)
	v_pk_fma_f32 v[100:101], v[98:99], v[138:139], 0 op_sel_hi:[0,1,0] neg_lo:[1,0,0] neg_hi:[1,0,0]
	v_pk_fma_f32 v[98:99], v[98:99], v[140:141], 0 op_sel_hi:[0,1,0] neg_lo:[1,0,0] neg_hi:[1,0,0]
	v_cvt_pk_bf16_f32 v100, v100, v101
	v_cvt_pk_bf16_f32 v101, v98, v99
	ds_write_b64 v186, v[100:101] offset:1088
	ds_read_b32 v98, v187 offset:24
	s_waitcnt lgkmcnt(0)
	v_pk_fma_f32 v[100:101], v[98:99], v[130:131], 0 op_sel_hi:[0,1,0] neg_lo:[1,0,0] neg_hi:[1,0,0]
	v_pk_fma_f32 v[98:99], v[98:99], v[132:133], 0 op_sel_hi:[0,1,0] neg_lo:[1,0,0] neg_hi:[1,0,0]
	v_cvt_pk_bf16_f32 v100, v100, v101
	v_cvt_pk_bf16_f32 v101, v98, v99
	ds_write_b64 v186, v[100:101] offset:1632
	ds_read_b32 v98, v187 offset:32
	s_waitcnt lgkmcnt(0)
	v_pk_fma_f32 v[100:101], v[98:99], v[126:127], 0 op_sel_hi:[0,1,0] neg_lo:[1,0,0] neg_hi:[1,0,0]
	v_pk_fma_f32 v[98:99], v[98:99], v[128:129], 0 op_sel_hi:[0,1,0] neg_lo:[1,0,0] neg_hi:[1,0,0]
	v_cvt_pk_bf16_f32 v100, v100, v101
	v_cvt_pk_bf16_f32 v101, v98, v99
	ds_write_b64 v186, v[100:101] offset:2176
	ds_read_b32 v98, v187 offset:40
	s_waitcnt lgkmcnt(0)
	v_pk_fma_f32 v[100:101], v[98:99], v[122:123], 0 op_sel_hi:[0,1,0] neg_lo:[1,0,0] neg_hi:[1,0,0]
	v_pk_fma_f32 v[98:99], v[98:99], v[124:125], 0 op_sel_hi:[0,1,0] neg_lo:[1,0,0] neg_hi:[1,0,0]
	v_cvt_pk_bf16_f32 v100, v100, v101
	v_cvt_pk_bf16_f32 v101, v98, v99
	ds_write_b64 v186, v[100:101] offset:2720
	ds_read_b32 v98, v187 offset:48
	s_waitcnt lgkmcnt(0)
	v_pk_fma_f32 v[100:101], v[98:99], v[114:115], 0 op_sel_hi:[0,1,0] neg_lo:[1,0,0] neg_hi:[1,0,0]
	v_pk_fma_f32 v[98:99], v[98:99], v[116:117], 0 op_sel_hi:[0,1,0] neg_lo:[1,0,0] neg_hi:[1,0,0]
	v_cvt_pk_bf16_f32 v100, v100, v101
	v_cvt_pk_bf16_f32 v101, v98, v99
	ds_write_b64 v186, v[100:101] offset:3264
	ds_read_b32 v98, v187 offset:56
	s_waitcnt lgkmcnt(0)
	v_pk_fma_f32 v[100:101], v[98:99], v[102:103], 0 op_sel_hi:[0,1,0] neg_lo:[1,0,0] neg_hi:[1,0,0]
	v_pk_fma_f32 v[98:99], v[98:99], v[104:105], 0 op_sel_hi:[0,1,0] neg_lo:[1,0,0] neg_hi:[1,0,0]
	v_cvt_pk_bf16_f32 v100, v100, v101
	v_cvt_pk_bf16_f32 v101, v98, v99
	ds_write_b64 v186, v[100:101] offset:3808
	ds_read_b128 v[98:101], v1
	ds_read_b128 v[102:105], v1 offset:64
	ds_read_b128 v[106:109], v1 offset:128
	ds_read_b128 v[110:113], v1 offset:192
	v_lshl_add_u64 v[114:115], v[168:169], 0, s[0:1]
	v_lshl_add_u64 v[126:127], v[176:177], 0, s[0:1]
	v_lshl_add_u64 v[176:177], v[180:181], 0, s[0:1]
	v_lshl_add_u64 v[180:181], v[182:183], 0, s[0:1]
	v_lshl_add_u64 v[116:117], v[170:171], 0, s[0:1]
	v_lshl_add_u64 v[122:123], v[172:173], 0, s[0:1]
	v_lshl_add_u64 v[124:125], v[174:175], 0, s[0:1]
	v_lshl_add_u64 v[128:129], v[178:179], 0, s[0:1]
	global_load_dwordx4 v[130:133], v[114:115], off nt
	global_load_dwordx4 v[138:141], v[116:117], off nt
	global_load_dwordx4 v[142:145], v[122:123], off nt
	global_load_dwordx4 v[146:149], v[124:125], off nt
	global_load_dwordx4 v[168:171], v[126:127], off nt
	global_load_dwordx4 v[172:175], v[128:129], off nt
	s_nop 0
	global_load_dwordx4 v[176:179], v[176:177], off nt
	s_nop 0
	global_load_dwordx4 v[180:183], v[180:181], off nt
	v_mov_b32_e32 v114, v188
	s_waitcnt vmcnt(15)
	s_waitcnt vmcnt(14)
	s_waitcnt vmcnt(13)
	s_waitcnt vmcnt(12)
	s_waitcnt vmcnt(11)
	s_waitcnt vmcnt(10)
	s_waitcnt vmcnt(9)
	s_waitcnt vmcnt(8)
	ds_read_b32 v114, v187 offset:64
	s_waitcnt lgkmcnt(0)
	v_pk_fma_f32 v[116:117], v[114:115], v[118:119], 0 op_sel_hi:[0,1,0] neg_lo:[1,0,0] neg_hi:[1,0,0]
	v_pk_fma_f32 v[114:115], v[114:115], v[120:121], 0 op_sel_hi:[0,1,0] neg_lo:[1,0,0] neg_hi:[1,0,0]
	v_cvt_pk_bf16_f32 v116, v116, v117
	v_cvt_pk_bf16_f32 v117, v114, v115
	ds_write_b64 v186, v[116:117]
	ds_read_b32 v114, v187 offset:72
	s_waitcnt lgkmcnt(0)
	v_pk_fma_f32 v[116:117], v[114:115], v[134:135], 0 op_sel_hi:[0,1,0] neg_lo:[1,0,0] neg_hi:[1,0,0]
	v_pk_fma_f32 v[114:115], v[114:115], v[136:137], 0 op_sel_hi:[0,1,0] neg_lo:[1,0,0] neg_hi:[1,0,0]
	v_cvt_pk_bf16_f32 v116, v116, v117
	v_cvt_pk_bf16_f32 v117, v114, v115
	ds_write_b64 v186, v[116:117] offset:544
	ds_read_b32 v114, v187 offset:80
	s_waitcnt lgkmcnt(0)
	v_pk_fma_f32 v[116:117], v[114:115], v[150:151], 0 op_sel_hi:[0,1,0] neg_lo:[1,0,0] neg_hi:[1,0,0]
	v_pk_fma_f32 v[114:115], v[114:115], v[152:153], 0 op_sel_hi:[0,1,0] neg_lo:[1,0,0] neg_hi:[1,0,0]
	v_cvt_pk_bf16_f32 v116, v116, v117
	v_cvt_pk_bf16_f32 v117, v114, v115
	ds_write_b64 v186, v[116:117] offset:1088
	ds_read_b32 v114, v187 offset:88
	s_waitcnt lgkmcnt(0)
	v_pk_fma_f32 v[116:117], v[114:115], v[156:157], 0 op_sel_hi:[0,1,0] neg_lo:[1,0,0] neg_hi:[1,0,0]
	v_pk_fma_f32 v[114:115], v[114:115], v[158:159], 0 op_sel_hi:[0,1,0] neg_lo:[1,0,0] neg_hi:[1,0,0]
	v_cvt_pk_bf16_f32 v116, v116, v117
	v_cvt_pk_bf16_f32 v117, v114, v115
	ds_write_b64 v186, v[116:117] offset:1632
	ds_read_b32 v114, v187 offset:96
	s_waitcnt lgkmcnt(0)
	v_pk_fma_f32 v[116:117], v[114:115], v[160:161], 0 op_sel_hi:[0,1,0] neg_lo:[1,0,0] neg_hi:[1,0,0]
	v_pk_fma_f32 v[114:115], v[114:115], v[162:163], 0 op_sel_hi:[0,1,0] neg_lo:[1,0,0] neg_hi:[1,0,0]
	v_cvt_pk_bf16_f32 v116, v116, v117
	v_cvt_pk_bf16_f32 v117, v114, v115
	ds_write_b64 v186, v[116:117] offset:2176
	ds_read_b32 v114, v187 offset:104
	s_waitcnt lgkmcnt(0)
	v_pk_fma_f32 v[116:117], v[114:115], v[164:165], 0 op_sel_hi:[0,1,0] neg_lo:[1,0,0] neg_hi:[1,0,0]
	v_pk_fma_f32 v[114:115], v[114:115], v[166:167], 0 op_sel_hi:[0,1,0] neg_lo:[1,0,0] neg_hi:[1,0,0]
	v_cvt_pk_bf16_f32 v116, v116, v117
	v_cvt_pk_bf16_f32 v117, v114, v115
	ds_write_b64 v186, v[116:117] offset:2720
	ds_read_b32 v114, v187 offset:112
	s_waitcnt lgkmcnt(0)
	v_pk_fma_f32 v[116:117], v[114:115], v[192:193], 0 op_sel_hi:[0,1,0] neg_lo:[1,0,0] neg_hi:[1,0,0]
	v_pk_fma_f32 v[114:115], v[114:115], v[194:195], 0 op_sel_hi:[0,1,0] neg_lo:[1,0,0] neg_hi:[1,0,0]
	v_cvt_pk_bf16_f32 v116, v116, v117
	v_cvt_pk_bf16_f32 v117, v114, v115
	ds_write_b64 v186, v[116:117] offset:3264
	ds_read_b32 v114, v187 offset:120
	s_waitcnt lgkmcnt(0)
	v_pk_fma_f32 v[116:117], v[114:115], v[196:197], 0 op_sel_hi:[0,1,0] neg_lo:[1,0,0] neg_hi:[1,0,0]
	v_pk_fma_f32 v[114:115], v[114:115], v[198:199], 0 op_sel_hi:[0,1,0] neg_lo:[1,0,0] neg_hi:[1,0,0]
	v_cvt_pk_bf16_f32 v116, v116, v117
	v_cvt_pk_bf16_f32 v117, v114, v115
	ds_write_b64 v186, v[116:117] offset:3808
	ds_read_b128 v[114:117], v1
	ds_read_b128 v[118:121], v1 offset:64
	ds_read_b128 v[122:125], v1 offset:128
	ds_read_b128 v[126:129], v1 offset:192
	s_waitcnt vmcnt(7)
	s_waitcnt vmcnt(6)
	s_waitcnt vmcnt(5)
	s_waitcnt vmcnt(4)
	s_waitcnt vmcnt(3)
	s_waitcnt vmcnt(2)
	s_waitcnt vmcnt(1)
	s_waitcnt vmcnt(0)
	ds_read_b32 v134, v187 offset:128
	s_waitcnt lgkmcnt(0)
	v_pk_fma_f32 v[130:131], v[134:135], v[130:131], 0 op_sel_hi:[0,1,0] neg_lo:[1,0,0] neg_hi:[1,0,0]
	v_pk_fma_f32 v[132:133], v[134:135], v[132:133], 0 op_sel_hi:[0,1,0] neg_lo:[1,0,0] neg_hi:[1,0,0]
	v_cvt_pk_bf16_f32 v130, v130, v131
	v_cvt_pk_bf16_f32 v131, v132, v133
	ds_write_b64 v186, v[130:131]
	ds_read_b32 v130, v187 offset:136
	s_waitcnt lgkmcnt(0)
	v_pk_fma_f32 v[132:133], v[130:131], v[138:139], 0 op_sel_hi:[0,1,0] neg_lo:[1,0,0] neg_hi:[1,0,0]
	v_pk_fma_f32 v[130:131], v[130:131], v[140:141], 0 op_sel_hi:[0,1,0] neg_lo:[1,0,0] neg_hi:[1,0,0]
	v_cvt_pk_bf16_f32 v132, v132, v133
	v_cvt_pk_bf16_f32 v133, v130, v131
	ds_write_b64 v186, v[132:133] offset:544
	ds_read_b32 v130, v187 offset:144
	s_waitcnt lgkmcnt(0)
	v_pk_fma_f32 v[132:133], v[130:131], v[142:143], 0 op_sel_hi:[0,1,0] neg_lo:[1,0,0] neg_hi:[1,0,0]
	v_pk_fma_f32 v[130:131], v[130:131], v[144:145], 0 op_sel_hi:[0,1,0] neg_lo:[1,0,0] neg_hi:[1,0,0]
	v_cvt_pk_bf16_f32 v132, v132, v133
	v_cvt_pk_bf16_f32 v133, v130, v131
	ds_write_b64 v186, v[132:133] offset:1088
	ds_read_b32 v130, v187 offset:152
	s_waitcnt lgkmcnt(0)
	v_pk_fma_f32 v[132:133], v[130:131], v[146:147], 0 op_sel_hi:[0,1,0] neg_lo:[1,0,0] neg_hi:[1,0,0]
	v_pk_fma_f32 v[130:131], v[130:131], v[148:149], 0 op_sel_hi:[0,1,0] neg_lo:[1,0,0] neg_hi:[1,0,0]
	v_cvt_pk_bf16_f32 v132, v132, v133
	v_cvt_pk_bf16_f32 v133, v130, v131
	ds_write_b64 v186, v[132:133] offset:1632
	ds_read_b32 v130, v187 offset:160
	s_waitcnt lgkmcnt(0)
	v_pk_fma_f32 v[132:133], v[130:131], v[168:169], 0 op_sel_hi:[0,1,0] neg_lo:[1,0,0] neg_hi:[1,0,0]
	v_pk_fma_f32 v[130:131], v[130:131], v[170:171], 0 op_sel_hi:[0,1,0] neg_lo:[1,0,0] neg_hi:[1,0,0]
	v_cvt_pk_bf16_f32 v132, v132, v133
	v_cvt_pk_bf16_f32 v133, v130, v131
	ds_write_b64 v186, v[132:133] offset:2176
	ds_read_b32 v130, v187 offset:168
	s_waitcnt lgkmcnt(0)
	v_pk_fma_f32 v[132:133], v[130:131], v[172:173], 0 op_sel_hi:[0,1,0] neg_lo:[1,0,0] neg_hi:[1,0,0]
	v_pk_fma_f32 v[130:131], v[130:131], v[174:175], 0 op_sel_hi:[0,1,0] neg_lo:[1,0,0] neg_hi:[1,0,0]
	v_cvt_pk_bf16_f32 v132, v132, v133
	v_cvt_pk_bf16_f32 v133, v130, v131
	ds_write_b64 v186, v[132:133] offset:2720
	ds_read_b32 v130, v187 offset:176
	s_waitcnt lgkmcnt(0)
	v_pk_fma_f32 v[132:133], v[130:131], v[176:177], 0 op_sel_hi:[0,1,0] neg_lo:[1,0,0] neg_hi:[1,0,0]
	v_pk_fma_f32 v[130:131], v[130:131], v[178:179], 0 op_sel_hi:[0,1,0] neg_lo:[1,0,0] neg_hi:[1,0,0]
	v_cvt_pk_bf16_f32 v132, v132, v133
	v_cvt_pk_bf16_f32 v133, v130, v131
	ds_write_b64 v186, v[132:133] offset:3264
	ds_read_b32 v130, v187 offset:184
	s_waitcnt lgkmcnt(0)
	v_pk_fma_f32 v[132:133], v[130:131], v[180:181], 0 op_sel_hi:[0,1,0] neg_lo:[1,0,0] neg_hi:[1,0,0]
	v_pk_fma_f32 v[130:131], v[130:131], v[182:183], 0 op_sel_hi:[0,1,0] neg_lo:[1,0,0] neg_hi:[1,0,0]
	v_cvt_pk_bf16_f32 v132, v132, v133
	v_cvt_pk_bf16_f32 v133, v130, v131
	ds_write_b64 v186, v[132:133] offset:3808
	ds_read_b128 v[130:133], v1
	ds_read_b128 v[134:137], v1 offset:64
	ds_read_b128 v[138:141], v1 offset:128
	ds_read_b128 v[142:145], v1 offset:192
	s_ashr_i32 s7, s6, 31
	s_lshl_b64 s[0:1], s[6:7], 2
	s_add_u32 s0, s4, s0
	s_addc_u32 s1, s5, s1
	v_lshlrev_b32_e32 v1, 4, v0
	s_add_i32 s20, s34, 1
	s_add_i32 s34, s34, -1
	v_or_b32_e32 v153, s10, v206
	s_xor_b32 s26, s3, 2
	s_lshl_b64 s[10:11], s[10:11], 3
	s_and_b32 s20, s20, 3
	s_and_b32 s27, s34, 3
	s_add_u32 s10, s14, s10
	s_addc_u32 s11, s15, s11
	s_lshl_b32 s42, s35, 2
	s_add_i32 s41, s42, 0x26a20
	s_add_i32 s42, s42, 0x26a00
	v_lshlrev_b32_e32 v190, 3, v206
	s_cmp_eq_u32 s35, 3
	v_lshlrev_b32_e32 v150, 3, v0
	v_and_b32_e32 v151, 1, v0
	v_lshl_add_u64 v[0:1], v[154:155], 3, s[14:15]
	v_lshl_add_u64 v[192:193], s[10:11], 0, v[190:191]
	s_cselect_b64 s[10:11], -1, 0
	s_lshl_b32 s14, s3, 2
	s_add_u32 s24, s16, s14
	v_or_b32_e32 v155, 0x20000, v150
	v_add_u32_e32 v156, 0x20880, v150
	v_lshlrev_b32_e32 v150, 1, v153
	s_addc_u32 s25, s17, 0
	s_lshl_b32 s43, s3, 9
	v_lshl_add_u32 v212, s26, 9, v150
	s_lshl_b32 s15, s26, 8
	s_add_i32 s26, s43, 0x200
	v_mov_b32_e32 v152, 0x880
	v_cmp_lt_u32_e64 s[0:1], 15, v206
	v_cmp_eq_u32_e32 vcc, 1, v151
	s_and_b32 s45, s26, 0x600
	s_add_i32 s26, s43, 0x500
	v_cndmask_b32_e32 v211, 0, v152, vcc
	s_and_b32 s56, s26, 0x700
	s_add_i32 s26, s43, 0x540
	v_lshl_add_u32 v213, s20, 9, v150
	v_lshl_add_u32 v214, s27, 9, v150
	s_and_b32 s57, s26, 0x740
	s_add_i32 s26, s43, 0x580
	s_and_b32 s58, s26, 0x780
	s_add_i32 s26, s43, 0x5c0
	s_and_b32 s59, s26, 0x7c0
	s_add_i32 s26, s43, 0x600
	s_and_b32 s60, s26, 0x600
	s_add_i32 s26, s43, 0x640
	s_and_b32 s61, s26, 0x640
	s_add_i32 s26, s43, 0x680
	s_and_b32 s62, s26, 0x680
	s_add_i32 s26, s43, 0x6c0
	s_and_b32 s63, s26, 0x6c0
	s_add_i32 s26, s43, 0x700
	s_and_b32 s64, s26, 0x700
	s_add_i32 s26, s43, 0x740
	s_and_b32 s65, s26, 0x740
	s_add_i32 s26, s43, 0x780
	s_lshl_b32 s14, s27, 8
	s_lshl_b32 s20, s20, 8
	s_add_i32 s27, s43, 0x240
	s_add_i32 s28, s43, 0x280
	s_add_i32 s29, s43, 0x2c0
	s_add_i32 s30, s43, 0x300
	s_add_i32 s31, s43, 0x340
	s_add_i32 s34, s43, 0x380
	s_add_i32 s35, s43, 0x3c0
	s_add_i32 s36, s43, 0x440
	s_add_i32 s37, s43, 0x480
	s_add_i32 s38, s43, 0x4c0
	s_and_b32 s66, s26, 0x780
	s_add_i32 s26, s43, 0x7c0
	s_mul_hi_i32 s23, s18, 0x65
	s_mul_i32 s22, s18, 0x65
	v_cmp_eq_u32_e64 s[4:5], 1, v185
	v_cmp_eq_u32_e64 s[6:7], 2, v185
	v_cmp_eq_u32_e64 s[8:9], 63, v206
	s_xor_b32 s44, s43, 0x400
	s_and_b32 s46, s27, 0x640
	s_and_b32 s47, s28, 0x680
	s_waitcnt lgkmcnt(0)
	v_mov_b32_e32 v146, 0x20000
	s_and_b32 s48, s29, 0x6c0
	s_and_b32 s49, s30, 0x700
	s_and_b32 s50, s31, 0x740
	s_and_b32 s51, s34, 0x780
	s_and_b32 s52, s35, 0x7c0
	s_and_b32 s53, s36, 0x640
	s_and_b32 s54, s37, 0x680
	s_and_b32 s55, s38, 0x6c0
	s_and_b32 s67, s26, 0x7c0
	s_and_b64 s[26:27], s[10:11], s[12:13]
	v_lshl_add_u32 v215, v154, 1, v146
	v_mov_b32_e32 v216, 1
	s_lshl_b32 s28, s14, 3
	s_lshl_b32 s30, s15, 3
	s_lshl_b32 s34, s20, 3
	s_movk_i32 s68, 0x7fff
	s_mov_b32 s69, 0
	v_and_b32_e32 v220, 24, v206
	v_lshlrev_b32_e32 v220, 2, v220
	v_and_b32_e32 v221, 2, v206
	v_lshl_or_b32 v220, v221, 3, v220
	v_and_b32_e32 v221, 32, v206
	v_lshrrev_b32_e32 v221, 2, v221
	v_or_b32_e32 v220, v220, v221
	v_and_b32_e32 v221, 4, v206
	v_or_b32_e32 v220, v220, v221
	v_and_b32_e32 v221, 1, v206
	v_lshl_or_b32 v220, v221, 1, v220
	v_mov_b32_e32 v220, v254
	s_lshr_b32 s76, s19, 8
	s_add_i32 s76, s76, 0x20000
	v_add_u32_e32 v220, s76, v220
	v_add_u32_e32 v225, s45, v220
	v_add_u32_e32 v226, s44, v220
	v_add_u32_e32 v227, s60, v220
	v_add_u32_e32 v228, s43, v220
	v_and_b32_e32 v221, 1, v206
	v_mul_u32_u24_e32 v221, 0x880, v221
	v_lshrrev_b32_e32 v220, 4, v206
	v_lshl_add_u32 v221, v220, 5, v221
	v_and_b32_e32 v220, 2, v206
	v_lshl_add_u32 v221, v220, 3, v221
	v_add_u32_e32 v222, 0x20000, v221
	v_cmp_ne_u32_e32 vcc, 0, v220
	v_mov_b32_e32 v220, 0x44444444
	v_mov_b32_e32 v221, 0xeeeeeeee
	s_nop 1
	v_cndmask_b32_e32 v223, v220, v221, vcc
	v_cmp_lt_u32_e64 s[74:75], 47, v206
	s_lshr_b32 s82, s19, 15
	s_mul_i32 s83, s82, 0x1100
	s_add_i32 s83, s83, 0x22200
	v_lshl_add_u32 v254, v206, 2, s83
	v_mov_b32_e32 v220, s41
	s_nop 1
	v_cndmask_b32_e64 v254, v254, v220, s[12:13]
	v_mov_b32_e32 v224, v184
	s_mov_b32 s86, 0x55555555
	s_mov_b32 s87, 0x55555555
	s_lshr_b32 s78, s19, 15
	s_lshl_b32 s79, s78, 11
	v_add_u32_e32 v255, s79, v224
	ds_read_b128 v[166:169], v224 offset:0
	ds_read_b128 v[170:173], v224 offset:1024
	ds_read_b128 v[174:177], v224 offset:2048
	ds_read_b128 v[178:181], v224 offset:3072
	ds_read_b128 v[182:185], v224 offset:4096
	ds_read_b128 v[186:189], v224 offset:5120
	s_mov_b32 s20, 0
.Lj_loop:
	s_and_b32 s70, s20, 1
	s_waitcnt lgkmcnt(0)
	s_barrier
	s_mul_i32 s38, s70, 0x1100
	v_add_u32_e32 v229, s38, v222
	v_add_u32_e32 v230, s43, v229
	ds_read_b128 v[150:153], v230 offset:0
	ds_read_b128 v[194:197], v230 offset:128
	ds_read_b128 v[198:201], v230 offset:256
	ds_read_b128 v[232:235], v230 offset:384
	s_xor_b32 s83, s70, 1
	s_lshl_b32 s83, s83, 4
	s_add_i32 s83, s83, 0x26a20
	v_mov_b32_e32 v239, s83
	ds_read_b128 v[240:243], v239
	s_cmp_lg_u32 s20, 1
	s_cselect_b64 s[10:11], -1, 0
	s_and_b64 s[14:15], s[10:11], s[26:27]
	s_and_saveexec_b64 s[10:11], s[14:15]
	s_cbranch_execz .Lj_norr
	s_lshl_b32 s14, s70, 4
	s_or_b32 s14, s14, 0x26a00
	v_mov_b32_e32 v236, s14
	s_add_i32 s14, s20, -2
	ds_read_b128 v[236:239], v236
	s_cmp_lg_u32 s20, 0
	s_cselect_b32 s14, s14, 0x64
	s_ashr_i32 s15, s14, 31
	s_add_u32 s14, s22, s14
	s_addc_u32 s15, s23, s15
	s_lshl_b64 s[14:15], s[14:15], 4
	s_add_u32 s14, s24, s14
	s_addc_u32 s15, s25, s15
	s_waitcnt lgkmcnt(0)
	v_add_f32_e32 v236, v236, v237
	v_add_f32_e32 v238, v238, v239
	v_add_f32_e32 v236, v236, v238
	global_store_dword v191, v236, s[14:15]
.Lj_norr:
	s_or_b64 exec, exec, s[10:11]
	v_mov_b64_e32 v[146:147], 0
	v_mov_b64_e32 v[148:149], 0
	v_mov_b64_e32 v[154:155], 0
	v_mov_b64_e32 v[156:157], 0
	v_mov_b64_e32 v[158:159], 0
	v_mov_b64_e32 v[160:161], 0
	v_mov_b64_e32 v[162:163], 0
	v_mov_b64_e32 v[164:165], 0
	v_mov_b32_e32 v231, 0
	s_lshl_b32 s10, s70, 13
	s_add_i32 s14, s10, s34
	s_mov_b32 s15, 0
	v_lshl_add_u64 v[244:245], v[192:193], 0, s[14:15]
	s_add_i32 s14, s10, s30
	v_lshl_add_u64 v[246:247], v[192:193], 0, s[14:15]
	s_add_i32 s14, s10, s28
	v_lshl_add_u64 v[248:249], v[192:193], 0, s[14:15]
	s_waitcnt lgkmcnt(4)
	v_smfmac_f32_16x16x64_bf16 v[162:165], v[150:153], v[166:173], v223
	ds_read_b128 v[166:169], v224 offset:6144
	v_smfmac_f32_16x16x64_bf16 v[146:149], v[150:153], v[2:9], v223
	ds_read_b128 v[170:173], v224 offset:7168
	v_smfmac_f32_16x16x64_bf16 v[154:157], v[150:153], v[18:25], v223
	v_smfmac_f32_16x16x64_bf16 v[158:161], v[150:153], v[34:41], v223
	s_cmp_eq_u32 s20, 0
	s_cbranch_scc1 .Lj_nopoll0
	global_load_dwordx2 v[204:205], v[244:245], off sc1
	global_load_dwordx2 v[202:203], v[246:247], off sc1
	global_load_dwordx2 v[218:219], v[248:249], off sc1
.Lj_nopoll0:
	s_waitcnt lgkmcnt(5)
	v_smfmac_f32_16x16x64_bf16 v[162:165], v[194:197], v[174:181], v223
	ds_read_b128 v[174:177], v224 offset:8192
	v_smfmac_f32_16x16x64_bf16 v[146:149], v[194:197], v[10:17], v223
	ds_read_b128 v[178:181], v224 offset:9216
	v_smfmac_f32_16x16x64_bf16 v[154:157], v[194:197], v[26:33], v223
	v_smfmac_f32_16x16x64_bf16 v[158:161], v[194:197], v[42:49], v223
	s_waitcnt lgkmcnt(6)
	v_smfmac_f32_16x16x64_bf16 v[162:165], v[198:201], v[182:189], v223
	ds_read_b128 v[182:185], v224 offset:10240
	v_smfmac_f32_16x16x64_bf16 v[146:149], v[198:201], v[50:57], v223
	ds_read_b128 v[186:189], v224 offset:11264
	v_smfmac_f32_16x16x64_bf16 v[154:157], v[198:201], v[66:73], v223
	v_smfmac_f32_16x16x64_bf16 v[158:161], v[198:201], v[82:89], v223
	s_waitcnt lgkmcnt(4)
	v_smfmac_f32_16x16x64_bf16 v[162:165], v[232:235], v[166:173], v223
	ds_read_b128 v[166:169], v224 offset:12288
	v_smfmac_f32_16x16x64_bf16 v[146:149], v[232:235], v[58:65], v223
	ds_read_b128 v[170:173], v224 offset:13312
	v_smfmac_f32_16x16x64_bf16 v[154:157], v[232:235], v[74:81], v223
	v_smfmac_f32_16x16x64_bf16 v[158:161], v[232:235], v[90:97], v223
	v_and_b32_e32 v240, v240, v241
	v_and_b32_e32 v242, v242, v243
	v_and_b32_e32 v240, v240, v242
	s_nop 0
	v_readfirstlane_b32 s83, v240
	s_cmp_lt_u32 s20, 2
	s_cbranch_scc1 .Lj_nostop
	s_cmp_eq_u32 s83, 0
	s_cbranch_scc0 .Lj_stop
.Lj_nostop:
	s_cmp_eq_u32 s20, 0
	s_cbranch_scc1 .Lj_gdone
	s_mov_b32 s29, 0

.Lj_got:
	v_cvt_pk_bf16_f32 v236, v204, v204
	v_lshlrev_b32_e32 v237, 16, v236
	v_sub_f32_e32 v237, v204, v237
	v_add_u32_e32 v238, s38, v225
	v_cvt_pk_bf16_f32 v237, v237, v237
	ds_write_b16 v238, v236
	ds_write_b16 v238, v237 offset:2176
	v_cvt_pk_bf16_f32 v244, v202, v202
	v_lshlrev_b32_e32 v245, 16, v244
	v_sub_f32_e32 v245, v202, v245
	v_add_u32_e32 v238, s38, v226
	v_cvt_pk_bf16_f32 v245, v245, v245
	ds_write_b16 v238, v244
	ds_write_b16 v238, v245 offset:2176
	v_cvt_pk_bf16_f32 v246, v218, v218
	v_lshlrev_b32_e32 v247, 16, v246
	v_sub_f32_e32 v247, v218, v247
	v_add_u32_e32 v238, s38, v227
	v_cvt_pk_bf16_f32 v247, v247, v247
	ds_write_b16 v238, v246
	ds_write_b16 v238, v247 offset:2176
.Lj_gdone:
	s_waitcnt lgkmcnt(0)
	s_barrier
	v_add_u32_e32 v240, s45, v229
	v_add_u32_e32 v241, s44, v229
	v_add_u32_e32 v242, s60, v229
	ds_read_b128 v[150:153], v240 offset:0
	ds_read_b128 v[194:197], v240 offset:128
	ds_read_b128 v[198:201], v240 offset:256
	ds_read_b128 v[232:235], v240 offset:384
	s_cmp_eq_u32 s20, 0
	s_cselect_b64 s[36:37], -1, 0
	s_add_i32 s29, s20, 1
	s_and_b32 s14, s29, 1
	s_lshl_b32 s10, s14, 13
	s_mov_b32 s11, 0
	v_lshl_add_u64 v[250:251], v[0:1], 0, s[10:11]
	s_mul_i32 s15, s14, 0x1100
	v_add_u32_e32 v243, s15, v228
	v_mov_b32_e32 v253, s29
	s_waitcnt lgkmcnt(3)
	v_smfmac_f32_16x16x64_bf16 v[162:165], v[150:153], v[174:181], v223
	ds_read_b128 v[174:177], v224 offset:14336
	v_smfmac_f32_16x16x64_bf16 v[146:149], v[150:153], v[98:105], v223
	ds_read_b128 v[178:181], v224 offset:15360
	v_smfmac_f32_16x16x64_bf16 v[154:157], v[150:153], v[114:121], v223
	v_or3_b32 v231, v236, v237, v216
	v_smfmac_f32_16x16x64_bf16 v[158:161], v[150:153], v[130:137], v223
	v_or3_b32 v231, v244, v245, v231
	ds_read_b128 v[150:153], v241 offset:0
	s_waitcnt lgkmcnt(5)
	v_smfmac_f32_16x16x64_bf16 v[162:165], v[194:197], v[182:189], v223
	ds_read_b128 v[182:185], v224 offset:16384
	v_smfmac_f32_16x16x64_bf16 v[146:149], v[194:197], v[106:113], v223
	ds_read_b128 v[186:189], v224 offset:17408
	v_smfmac_f32_16x16x64_bf16 v[154:157], v[194:197], v[122:129], v223
	v_or3_b32 v231, v246, v247, v231
	v_smfmac_f32_16x16x64_bf16 v[158:161], v[194:197], v[138:145], v223
	v_and_b32_e32 v231, 0x7fff7fff, v231
	ds_read_b128 v[194:197], v241 offset:128
	s_waitcnt lgkmcnt(7)
	v_smfmac_f32_16x16x64_bf16 v[162:165], v[198:201], v[166:173], v223
	ds_read_b128 v[166:169], v224 offset:18432
	v_smfmac_f32_16x16x64_bf16 v[146:149], v[198:201], a[0:7], v223
	ds_read_b128 v[170:173], v224 offset:19456
	v_smfmac_f32_16x16x64_bf16 v[154:157], v[198:201], a[16:23], v223
	v_cmp_eq_u32_e32 vcc, 0, v231
	v_smfmac_f32_16x16x64_bf16 v[158:161], v[198:201], a[32:39], v223
	s_lshl_b32 s83, s70, 4
	ds_read_b128 v[198:201], v241 offset:256
	s_waitcnt lgkmcnt(7)
	v_smfmac_f32_16x16x64_bf16 v[162:165], v[232:235], v[174:181], v223
	ds_read_b128 v[174:177], v224 offset:20480
	v_smfmac_f32_16x16x64_bf16 v[146:149], v[232:235], a[8:15], v223
	ds_read_b128 v[178:181], v224 offset:21504
	v_smfmac_f32_16x16x64_bf16 v[154:157], v[232:235], a[24:31], v223
	s_cmp_eq_u64 vcc, exec
	v_smfmac_f32_16x16x64_bf16 v[158:161], v[232:235], a[40:47], v223
	s_cselect_b32 s82, 1, 0
	ds_read_b128 v[232:235], v241 offset:384
	s_waitcnt lgkmcnt(7)
	v_smfmac_f32_16x16x64_bf16 v[162:165], v[150:153], v[182:189], v223
	ds_read_b128 v[182:185], v224 offset:22528
	v_smfmac_f32_16x16x64_bf16 v[146:149], v[150:153], a[48:55], v223
	ds_read_b128 v[186:189], v224 offset:23552
	v_smfmac_f32_16x16x64_bf16 v[154:157], v[150:153], a[64:71], v223
	v_mov_b32_e32 v238, s82
	v_smfmac_f32_16x16x64_bf16 v[158:161], v[150:153], a[80:87], v223
	v_add_u32_e32 v239, s83, v254
	ds_read_b128 v[150:153], v242 offset:0
	s_waitcnt lgkmcnt(7)
	v_smfmac_f32_16x16x64_bf16 v[162:165], v[194:197], v[166:173], v223
	ds_read_b128 v[166:169], v224 offset:24576
	v_smfmac_f32_16x16x64_bf16 v[146:149], v[194:197], a[56:63], v223
	ds_read_b128 v[170:173], v224 offset:25600
	v_smfmac_f32_16x16x64_bf16 v[154:157], v[194:197], a[72:79], v223
	v_smfmac_f32_16x16x64_bf16 v[158:161], v[194:197], a[88:95], v223
	ds_write_b32 v239, v238
	ds_read_b128 v[194:197], v242 offset:128
	s_waitcnt lgkmcnt(8)
	v_smfmac_f32_16x16x64_bf16 v[162:165], v[198:201], v[174:181], v223
	ds_read_b128 v[174:177], v224 offset:26624
	v_smfmac_f32_16x16x64_bf16 v[146:149], v[198:201], a[96:103], v223
	ds_read_b128 v[178:181], v224 offset:27648
	v_smfmac_f32_16x16x64_bf16 v[154:157], v[198:201], a[112:119], v223
	v_smfmac_f32_16x16x64_bf16 v[158:161], v[198:201], a[128:135], v223
	ds_read_b128 v[198:201], v242 offset:256
	s_waitcnt lgkmcnt(8)
	v_smfmac_f32_16x16x64_bf16 v[162:165], v[232:235], v[182:189], v223
	ds_read_b128 v[182:185], v224 offset:28672
	v_smfmac_f32_16x16x64_bf16 v[146:149], v[232:235], a[104:111], v223
	ds_read_b128 v[186:189], v224 offset:29696
	v_smfmac_f32_16x16x64_bf16 v[154:157], v[232:235], a[120:127], v223
	v_smfmac_f32_16x16x64_bf16 v[158:161], v[232:235], a[136:143], v223
	ds_read_b128 v[232:235], v242 offset:384
	s_waitcnt lgkmcnt(8)
	v_smfmac_f32_16x16x64_bf16 v[162:165], v[150:153], v[166:173], v223
	ds_read_b128 v[166:169], v224 offset:30720
	v_smfmac_f32_16x16x64_bf16 v[146:149], v[150:153], a[144:151], v223
	ds_read_b128 v[170:173], v224 offset:31744
	v_smfmac_f32_16x16x64_bf16 v[154:157], v[150:153], a[160:167], v223
	v_smfmac_f32_16x16x64_bf16 v[158:161], v[150:153], a[176:183], v223
	s_waitcnt lgkmcnt(6)
	v_smfmac_f32_16x16x64_bf16 v[162:165], v[194:197], v[174:181], v223
	ds_read_b128 v[174:177], v224 offset:2048
	v_smfmac_f32_16x16x64_bf16 v[146:149], v[194:197], a[152:159], v223
	ds_read_b128 v[178:181], v224 offset:3072
	v_smfmac_f32_16x16x64_bf16 v[154:157], v[194:197], a[168:175], v223
	v_smfmac_f32_16x16x64_bf16 v[158:161], v[194:197], a[184:191], v223
	s_waitcnt lgkmcnt(5)
	v_smfmac_f32_16x16x64_bf16 v[162:165], v[198:201], v[182:189], v223
	ds_read_b128 v[182:185], v224 offset:4096
	v_smfmac_f32_16x16x64_bf16 v[146:149], v[198:201], a[192:199], v223
	ds_read_b128 v[186:189], v224 offset:5120
	v_smfmac_f32_16x16x64_bf16 v[154:157], v[198:201], a[208:215], v223
	v_smfmac_f32_16x16x64_bf16 v[158:161], v[198:201], a[224:231], v223
	s_waitcnt lgkmcnt(4)
	v_smfmac_f32_16x16x64_bf16 v[162:165], v[232:235], v[166:173], v223
	ds_read_b128 v[166:169], v224 offset:0
	v_smfmac_f32_16x16x64_bf16 v[146:149], v[232:235], a[200:207], v223
	ds_read_b128 v[170:173], v224 offset:1024
	v_smfmac_f32_16x16x64_bf16 v[154:157], v[232:235], a[216:223], v223
	v_smfmac_f32_16x16x64_bf16 v[158:161], v[232:235], a[232:239], v223
	s_nop 5
	v_pk_add_f32 v[244:245], v[162:163], v[164:165]
	v_pk_add_f32 v[236:237], v[146:147], v[148:149]
	v_pk_add_f32 v[238:239], v[154:155], v[156:157]
	v_pk_add_f32 v[240:241], v[158:159], v[160:161]
	v_add_f32_e32 v236, v236, v237
	v_add_f32_e32 v237, v238, v239
	v_add_f32_e32 v238, v240, v241
	v_add_f32_e32 v239, v244, v245
	v_cndmask_b32_e64 v236, v236, v237, s[4:5]
	v_cndmask_b32_e64 v236, v236, v238, s[6:7]
	v_cndmask_b32_e64 v156, v236, v239, s[74:75]
	s_cmpk_eq_i32 s20, 0x64
	s_cbranch_scc1 .Lj_nopub
	v_add_f32_e32 v236, v208, v156
	v_cndmask_b32_e64 v252, v156, v236, s[36:37]
	global_store_dwordx2 v[250:251], v[252:253], off sc1
	v_cvt_pk_bf16_f32 v237, v252, v252
	v_lshlrev_b32_e32 v238, 16, v237
	v_sub_f32_e32 v238, v252, v238
	v_cvt_pk_bf16_f32 v238, v238, v238
	ds_write_b16 v243, v237
	ds_write_b16 v243, v238 offset:2176
	v_or_b32_e32 v216, v237, v238
